# adds: in-proj epilogue k_r rotary cos/sin rows prefetched through a 2-deep ring with counted waits
# speedup vs baseline: 1.0039x; 1.0009x over previous
; __device__ __forceinline__ u32x4 pack8(f32x4 a, f32x4 b) { u32x4 w; w.x = pk2(a[0], a[1]); w.y = pk2(a[2], a[3]); w.z = pk2(b[0], b[1]); w.w = pk2(b[2], b[3]); return w; }
; __device__ __forceinline__ float sq8(const f32x4& a, const f32x4& b) { return ((a[0] * a[0] + a[1] * a[1]) + (a[2] * a[2] + a[3] * a[3])) + ((b[0] * b[0] + b[1] * b[1]) + (b[2] * b[2] + b[3] * b[3])); }
; __device__ __forceinline__ f32x2 rtab_get(LAS unsigned char* lds, int ui, int r) { return ((const LAS f32x2*)(lds + RTAB_OFF))[(ui & 1) * 256 + r]; }
;     __device__ __forceinline__ void operator()(const f32x4 (&acc)[2][2][4][2], const Unit& u, int ui, int wr, int wc, int fr, int fq, LAS unsigned char* lds) const {
;     ...
;                 const int rr = ai * 128 + wr * 64 + m * 16 + fr, row = u.pm * 256 + rr; const float rs = rtab_get(lds, ui, rr)[0];
;                 float sq = 0.f;
; #pragma unroll
;                 for (int bj = 0; bj < 2; ++bj) {
;                     const int c = bj * 128 + wc * 32 + fq * 8;
;                     f32x4 v0 = acc[ai][bj][m][0] * rs, v1 = acc[ai][bj][m][1] * rs;
;                     if (pn < 6) { if (pn < 2) { v0 = v0 * QS_SB; v1 = v1 * QS_SB; } *(u32x4*)(QKV + (size_t)row * 1536 + pn * 256 + c) = pack8(v0, v1); }
;                     else if (pn == 6) { *(u32x4*)(CKV + (size_t)row * 256 + c) = pack8(v0, v1); sq += sq8(v0, v1); }
;                     else if (pn == 7) { *(u32x4*)(CQ + (size_t)row * 384 + c) = pack8(v0, v1); sq += sq8(v0, v1); }
;                     else if (bj == 0) { *(u32x4*)(CQ + (size_t)row * 384 + 256 + c) = pack8(v0, v1); sq += sq8(v0, v1); }
.Lpf_in_skip:
	s_lshl_b32 s6, s6, 11
	v_mov_b32_e32 v0, v188
	s_and_b32 s6, s6, 0x800
	s_add_i32 s6, s6, 0
	v_and_or_b32 v151, v0, 15, s94
	v_bfe_u32 v152, v0, 4, 2
	v_lshl_add_u32 v0, v151, 3, s6
	v_add_u32_e32 v150, 0x22400, v0
	ds_read_b32 v144, v150
	s_lshl_b32 s3, s3, 8
	v_lshlrev_b32_e32 v149, 3, v152
	s_cmp_gt_i32 s26, 5
	v_add_u32_e32 v138, s3, v151
	s_cselect_b64 s[14:15], -1, 0
	s_cmp_lt_i32 s26, 2
	v_ashrrev_i32_e32 v139, 31, v138
	v_or_b32_e32 v145, s95, v149
	s_cselect_b64 s[12:13], -1, 0
	v_mad_i64_i32 v[142:143], s[6:7], v138, s59, 0
	v_lshlrev_b64 v[140:141], 9, v[138:139]
	s_waitcnt lgkmcnt(0)
	v_pk_mul_f32 v[132:133], v[132:133], v[144:145] op_sel_hi:[1,0]
	v_pk_mul_f32 v[130:131], v[130:131], v[144:145] op_sel_hi:[1,0]
	v_pk_mul_f32 v[128:129], v[128:129], v[144:145] op_sel_hi:[1,0]
	v_pk_mul_f32 v[126:127], v[126:127], v[144:145] op_sel_hi:[1,0]
	s_cmp_lg_u32 s26, 8
	s_cbranch_scc1 .Lin_nopf
	s_andn2_b64 vcc, exec, s[56:57]
	s_cbranch_vccnz .Lin_nopf
	v_lshlrev_b64 v[202:203], 6, v[138:139]
	v_and_b32_e32 v206, 8, v149
	v_lshlrev_b32_e32 v206, 2, v206
	v_mov_b32_e32 v207, v1
	v_lshl_add_u64 v[204:205], s[46:47], 0, v[202:203]
	v_lshl_add_u64 v[202:203], s[44:45], 0, v[202:203]
	v_lshl_add_u64 v[202:203], v[202:203], 0, v[206:207]
	v_lshl_add_u64 v[204:205], v[204:205], 0, v[206:207]
	global_load_dwordx4 v[214:217], v[202:203], off
	global_load_dwordx4 v[218:221], v[202:203], off offset:16
	global_load_dwordx4 v[222:225], v[204:205], off
	global_load_dwordx4 v[226:229], v[204:205], off offset:16
	global_load_dwordx4 v[174:177], v[202:203], off offset:1024
	global_load_dwordx4 v[178:181], v[202:203], off offset:1040
	global_load_dwordx4 v[182:185], v[204:205], off offset:1024
	global_load_dwordx4 v[230:233], v[204:205], off offset:1040
	s_mov_b64 s[100:101], 0x2000
	v_lshl_add_u64 v[206:207], v[202:203], 0, s[100:101]
	v_lshl_add_u64 v[208:209], v[204:205], 0, s[100:101]
.Lin_nopf:
	s_mov_b64 s[16:17], -1
	s_and_b64 vcc, exec, s[14:15]
	s_cbranch_vccz .LBB0_362
	v_cvt_pk_bf16_f32 v114, v130, v131
	v_cvt_pk_bf16_f32 v115, v132, v133
	v_cvt_pk_bf16_f32 v116, v126, v127
	v_cvt_pk_bf16_f32 v117, v128, v129
	s_cmp_lt_i32 s26, 7
	s_cbranch_scc1 .LBB0_359
	s_cmp_lg_u32 s26, 7
	s_cbranch_scc0 .LBB0_356
	v_lshl_add_u64 v[154:155], s[40:41], 0, v[142:143]
	v_lshlrev_b32_e32 v0, 1, v145
	v_lshl_add_u64 v[154:155], v[154:155], 0, v[0:1]
	v_mov_b32_e32 v156, v131
	v_mov_b32_e32 v157, v127
	global_store_dwordx4 v[154:155], v[114:117], off offset:512
	v_mov_b32_e32 v154, v130
	v_mov_b32_e32 v155, v126
	v_pk_mul_f32 v[156:157], v[156:157], v[156:157]
	v_mov_b32_e32 v158, v133
	v_mov_b32_e32 v159, v129
	v_pk_fma_f32 v[154:155], v[154:155], v[154:155], v[156:157]
	v_mov_b32_e32 v156, v132
	v_mov_b32_e32 v157, v128
	v_pk_mul_f32 v[158:159], v[158:159], v[158:159]
	s_mov_b64 s[16:17], 0
	v_pk_fma_f32 v[156:157], v[156:157], v[156:157], v[158:159]
	s_nop 0
	v_pk_add_f32 v[154:155], v[154:155], v[156:157]
	s_nop 0
	v_add_f32_e32 v153, v154, v155
.LBB0_356:
	s_andn2_b64 vcc, exec, s[16:17]
	s_cbranch_vccnz .LBB0_358
	v_lshl_add_u64 v[154:155], s[40:41], 0, v[142:143]
	v_lshlrev_b32_e32 v0, 1, v145
	v_lshl_add_u64 v[154:155], v[154:155], 0, v[0:1]
	v_mov_b32_e32 v156, v131
	v_mov_b32_e32 v157, v127
	global_store_dwordx4 v[154:155], v[114:117], off
	v_mov_b32_e32 v154, v130
	v_mov_b32_e32 v155, v126
	v_pk_mul_f32 v[156:157], v[156:157], v[156:157]
	v_mov_b32_e32 v158, v133
	v_mov_b32_e32 v159, v129
	v_pk_fma_f32 v[154:155], v[154:155], v[154:155], v[156:157]
	v_mov_b32_e32 v156, v132
	v_mov_b32_e32 v157, v128
	v_pk_mul_f32 v[158:159], v[158:159], v[158:159]
	s_nop 0
	v_pk_fma_f32 v[156:157], v[156:157], v[156:157], v[158:159]
	s_nop 0
	v_pk_add_f32 v[154:155], v[154:155], v[156:157]
	s_nop 0
	v_add_f32_e32 v153, v154, v155

; __device__ __forceinline__ u32x4 pack8(f32x4 a, f32x4 b) { u32x4 w; w.x = pk2(a[0], a[1]); w.y = pk2(a[2], a[3]); w.z = pk2(b[0], b[1]); w.w = pk2(b[2], b[3]); return w; }
; __device__ __forceinline__ float sq8(const f32x4& a, const f32x4& b) { return ((a[0] * a[0] + a[1] * a[1]) + (a[2] * a[2] + a[3] * a[3])) + ((b[0] * b[0] + b[1] * b[1]) + (b[2] * b[2] + b[3] * b[3])); }
;     __device__ __forceinline__ void operator()(const f32x4 (&acc)[2][2][4][2], const Unit& u, int ui, int wr, int wc, int fr, int fq, LAS unsigned char* lds) const {
;     ...
;                     else if (pn == 6) { *(u32x4*)(CKV + (size_t)row * 256 + c) = pack8(v0, v1); sq += sq8(v0, v1); }
;                     else if (pn == 7) { *(u32x4*)(CQ + (size_t)row * 384 + c) = pack8(v0, v1); sq += sq8(v0, v1); }
.LBB0_359:
	s_andn2_b64 vcc, exec, s[16:17]
	s_cbranch_vccnz .LBB0_361
	v_lshl_add_u64 v[154:155], s[38:39], 0, v[140:141]
	v_lshlrev_b32_e32 v0, 1, v145
	v_lshl_add_u64 v[154:155], v[154:155], 0, v[0:1]
	global_store_dwordx4 v[154:155], v[114:117], off
	v_mov_b32_e32 v154, v133
	v_mov_b32_e32 v155, v129
	v_mov_b32_e32 v116, v131
	v_mov_b32_e32 v117, v127
	v_mov_b32_e32 v114, v130
	v_mov_b32_e32 v115, v126
	v_pk_mul_f32 v[116:117], v[116:117], v[116:117]
	v_pk_mul_f32 v[154:155], v[154:155], v[154:155]
	v_pk_fma_f32 v[114:115], v[114:115], v[114:115], v[116:117]
	v_mov_b32_e32 v116, v132
	v_mov_b32_e32 v117, v128
	v_pk_fma_f32 v[116:117], v[116:117], v[116:117], v[154:155]
	s_nop 0
	v_pk_add_f32 v[114:115], v[114:115], v[116:117]
	s_nop 0
	v_add_f32_e32 v153, v114, v115

; __device__ __forceinline__ float xor32(float x) { auto rr = __builtin_amdgcn_permlane32_swap(__float_as_uint(x), __float_as_uint(x), false, false); return __uint_as_float(((unsigned)(threadIdx.x & 32)) ? rr[0] : rr[1]); }
; __device__ __forceinline__ u32x4 pack8(f32x4 a, f32x4 b) { u32x4 w; w.x = pk2(a[0], a[1]); w.y = pk2(a[2], a[3]); w.z = pk2(b[0], b[1]); w.w = pk2(b[2], b[3]); return w; }
; __device__ __forceinline__ float sq8(const f32x4& a, const f32x4& b) { return ((a[0] * a[0] + a[1] * a[1]) + (a[2] * a[2] + a[3] * a[3])) + ((b[0] * b[0] + b[1] * b[1]) + (b[2] * b[2] + b[3] * b[3])); }
;     __device__ __forceinline__ void operator()(const f32x4 (&acc)[2][2][4][2], const Unit& u, int ui, int wr, int wc, int fr, int fq, LAS unsigned char* lds) const {
;     ...
;                     if (pn < 6) { if (pn < 2) { v0 = v0 * QS_SB; v1 = v1 * QS_SB; } *(u32x4*)(QKV + (size_t)row * 1536 + pn * 256 + c) = pack8(v0, v1); }
;                     else if (pn == 6) { *(u32x4*)(CKV + (size_t)row * 256 + c) = pack8(v0, v1); sq += sq8(v0, v1); }
;                     else if (pn == 7) { *(u32x4*)(CQ + (size_t)row * 384 + c) = pack8(v0, v1); sq += sq8(v0, v1); }
;                     else if (bj == 0) { *(u32x4*)(CQ + (size_t)row * 384 + 256 + c) = pack8(v0, v1); sq += sq8(v0, v1); }
;                     else if (wc == 0) {
;                         const int ib = 8 * (fq & 1);
;                         const f32x4 c0 = *(const f32x4*)(COS + (size_t)row * 16 + ib), c1 = *(const f32x4*)(COS + (size_t)row * 16 + ib + 4);
;                         const f32x4 s0 = *(const f32x4*)(SIN + (size_t)row * 16 + ib), s1 = *(const f32x4*)(SIN + (size_t)row * 16 + ib + 4);
;                         f32x4 p0, p1;
; #pragma unroll
;                         for (int i = 0; i < 4; ++i) { p0[i] = xor32(v0[i]); p1[i] = xor32(v1[i]); }
;                         const float sg = (fq < 2) ? -1.f : 1.f;
;                         const f32x4 o0 = v0 * c0 + p0 * s0 * sg, o1 = v1 * c1 + p1 * s1 * sg;
;                         *(u32x4*)(KR + (size_t)row * 32 + fq * 8) = pack8(o0, o1);
.LBB0_362:
	s_movk_i32 s6, 0xc00
	s_lshl_b32 s62, s26, 8
	v_mad_i64_i32 v[114:115], s[6:7], v138, s6, 0
	s_ashr_i32 s63, s62, 31
	v_lshl_add_u64 v[114:115], s[36:37], 0, v[114:115]
	s_and_b64 vcc, exec, s[16:17]
	v_lshlrev_b32_e32 v0, 1, v145
	v_lshl_add_u64 v[116:117], s[62:63], 1, v[114:115]
	s_cbranch_vccz .LBB0_364
	v_pk_mul_f32 v[114:115], v[132:133], s[96:97] op_sel_hi:[1,0]
	v_pk_mul_f32 v[154:155], v[130:131], s[96:97] op_sel_hi:[1,0]
	v_pk_mul_f32 v[156:157], v[128:129], s[96:97] op_sel_hi:[1,0]
	v_pk_mul_f32 v[158:159], v[126:127], s[96:97] op_sel_hi:[1,0]
	v_cndmask_b32_e64 v129, v129, v157, s[12:13]
	v_cndmask_b32_e64 v145, v128, v156, s[12:13]
	v_cndmask_b32_e64 v128, v127, v159, s[12:13]
	v_cndmask_b32_e64 v153, v126, v158, s[12:13]
	v_cndmask_b32_e64 v115, v133, v115, s[12:13]
	v_cndmask_b32_e64 v114, v132, v114, s[12:13]
	v_cndmask_b32_e64 v126, v131, v155, s[12:13]
	v_cndmask_b32_e64 v127, v130, v154, s[12:13]
	v_cvt_pk_bf16_f32 v126, v127, v126
	v_cvt_pk_bf16_f32 v127, v114, v115
	v_cvt_pk_bf16_f32 v128, v153, v128
	v_cvt_pk_bf16_f32 v129, v145, v129
	v_lshl_add_u64 v[114:115], v[116:117], 0, v[0:1]
	v_mov_b32_e32 v153, 0
	global_store_dwordx4 v[114:115], v[126:129], off
.LBB0_364:
	v_cmp_gt_u32_e32 vcc, 2, v152
	v_mov_b32_e32 v145, v144
	v_mov_b32_e32 v130, v144
	v_cndmask_b32_e64 v114, 1.0, -1.0, vcc
	v_mov_b32_e32 v131, v144
	v_cndmask_b32_e64 v129, 0, 1, s[14:15]
	v_and_b32_e32 v128, 8, v149
	v_mov_b32_e32 v115, v114
	v_lshlrev_b64 v[126:127], 4, v[138:139]
	v_pk_mul_f32 v[124:125], v[124:125], v[130:131]
	v_pk_mul_f32 v[122:123], v[122:123], v[144:145]
	v_pk_mul_f32 v[120:121], v[120:121], v[130:131]
	v_pk_mul_f32 v[118:119], v[118:119], v[144:145]
	v_cmp_ne_u32_e64 s[18:19], 1, v129
	s_andn2_b64 vcc, exec, s[14:15]
	s_mov_b64 s[14:15], -1
	s_cbranch_vccnz .LBB0_376
	s_cmp_lt_i32 s26, 7
	s_cbranch_scc1 .LBB0_373
	s_cmp_lg_u32 s26, 7
	s_cbranch_scc0 .LBB0_370
	s_andn2_b64 vcc, exec, s[56:57]
	s_cbranch_vccnz .LBB0_369
	v_lshlrev_b64 v[158:159], 2, v[126:127]
	v_lshl_add_u64 v[130:131], s[44:45], 0, v[158:159]
	v_lshlrev_b32_e32 v160, 2, v128
	v_mov_b32_e32 v161, v1
	v_lshl_add_u64 v[158:159], s[46:47], 0, v[158:159]
	v_lshl_add_u64 v[154:155], v[130:131], 0, v[160:161]
	v_lshl_add_u64 v[162:163], v[158:159], 0, v[160:161]
	s_waitcnt vmcnt(5)
	v_mov_b32_e32 v130, v214
	v_mov_b32_e32 v131, v215
	v_mov_b32_e32 v132, v216
	v_mov_b32_e32 v133, v217
	v_mov_b32_e32 v154, v218
	v_mov_b32_e32 v155, v219
	v_mov_b32_e32 v156, v220
	v_mov_b32_e32 v157, v221
	v_mov_b32_e32 v158, v222
	v_mov_b32_e32 v159, v223
	v_mov_b32_e32 v160, v224
	v_mov_b32_e32 v161, v225
	v_mov_b32_e32 v162, v226
	v_mov_b32_e32 v163, v227
	v_mov_b32_e32 v164, v228
	v_mov_b32_e32 v165, v229
	global_load_dwordx4 v[214:217], v[202:203], off offset:2048
	global_load_dwordx4 v[218:221], v[202:203], off offset:2064
	global_load_dwordx4 v[222:225], v[204:205], off offset:2048
	global_load_dwordx4 v[226:229], v[204:205], off offset:2064
	v_mov_b32_e32 v129, v122
	v_mov_b32_e32 v166, v122
	s_nop 1
	v_permlane32_swap_b32_e32 v129, v166
	v_cndmask_b32_e64 v166, v129, v166, s[4:5]
	v_mov_b32_e32 v129, v118
	v_mov_b32_e32 v167, v118
	s_nop 1
	v_permlane32_swap_b32_e32 v129, v167
	v_cndmask_b32_e64 v168, v129, v167, s[4:5]
	v_mov_b32_e32 v129, v123
	v_mov_b32_e32 v167, v123
	s_nop 1
	v_permlane32_swap_b32_e32 v129, v167
	v_cndmask_b32_e64 v167, v129, v167, s[4:5]
	v_mov_b32_e32 v129, v119
	v_mov_b32_e32 v169, v119
	s_nop 1
	v_permlane32_swap_b32_e32 v129, v169
	v_cndmask_b32_e64 v169, v129, v169, s[4:5]
	v_mov_b32_e32 v129, v124
	v_mov_b32_e32 v170, v124
	s_nop 1
	v_permlane32_swap_b32_e32 v129, v170
	v_cndmask_b32_e64 v170, v129, v170, s[4:5]
	v_mov_b32_e32 v129, v120
	v_mov_b32_e32 v171, v120
	s_nop 1
	v_permlane32_swap_b32_e32 v129, v171
	v_cndmask_b32_e64 v172, v129, v171, s[4:5]
	v_mov_b32_e32 v129, v125
	v_mov_b32_e32 v171, v125
	s_nop 1
	v_permlane32_swap_b32_e32 v129, v171
	v_cndmask_b32_e64 v171, v129, v171, s[4:5]
	v_mov_b32_e32 v129, v121
	v_mov_b32_e32 v173, v121
	s_nop 1
	v_permlane32_swap_b32_e32 v129, v173
	v_cndmask_b32_e64 v173, v129, v173, s[4:5]
	v_lshlrev_b64 v[144:145], 6, v[138:139]
	v_lshl_add_u64 v[144:145], s[42:43], 0, v[144:145]
	s_waitcnt lgkmcnt(0)
	v_pk_mul_f32 v[160:161], v[160:161], v[170:171]
	v_pk_mul_f32 v[158:159], v[158:159], v[166:167]
	v_mov_b32_e32 v166, v114
	v_mov_b32_e32 v167, v114
	v_pk_mul_f32 v[160:161], v[166:167], v[160:161]
	v_pk_mul_f32 v[158:159], v[114:115], v[158:159]
	v_pk_fma_f32 v[132:133], v[124:125], v[132:133], v[160:161]
	v_pk_mul_f32 v[160:161], v[162:163], v[168:169]
	v_pk_fma_f32 v[130:131], v[122:123], v[130:131], v[158:159]
	v_pk_mul_f32 v[158:159], v[164:165], v[172:173]
	v_pk_mul_f32 v[160:161], v[114:115], v[160:161]
	v_pk_mul_f32 v[158:159], v[166:167], v[158:159]
	v_pk_fma_f32 v[154:155], v[118:119], v[154:155], v[160:161]
	v_pk_fma_f32 v[156:157], v[120:121], v[156:157], v[158:159]
	v_cvt_pk_bf16_f32 v130, v130, v131
	v_cvt_pk_bf16_f32 v131, v132, v133
	v_cvt_pk_bf16_f32 v132, v154, v155
	v_lshlrev_b32_e32 v154, 1, v149
	v_mov_b32_e32 v155, v1
	v_cvt_pk_bf16_f32 v133, v156, v157
	v_lshl_add_u64 v[144:145], v[144:145], 0, v[154:155]
	global_store_dwordx4 v[144:145], v[130:133], off

; __device__ __forceinline__ u32x4 pack8(f32x4 a, f32x4 b) { u32x4 w; w.x = pk2(a[0], a[1]); w.y = pk2(a[2], a[3]); w.z = pk2(b[0], b[1]); w.w = pk2(b[2], b[3]); return w; }
; __device__ __forceinline__ float sq8(const f32x4& a, const f32x4& b) { return ((a[0] * a[0] + a[1] * a[1]) + (a[2] * a[2] + a[3] * a[3])) + ((b[0] * b[0] + b[1] * b[1]) + (b[2] * b[2] + b[3] * b[3])); }
;     __device__ __forceinline__ void operator()(const f32x4 (&acc)[2][2][4][2], const Unit& u, int ui, int wr, int wc, int fr, int fq, LAS unsigned char* lds) const {
;     ...
;                     else if (pn == 6) { *(u32x4*)(CKV + (size_t)row * 256 + c) = pack8(v0, v1); sq += sq8(v0, v1); }
;                     else if (pn == 7) { *(u32x4*)(CQ + (size_t)row * 384 + c) = pack8(v0, v1); sq += sq8(v0, v1); }
;                     else if (bj == 0) { *(u32x4*)(CQ + (size_t)row * 384 + 256 + c) = pack8(v0, v1); sq += sq8(v0, v1); }
.LBB0_370:
	s_andn2_b64 vcc, exec, s[14:15]
	v_mov_b32_e32 v129, v153
	s_cbranch_vccnz .LBB0_372
	v_lshl_add_u64 v[142:143], s[40:41], 0, v[142:143]
	v_cvt_pk_bf16_f32 v130, v122, v123
	v_cvt_pk_bf16_f32 v131, v124, v125
	v_cvt_pk_bf16_f32 v132, v118, v119
	v_cvt_pk_bf16_f32 v133, v120, v121
	v_lshl_add_u64 v[142:143], v[142:143], 0, v[0:1]
	global_store_dwordx4 v[142:143], v[130:133], off offset:256
	v_mov_b32_e32 v142, v125
	v_mov_b32_e32 v143, v121
	v_mov_b32_e32 v132, v123
	v_mov_b32_e32 v133, v119
	v_mov_b32_e32 v130, v122
	v_mov_b32_e32 v131, v118
	v_pk_mul_f32 v[132:133], v[132:133], v[132:133]
	v_pk_mul_f32 v[142:143], v[142:143], v[142:143]
	v_pk_fma_f32 v[130:131], v[130:131], v[130:131], v[132:133]
	v_mov_b32_e32 v132, v124
	v_mov_b32_e32 v133, v120
	v_pk_fma_f32 v[132:133], v[132:133], v[132:133], v[142:143]
	s_nop 0
	v_pk_add_f32 v[130:131], v[130:131], v[132:133]
	s_nop 0
	v_add_f32_e32 v129, v130, v131
	v_add_f32_e32 v129, v129, v153

; __device__ __forceinline__ u32x4 pack8(f32x4 a, f32x4 b) { u32x4 w; w.x = pk2(a[0], a[1]); w.y = pk2(a[2], a[3]); w.z = pk2(b[0], b[1]); w.w = pk2(b[2], b[3]); return w; }
; __device__ __forceinline__ float sq8(const f32x4& a, const f32x4& b) { return ((a[0] * a[0] + a[1] * a[1]) + (a[2] * a[2] + a[3] * a[3])) + ((b[0] * b[0] + b[1] * b[1]) + (b[2] * b[2] + b[3] * b[3])); }
;     __device__ __forceinline__ void operator()(const f32x4 (&acc)[2][2][4][2], const Unit& u, int ui, int wr, int wc, int fr, int fq, LAS unsigned char* lds) const {
;     ...
;                     else if (pn == 6) { *(u32x4*)(CKV + (size_t)row * 256 + c) = pack8(v0, v1); sq += sq8(v0, v1); }
;                     else if (pn == 7) { *(u32x4*)(CQ + (size_t)row * 384 + c) = pack8(v0, v1); sq += sq8(v0, v1); }
.LBB0_373:
	s_andn2_b64 vcc, exec, s[14:15]
	s_cbranch_vccnz .LBB0_375
	v_lshl_add_u64 v[140:141], s[38:39], 0, v[140:141]
	v_cvt_pk_bf16_f32 v130, v122, v123
	v_cvt_pk_bf16_f32 v131, v124, v125
	v_cvt_pk_bf16_f32 v132, v118, v119
	v_cvt_pk_bf16_f32 v133, v120, v121
	v_lshl_add_u64 v[140:141], v[140:141], 0, v[0:1]
	global_store_dwordx4 v[140:141], v[130:133], off offset:256
	v_mov_b32_e32 v140, v125
	v_mov_b32_e32 v141, v121
	v_mov_b32_e32 v132, v123
	v_mov_b32_e32 v133, v119
	v_mov_b32_e32 v130, v122
	v_mov_b32_e32 v131, v118
	v_pk_mul_f32 v[132:133], v[132:133], v[132:133]
	v_pk_mul_f32 v[140:141], v[140:141], v[140:141]
	v_pk_fma_f32 v[130:131], v[130:131], v[130:131], v[132:133]
	v_mov_b32_e32 v132, v124
	v_mov_b32_e32 v133, v120
	v_pk_fma_f32 v[132:133], v[132:133], v[132:133], v[140:141]
	s_nop 0
	v_pk_add_f32 v[130:131], v[130:131], v[132:133]
	s_nop 0
	v_add_f32_e32 v129, v130, v131
	v_add_f32_e32 v129, v129, v153

; __device__ __forceinline__ float xor32(float x) { auto rr = __builtin_amdgcn_permlane32_swap(__float_as_uint(x), __float_as_uint(x), false, false); return __uint_as_float(((unsigned)(threadIdx.x & 32)) ? rr[0] : rr[1]); }
; __device__ __forceinline__ u32x4 pack8(f32x4 a, f32x4 b) { u32x4 w; w.x = pk2(a[0], a[1]); w.y = pk2(a[2], a[3]); w.z = pk2(b[0], b[1]); w.w = pk2(b[2], b[3]); return w; }
; __device__ __forceinline__ float sq8(const f32x4& a, const f32x4& b) { return ((a[0] * a[0] + a[1] * a[1]) + (a[2] * a[2] + a[3] * a[3])) + ((b[0] * b[0] + b[1] * b[1]) + (b[2] * b[2] + b[3] * b[3])); }
;     __device__ __forceinline__ void operator()(const f32x4 (&acc)[2][2][4][2], const Unit& u, int ui, int wr, int wc, int fr, int fq, LAS unsigned char* lds) const {
;     ...
;                     if (pn < 6) { if (pn < 2) { v0 = v0 * QS_SB; v1 = v1 * QS_SB; } *(u32x4*)(QKV + (size_t)row * 1536 + pn * 256 + c) = pack8(v0, v1); }
;                     else if (pn == 6) { *(u32x4*)(CKV + (size_t)row * 256 + c) = pack8(v0, v1); sq += sq8(v0, v1); }
;                     else if (pn == 7) { *(u32x4*)(CQ + (size_t)row * 384 + c) = pack8(v0, v1); sq += sq8(v0, v1); }
;                     else if (bj == 0) { *(u32x4*)(CQ + (size_t)row * 384 + 256 + c) = pack8(v0, v1); sq += sq8(v0, v1); }
;                     else if (wc == 0) {
;                         const int ib = 8 * (fq & 1);
;                         const f32x4 c0 = *(const f32x4*)(COS + (size_t)row * 16 + ib), c1 = *(const f32x4*)(COS + (size_t)row * 16 + ib + 4);
;                         const f32x4 s0 = *(const f32x4*)(SIN + (size_t)row * 16 + ib), s1 = *(const f32x4*)(SIN + (size_t)row * 16 + ib + 4);
;                         f32x4 p0, p1;
; #pragma unroll
;                         for (int i = 0; i < 4; ++i) { p0[i] = xor32(v0[i]); p1[i] = xor32(v1[i]); }
;                         const float sg = (fq < 2) ? -1.f : 1.f;
;                         const f32x4 o0 = v0 * c0 + p0 * s0 * sg, o1 = v1 * c1 + p1 * s1 * sg;
;                         *(u32x4*)(KR + (size_t)row * 32 + fq * 8) = pack8(o0, o1);
;                     }
;                 }
;                 if (pn >= 6) {
;                     sq = fq_sum(sq);
;                     if (fq == 0) { if (pn == 6) SQK[(size_t)row * 4 + wc] = sq; else SQQ[(size_t)row * 8 + (pn - 7) * 4 + wc] = sq; }
;                 }
.LBB0_376:
	s_and_b64 vcc, exec, s[14:15]
	s_cbranch_vccz .LBB0_378
	v_pk_mul_f32 v[130:131], v[124:125], s[96:97] op_sel_hi:[1,0]
	v_pk_mul_f32 v[132:133], v[122:123], s[96:97] op_sel_hi:[1,0]
	v_pk_mul_f32 v[140:141], v[120:121], s[96:97] op_sel_hi:[1,0]
	v_pk_mul_f32 v[142:143], v[118:119], s[96:97] op_sel_hi:[1,0]
	v_cndmask_b32_e64 v121, v121, v141, s[12:13]
	v_cndmask_b32_e64 v129, v120, v140, s[12:13]
	v_cndmask_b32_e64 v120, v119, v143, s[12:13]
	v_cndmask_b32_e64 v140, v118, v142, s[12:13]
	v_cndmask_b32_e64 v119, v125, v131, s[12:13]
	v_cndmask_b32_e64 v124, v124, v130, s[12:13]
	v_cndmask_b32_e64 v118, v123, v133, s[12:13]
	v_cndmask_b32_e64 v122, v122, v132, s[12:13]
	v_cvt_pk_bf16_f32 v118, v122, v118
	v_cvt_pk_bf16_f32 v119, v124, v119
	v_cvt_pk_bf16_f32 v120, v140, v120
	v_cvt_pk_bf16_f32 v121, v129, v121
	v_lshl_add_u64 v[116:117], v[116:117], 0, v[0:1]
	v_mov_b32_e32 v129, v153
	global_store_dwordx4 v[116:117], v[118:121], off offset:256
.LBB0_378:
	s_cmp_gt_i32 s26, 5
	s_cselect_b64 s[64:65], -1, 0
	s_cmp_eq_u32 s26, 6
	s_cselect_b64 s[14:15], -1, 0
	s_lshl_b32 s6, s26, 2
	s_sub_i32 s88, s6, 28
	s_cmp_lt_i32 s26, 6
	v_cmp_eq_u32_e64 s[16:17], 0, v152
	s_cbranch_scc1 .LBB0_382
	v_mov_b32_e32 v116, v129
	v_mov_b32_e32 v117, v129
	v_readlane_b32 s6, v255, 6
	s_nop 0
	v_permlane16_swap_b32_e32 v116, v117
	v_readlane_b32 s7, v255, 7
	s_nop 1
	v_cndmask_b32_e64 v116, v116, v117, s[6:7]
	v_add_f32_e32 v116, v129, v116
	v_mov_b32_e32 v117, v116
	v_mov_b32_e32 v118, v116
	s_nop 1
	v_permlane32_swap_b32_e32 v117, v118
	s_and_saveexec_b64 s[20:21], s[16:17]
	s_cbranch_execz .LBB0_381
	v_cndmask_b32_e64 v117, v117, v118, s[4:5]
	v_add_f32_e32 v120, v116, v117
	v_lshlrev_b64 v[116:117], 5, v[138:139]
	v_lshl_add_u64 v[116:117], s[48:49], 0, v[116:117]
	v_lshl_add_u64 v[116:117], s[88:89], 2, v[116:117]
	v_lshl_add_u64 v[118:119], s[50:51], 0, v[126:127]
	v_cndmask_b32_e64 v117, v117, v119, s[14:15]
	v_cndmask_b32_e64 v116, v116, v118, s[14:15]
	s_lshl_b32 s6, s91, 2
	s_mov_b32 s7, s89
	v_lshl_add_u64 v[116:117], v[116:117], 0, s[6:7]
	global_store_dword v[116:117], v120, off

; __device__ __forceinline__ u32x4 pack8(f32x4 a, f32x4 b) { u32x4 w; w.x = pk2(a[0], a[1]); w.y = pk2(a[2], a[3]); w.z = pk2(b[0], b[1]); w.w = pk2(b[2], b[3]); return w; }
; __device__ __forceinline__ float sq8(const f32x4& a, const f32x4& b) { return ((a[0] * a[0] + a[1] * a[1]) + (a[2] * a[2] + a[3] * a[3])) + ((b[0] * b[0] + b[1] * b[1]) + (b[2] * b[2] + b[3] * b[3])); }
; __device__ __forceinline__ f32x2 rtab_get(LAS unsigned char* lds, int ui, int r) { return ((const LAS f32x2*)(lds + RTAB_OFF))[(ui & 1) * 256 + r]; }
;     __device__ __forceinline__ void operator()(const f32x4 (&acc)[2][2][4][2], const Unit& u, int ui, int wr, int wc, int fr, int fq, LAS unsigned char* lds) const {
;     ...
;                 const int rr = ai * 128 + wr * 64 + m * 16 + fr, row = u.pm * 256 + rr; const float rs = rtab_get(lds, ui, rr)[0];
;                 float sq = 0.f;
; #pragma unroll
;                 for (int bj = 0; bj < 2; ++bj) {
;                     const int c = bj * 128 + wc * 32 + fq * 8;
;                     f32x4 v0 = acc[ai][bj][m][0] * rs, v1 = acc[ai][bj][m][1] * rs;
;                     if (pn < 6) { if (pn < 2) { v0 = v0 * QS_SB; v1 = v1 * QS_SB; } *(u32x4*)(QKV + (size_t)row * 1536 + pn * 256 + c) = pack8(v0, v1); }
;                     else if (pn == 6) { *(u32x4*)(CKV + (size_t)row * 256 + c) = pack8(v0, v1); sq += sq8(v0, v1); }
;                     else if (pn == 7) { *(u32x4*)(CQ + (size_t)row * 384 + c) = pack8(v0, v1); sq += sq8(v0, v1); }
;                     else if (bj == 0) { *(u32x4*)(CQ + (size_t)row * 384 + 256 + c) = pack8(v0, v1); sq += sq8(v0, v1); }
.LBB0_382:
	ds_read_b32 v122, v150 offset:128
	v_add3_u32 v116, s3, v151, 16
	v_ashrrev_i32_e32 v117, 31, v116
	v_mad_i64_i32 v[120:121], s[6:7], v116, s59, 0
	v_lshlrev_b64 v[118:119], 9, v[116:117]
	s_waitcnt lgkmcnt(0)
	v_pk_mul_f32 v[112:113], v[112:113], v[122:123] op_sel_hi:[1,0]
	v_pk_mul_f32 v[110:111], v[110:111], v[122:123] op_sel_hi:[1,0]
	v_pk_mul_f32 v[126:127], v[108:109], v[122:123] op_sel_hi:[1,0]
	v_pk_mul_f32 v[124:125], v[106:107], v[122:123] op_sel_hi:[1,0]
	s_and_b64 vcc, exec, s[18:19]
	s_mov_b64 s[20:21], -1
	s_cbranch_vccnz .LBB0_392
	v_cvt_pk_bf16_f32 v106, v110, v111
	v_cvt_pk_bf16_f32 v107, v112, v113
	v_cvt_pk_bf16_f32 v108, v124, v125
	v_cvt_pk_bf16_f32 v109, v126, v127
	s_cmp_lt_i32 s26, 7
	s_cbranch_scc1 .LBB0_389
	s_cmp_lg_u32 s26, 7
	s_cbranch_scc0 .LBB0_386
	v_lshl_add_u64 v[130:131], s[40:41], 0, v[120:121]
	v_lshl_add_u64 v[130:131], v[130:131], 0, v[0:1]
	v_mov_b32_e32 v132, v111
	v_mov_b32_e32 v133, v125
	global_store_dwordx4 v[130:131], v[106:109], off offset:512
	v_mov_b32_e32 v130, v110
	v_mov_b32_e32 v131, v124
	v_pk_mul_f32 v[132:133], v[132:133], v[132:133]
	v_mov_b32_e32 v140, v113
	v_mov_b32_e32 v141, v127
	v_pk_fma_f32 v[130:131], v[130:131], v[130:131], v[132:133]
	v_mov_b32_e32 v132, v112
	v_mov_b32_e32 v133, v126
	v_pk_mul_f32 v[140:141], v[140:141], v[140:141]
	s_mov_b64 s[20:21], 0
	v_pk_fma_f32 v[132:133], v[132:133], v[132:133], v[140:141]
	s_nop 0
	v_pk_add_f32 v[130:131], v[130:131], v[132:133]
	s_nop 0
	v_add_f32_e32 v129, v130, v131
.LBB0_386:
	s_andn2_b64 vcc, exec, s[20:21]
	s_cbranch_vccnz .LBB0_388
	v_lshl_add_u64 v[130:131], s[40:41], 0, v[120:121]
	v_lshl_add_u64 v[130:131], v[130:131], 0, v[0:1]
	v_mov_b32_e32 v132, v111
	v_mov_b32_e32 v133, v125
	global_store_dwordx4 v[130:131], v[106:109], off
	v_mov_b32_e32 v130, v110
	v_mov_b32_e32 v131, v124
	v_pk_mul_f32 v[132:133], v[132:133], v[132:133]
	v_mov_b32_e32 v140, v113
	v_mov_b32_e32 v141, v127
	v_pk_fma_f32 v[130:131], v[130:131], v[130:131], v[132:133]
	v_mov_b32_e32 v132, v112
	v_mov_b32_e32 v133, v126
	v_pk_mul_f32 v[140:141], v[140:141], v[140:141]
	s_nop 0
	v_pk_fma_f32 v[132:133], v[132:133], v[132:133], v[140:141]
	s_nop 0
	v_pk_add_f32 v[130:131], v[130:131], v[132:133]
	s_nop 0
	v_add_f32_e32 v129, v130, v131

; __device__ __forceinline__ u32x4 pack8(f32x4 a, f32x4 b) { u32x4 w; w.x = pk2(a[0], a[1]); w.y = pk2(a[2], a[3]); w.z = pk2(b[0], b[1]); w.w = pk2(b[2], b[3]); return w; }
; __device__ __forceinline__ float sq8(const f32x4& a, const f32x4& b) { return ((a[0] * a[0] + a[1] * a[1]) + (a[2] * a[2] + a[3] * a[3])) + ((b[0] * b[0] + b[1] * b[1]) + (b[2] * b[2] + b[3] * b[3])); }
;     __device__ __forceinline__ void operator()(const f32x4 (&acc)[2][2][4][2], const Unit& u, int ui, int wr, int wc, int fr, int fq, LAS unsigned char* lds) const {
;     ...
;                     else if (pn == 6) { *(u32x4*)(CKV + (size_t)row * 256 + c) = pack8(v0, v1); sq += sq8(v0, v1); }
;                     else if (pn == 7) { *(u32x4*)(CQ + (size_t)row * 384 + c) = pack8(v0, v1); sq += sq8(v0, v1); }
.LBB0_389:
	s_andn2_b64 vcc, exec, s[20:21]
	s_cbranch_vccnz .LBB0_391
	v_lshl_add_u64 v[130:131], s[38:39], 0, v[118:119]
	v_lshl_add_u64 v[130:131], v[130:131], 0, v[0:1]
	global_store_dwordx4 v[130:131], v[106:109], off
	v_mov_b32_e32 v130, v113
	v_mov_b32_e32 v131, v127
	v_mov_b32_e32 v108, v111
	v_mov_b32_e32 v109, v125
	v_mov_b32_e32 v106, v110
	v_mov_b32_e32 v107, v124
	v_pk_mul_f32 v[108:109], v[108:109], v[108:109]
	v_pk_mul_f32 v[130:131], v[130:131], v[130:131]
	v_pk_fma_f32 v[106:107], v[106:107], v[106:107], v[108:109]
	v_mov_b32_e32 v108, v112
	v_mov_b32_e32 v109, v126
	v_pk_fma_f32 v[108:109], v[108:109], v[108:109], v[130:131]
	s_nop 0
	v_pk_add_f32 v[106:107], v[106:107], v[108:109]
	s_nop 0
	v_add_f32_e32 v129, v106, v107

; __device__ __forceinline__ u32x4 pack8(f32x4 a, f32x4 b) { u32x4 w; w.x = pk2(a[0], a[1]); w.y = pk2(a[2], a[3]); w.z = pk2(b[0], b[1]); w.w = pk2(b[2], b[3]); return w; }
;     __device__ __forceinline__ void operator()(const f32x4 (&acc)[2][2][4][2], const Unit& u, int ui, int wr, int wc, int fr, int fq, LAS unsigned char* lds) const {
;     ...
;                     f32x4 v0 = acc[ai][bj][m][0] * rs, v1 = acc[ai][bj][m][1] * rs;
;                     if (pn < 6) { if (pn < 2) { v0 = v0 * QS_SB; v1 = v1 * QS_SB; } *(u32x4*)(QKV + (size_t)row * 1536 + pn * 256 + c) = pack8(v0, v1); }
.LBB0_392:
	s_movk_i32 s6, 0xc00
	v_mad_i64_i32 v[106:107], s[6:7], v116, s6, 0
	v_lshl_add_u64 v[106:107], s[36:37], 0, v[106:107]
	s_and_b64 vcc, exec, s[20:21]
	v_lshl_add_u64 v[106:107], s[62:63], 1, v[106:107]
	s_cbranch_vccz .LBB0_394
	v_pk_mul_f32 v[108:109], v[112:113], s[96:97] op_sel_hi:[1,0]
	v_pk_mul_f32 v[130:131], v[110:111], s[96:97] op_sel_hi:[1,0]
	v_pk_mul_f32 v[132:133], v[126:127], s[96:97] op_sel_hi:[1,0]
	v_pk_mul_f32 v[140:141], v[124:125], s[96:97] op_sel_hi:[1,0]
	v_cndmask_b32_e64 v123, v127, v133, s[12:13]
	v_cndmask_b32_e64 v126, v126, v132, s[12:13]
	v_cndmask_b32_e64 v125, v125, v141, s[12:13]
	v_cndmask_b32_e64 v124, v124, v140, s[12:13]
	v_cndmask_b32_e64 v109, v113, v109, s[12:13]
	v_cndmask_b32_e64 v112, v112, v108, s[12:13]
	v_cndmask_b32_e64 v108, v111, v131, s[12:13]
	v_cndmask_b32_e64 v110, v110, v130, s[12:13]
	v_cvt_pk_bf16_f32 v108, v110, v108
	v_cvt_pk_bf16_f32 v109, v112, v109
	v_cvt_pk_bf16_f32 v110, v124, v125
	v_cvt_pk_bf16_f32 v111, v126, v123
	v_lshl_add_u64 v[112:113], v[106:107], 0, v[0:1]
	v_mov_b32_e32 v129, 0
	global_store_dwordx4 v[112:113], v[108:111], off

; __device__ __forceinline__ float xor32(float x) { auto rr = __builtin_amdgcn_permlane32_swap(__float_as_uint(x), __float_as_uint(x), false, false); return __uint_as_float(((unsigned)(threadIdx.x & 32)) ? rr[0] : rr[1]); }
; __device__ __forceinline__ u32x4 pack8(f32x4 a, f32x4 b) { u32x4 w; w.x = pk2(a[0], a[1]); w.y = pk2(a[2], a[3]); w.z = pk2(b[0], b[1]); w.w = pk2(b[2], b[3]); return w; }
;     __device__ __forceinline__ void operator()(const f32x4 (&acc)[2][2][4][2], const Unit& u, int ui, int wr, int wc, int fr, int fq, LAS unsigned char* lds) const {
;     ...
;                     else if (wc == 0) {
;                         const int ib = 8 * (fq & 1);
;                         const f32x4 c0 = *(const f32x4*)(COS + (size_t)row * 16 + ib), c1 = *(const f32x4*)(COS + (size_t)row * 16 + ib + 4);
;                         const f32x4 s0 = *(const f32x4*)(SIN + (size_t)row * 16 + ib), s1 = *(const f32x4*)(SIN + (size_t)row * 16 + ib + 4);
;                         f32x4 p0, p1;
; #pragma unroll
;                         for (int i = 0; i < 4; ++i) { p0[i] = xor32(v0[i]); p1[i] = xor32(v1[i]); }
;                         const float sg = (fq < 2) ? -1.f : 1.f;
;                         const f32x4 o0 = v0 * c0 + p0 * s0 * sg, o1 = v1 * c1 + p1 * s1 * sg;
;                         *(u32x4*)(KR + (size_t)row * 32 + fq * 8) = pack8(o0, o1);
.LBB0_397:
	s_cmp_lt_i32 s26, 7
	s_cbranch_scc1 .LBB0_405
	s_cmp_lg_u32 s26, 7
	s_cbranch_scc0 .LBB0_402
	s_andn2_b64 vcc, exec, s[56:57]
	s_cbranch_vccnz .LBB0_401
	v_lshlrev_b64 v[130:131], 2, v[108:109]
	v_lshl_add_u64 v[110:111], s[44:45], 0, v[130:131]
	v_lshlrev_b32_e32 v132, 2, v128
	v_mov_b32_e32 v133, v1
	v_lshl_add_u64 v[130:131], s[46:47], 0, v[130:131]
	v_lshl_add_u64 v[122:123], v[110:111], 0, v[132:133]
	v_lshl_add_u64 v[140:141], v[130:131], 0, v[132:133]
	s_waitcnt vmcnt(8)
	v_mov_b32_e32 v110, v174
	v_mov_b32_e32 v111, v175
	v_mov_b32_e32 v112, v176
	v_mov_b32_e32 v113, v177
	v_mov_b32_e32 v122, v178
	v_mov_b32_e32 v123, v179
	v_mov_b32_e32 v124, v180
	v_mov_b32_e32 v125, v181
	v_mov_b32_e32 v130, v182
	v_mov_b32_e32 v131, v183
	v_mov_b32_e32 v132, v184
	v_mov_b32_e32 v133, v185
	v_mov_b32_e32 v140, v230
	v_mov_b32_e32 v141, v231
	v_mov_b32_e32 v142, v232
	v_mov_b32_e32 v143, v233
	global_load_dwordx4 v[174:177], v[202:203], off offset:3072
	global_load_dwordx4 v[178:181], v[202:203], off offset:3088
	global_load_dwordx4 v[182:185], v[204:205], off offset:3072
	global_load_dwordx4 v[230:233], v[204:205], off offset:3088
	v_mov_b32_e32 v139, v102
	v_mov_b32_e32 v144, v102
	s_nop 1
	v_permlane32_swap_b32_e32 v139, v144
	v_cndmask_b32_e64 v144, v139, v144, s[4:5]
	v_mov_b32_e32 v139, v98
	v_mov_b32_e32 v145, v98
	s_nop 1
	v_permlane32_swap_b32_e32 v139, v145
	v_cndmask_b32_e64 v152, v139, v145, s[4:5]
	v_mov_b32_e32 v139, v103
	v_mov_b32_e32 v145, v103
	s_nop 1
	v_permlane32_swap_b32_e32 v139, v145
	v_cndmask_b32_e64 v145, v139, v145, s[4:5]
	v_mov_b32_e32 v139, v99
	v_mov_b32_e32 v153, v99
	s_nop 1
	v_permlane32_swap_b32_e32 v139, v153
	v_cndmask_b32_e64 v153, v139, v153, s[4:5]
	v_mov_b32_e32 v139, v104
	v_mov_b32_e32 v154, v104
	s_nop 1
	v_permlane32_swap_b32_e32 v139, v154
	v_cndmask_b32_e64 v154, v139, v154, s[4:5]
	v_mov_b32_e32 v139, v100
	v_mov_b32_e32 v155, v100
	s_nop 1
	v_permlane32_swap_b32_e32 v139, v155
	v_cndmask_b32_e64 v156, v139, v155, s[4:5]
	v_mov_b32_e32 v139, v105
	v_mov_b32_e32 v155, v105
	s_nop 1
	v_permlane32_swap_b32_e32 v139, v155
	v_cndmask_b32_e64 v155, v139, v155, s[4:5]
	v_mov_b32_e32 v139, v101
	v_mov_b32_e32 v157, v101
	s_nop 1
	v_permlane32_swap_b32_e32 v139, v157
	v_cndmask_b32_e64 v157, v139, v157, s[4:5]
	v_lshlrev_b64 v[126:127], 6, v[116:117]
	s_waitcnt lgkmcnt(0)
	v_pk_mul_f32 v[132:133], v[132:133], v[154:155]
	v_pk_mul_f32 v[130:131], v[130:131], v[144:145]
	v_mov_b32_e32 v144, v114
	v_mov_b32_e32 v145, v114
	v_pk_mul_f32 v[130:131], v[114:115], v[130:131]
	v_pk_mul_f32 v[132:133], v[144:145], v[132:133]
	v_pk_fma_f32 v[110:111], v[102:103], v[110:111], v[130:131]
	v_pk_fma_f32 v[112:113], v[104:105], v[112:113], v[132:133]
	v_pk_mul_f32 v[130:131], v[142:143], v[156:157]
	v_pk_mul_f32 v[132:133], v[140:141], v[152:153]
	v_pk_mul_f32 v[130:131], v[144:145], v[130:131]
	v_pk_mul_f32 v[132:133], v[114:115], v[132:133]
	v_pk_fma_f32 v[124:125], v[100:101], v[124:125], v[130:131]
	v_pk_fma_f32 v[122:123], v[98:99], v[122:123], v[132:133]
	v_cvt_pk_bf16_f32 v110, v110, v111
	v_cvt_pk_bf16_f32 v111, v112, v113
	v_cvt_pk_bf16_f32 v112, v122, v123
	v_cvt_pk_bf16_f32 v113, v124, v125
	v_lshl_add_u64 v[122:123], s[42:43], 0, v[126:127]
	v_lshlrev_b32_e32 v124, 1, v149
	v_mov_b32_e32 v125, v1
	v_lshl_add_u64 v[122:123], v[122:123], 0, v[124:125]
	global_store_dwordx4 v[122:123], v[110:113], off

; __device__ __forceinline__ u32x4 pack8(f32x4 a, f32x4 b) { u32x4 w; w.x = pk2(a[0], a[1]); w.y = pk2(a[2], a[3]); w.z = pk2(b[0], b[1]); w.w = pk2(b[2], b[3]); return w; }
; __device__ __forceinline__ float sq8(const f32x4& a, const f32x4& b) { return ((a[0] * a[0] + a[1] * a[1]) + (a[2] * a[2] + a[3] * a[3])) + ((b[0] * b[0] + b[1] * b[1]) + (b[2] * b[2] + b[3] * b[3])); }
;     __device__ __forceinline__ void operator()(const f32x4 (&acc)[2][2][4][2], const Unit& u, int ui, int wr, int wc, int fr, int fq, LAS unsigned char* lds) const {
;     ...
;                     else if (pn == 6) { *(u32x4*)(CKV + (size_t)row * 256 + c) = pack8(v0, v1); sq += sq8(v0, v1); }
;                     else if (pn == 7) { *(u32x4*)(CQ + (size_t)row * 384 + c) = pack8(v0, v1); sq += sq8(v0, v1); }
;                     else if (bj == 0) { *(u32x4*)(CQ + (size_t)row * 384 + 256 + c) = pack8(v0, v1); sq += sq8(v0, v1); }
.LBB0_402:
	s_andn2_b64 vcc, exec, s[20:21]
	v_mov_b32_e32 v110, v129
	s_cbranch_vccnz .LBB0_404
	v_lshl_add_u64 v[120:121], s[40:41], 0, v[120:121]
	v_cvt_pk_bf16_f32 v110, v102, v103
	v_cvt_pk_bf16_f32 v111, v104, v105
	v_cvt_pk_bf16_f32 v112, v98, v99
	v_cvt_pk_bf16_f32 v113, v100, v101
	v_lshl_add_u64 v[120:121], v[120:121], 0, v[0:1]
	global_store_dwordx4 v[120:121], v[110:113], off offset:256
	v_mov_b32_e32 v120, v105
	v_mov_b32_e32 v121, v101
	v_mov_b32_e32 v112, v103
	v_mov_b32_e32 v113, v99
	v_mov_b32_e32 v110, v102
	v_mov_b32_e32 v111, v98
	v_pk_mul_f32 v[112:113], v[112:113], v[112:113]
	v_pk_mul_f32 v[120:121], v[120:121], v[120:121]
	v_pk_fma_f32 v[110:111], v[110:111], v[110:111], v[112:113]
	v_mov_b32_e32 v112, v104
	v_mov_b32_e32 v113, v100
	v_pk_fma_f32 v[112:113], v[112:113], v[112:113], v[120:121]
	s_nop 0
	v_pk_add_f32 v[110:111], v[110:111], v[112:113]
	s_nop 0
	v_add_f32_e32 v110, v110, v111
	v_add_f32_e32 v110, v110, v129

; __device__ __forceinline__ u32x4 pack8(f32x4 a, f32x4 b) { u32x4 w; w.x = pk2(a[0], a[1]); w.y = pk2(a[2], a[3]); w.z = pk2(b[0], b[1]); w.w = pk2(b[2], b[3]); return w; }
; __device__ __forceinline__ float sq8(const f32x4& a, const f32x4& b) { return ((a[0] * a[0] + a[1] * a[1]) + (a[2] * a[2] + a[3] * a[3])) + ((b[0] * b[0] + b[1] * b[1]) + (b[2] * b[2] + b[3] * b[3])); }
;     __device__ __forceinline__ void operator()(const f32x4 (&acc)[2][2][4][2], const Unit& u, int ui, int wr, int wc, int fr, int fq, LAS unsigned char* lds) const {
;     ...
;                     else if (pn == 6) { *(u32x4*)(CKV + (size_t)row * 256 + c) = pack8(v0, v1); sq += sq8(v0, v1); }
;                     else if (pn == 7) { *(u32x4*)(CQ + (size_t)row * 384 + c) = pack8(v0, v1); sq += sq8(v0, v1); }
.LBB0_405:
	s_andn2_b64 vcc, exec, s[20:21]
	s_cbranch_vccnz .LBB0_407
	v_lshl_add_u64 v[118:119], s[38:39], 0, v[118:119]
	v_cvt_pk_bf16_f32 v110, v102, v103
	v_cvt_pk_bf16_f32 v111, v104, v105
	v_cvt_pk_bf16_f32 v112, v98, v99
	v_cvt_pk_bf16_f32 v113, v100, v101
	v_lshl_add_u64 v[118:119], v[118:119], 0, v[0:1]
	global_store_dwordx4 v[118:119], v[110:113], off offset:256
	v_mov_b32_e32 v118, v105
	v_mov_b32_e32 v119, v101
	v_mov_b32_e32 v112, v103
	v_mov_b32_e32 v113, v99
	v_mov_b32_e32 v110, v102
	v_mov_b32_e32 v111, v98
	v_pk_mul_f32 v[112:113], v[112:113], v[112:113]
	v_pk_mul_f32 v[118:119], v[118:119], v[118:119]
	v_pk_fma_f32 v[110:111], v[110:111], v[110:111], v[112:113]
	v_mov_b32_e32 v112, v104
	v_mov_b32_e32 v113, v100
	v_pk_fma_f32 v[112:113], v[112:113], v[112:113], v[118:119]
	s_nop 0
	v_pk_add_f32 v[110:111], v[110:111], v[112:113]
	s_nop 0
	v_add_f32_e32 v110, v110, v111
	v_add_f32_e32 v110, v110, v129

; __device__ __forceinline__ u32x4 pack8(f32x4 a, f32x4 b) { u32x4 w; w.x = pk2(a[0], a[1]); w.y = pk2(a[2], a[3]); w.z = pk2(b[0], b[1]); w.w = pk2(b[2], b[3]); return w; }
; __device__ __forceinline__ float fq_sum(float v) { v += xor16(v); v += xor32(v); return v; }
;     __device__ __forceinline__ void operator()(const f32x4 (&acc)[2][2][4][2], const Unit& u, int ui, int wr, int wc, int fr, int fq, LAS unsigned char* lds) const {
;     ...
;                     if (pn < 6) { if (pn < 2) { v0 = v0 * QS_SB; v1 = v1 * QS_SB; } *(u32x4*)(QKV + (size_t)row * 1536 + pn * 256 + c) = pack8(v0, v1); }
;     ...
;                 if (pn >= 6) {
;                     sq = fq_sum(sq);
;                     if (fq == 0) { if (pn == 6) SQK[(size_t)row * 4 + wc] = sq; else SQQ[(size_t)row * 8 + (pn - 7) * 4 + wc] = sq; }
;                 }
.LBB0_408:
	v_pk_mul_f32 v[110:111], v[104:105], s[96:97] op_sel_hi:[1,0]
	v_pk_mul_f32 v[112:113], v[102:103], s[96:97] op_sel_hi:[1,0]
	v_pk_mul_f32 v[118:119], v[100:101], s[96:97] op_sel_hi:[1,0]
	v_pk_mul_f32 v[120:121], v[98:99], s[96:97] op_sel_hi:[1,0]
	v_cndmask_b32_e64 v101, v101, v119, s[12:13]
	v_cndmask_b32_e64 v118, v100, v118, s[12:13]
	v_cndmask_b32_e64 v100, v99, v121, s[12:13]
	v_cndmask_b32_e64 v119, v98, v120, s[12:13]
	v_cndmask_b32_e64 v99, v105, v111, s[12:13]
	v_cndmask_b32_e64 v104, v104, v110, s[12:13]
	v_cndmask_b32_e64 v98, v103, v113, s[12:13]
	v_cndmask_b32_e64 v102, v102, v112, s[12:13]
	v_cvt_pk_bf16_f32 v98, v102, v98
	v_cvt_pk_bf16_f32 v99, v104, v99
	v_cvt_pk_bf16_f32 v100, v119, v100
	v_cvt_pk_bf16_f32 v101, v118, v101
	v_lshl_add_u64 v[102:103], v[106:107], 0, v[0:1]
	v_mov_b32_e32 v110, v129
	global_store_dwordx4 v[102:103], v[98:101], off offset:256
	s_nop 1
	v_cndmask_b32_e64 v98, 0, 1, s[64:65]
	v_cmp_ne_u32_e64 s[20:21], 1, v98
	s_andn2_b64 vcc, exec, s[64:65]
	s_cbranch_vccnz .LBB0_412
.LBB0_409:
	v_mov_b32_e32 v98, v110
	v_mov_b32_e32 v99, v110
	v_readlane_b32 s6, v255, 6
	s_nop 0
	v_permlane16_swap_b32_e32 v98, v99
	v_readlane_b32 s7, v255, 7
	s_nop 1
	v_cndmask_b32_e64 v98, v98, v99, s[6:7]
	v_add_f32_e32 v98, v110, v98
	v_mov_b32_e32 v99, v98
	v_mov_b32_e32 v100, v98
	s_nop 1
	v_permlane32_swap_b32_e32 v99, v100
	s_and_saveexec_b64 s[64:65], s[16:17]
	s_cbranch_execz .LBB0_411
	v_cndmask_b32_e64 v99, v99, v100, s[4:5]
	v_lshlrev_b64 v[100:101], 5, v[116:117]
	v_lshl_add_u64 v[100:101], s[48:49], 0, v[100:101]
	v_add_f32_e32 v102, v98, v99
	v_lshl_add_u64 v[98:99], s[50:51], 0, v[108:109]
	v_lshl_add_u64 v[100:101], s[88:89], 2, v[100:101]
	v_cndmask_b32_e64 v99, v101, v99, s[14:15]
	v_cndmask_b32_e64 v98, v100, v98, s[14:15]
	s_lshl_b32 s6, s91, 2
	s_mov_b32 s7, s89
	v_lshl_add_u64 v[98:99], v[98:99], 0, s[6:7]
	global_store_dword v[98:99], v102, off

; __device__ __forceinline__ u32x4 pack8(f32x4 a, f32x4 b) { u32x4 w; w.x = pk2(a[0], a[1]); w.y = pk2(a[2], a[3]); w.z = pk2(b[0], b[1]); w.w = pk2(b[2], b[3]); return w; }
; __device__ __forceinline__ float sq8(const f32x4& a, const f32x4& b) { return ((a[0] * a[0] + a[1] * a[1]) + (a[2] * a[2] + a[3] * a[3])) + ((b[0] * b[0] + b[1] * b[1]) + (b[2] * b[2] + b[3] * b[3])); }
; __device__ __forceinline__ f32x2 rtab_get(LAS unsigned char* lds, int ui, int r) { return ((const LAS f32x2*)(lds + RTAB_OFF))[(ui & 1) * 256 + r]; }
;     __device__ __forceinline__ void operator()(const f32x4 (&acc)[2][2][4][2], const Unit& u, int ui, int wr, int wc, int fr, int fq, LAS unsigned char* lds) const {
;     ...
;                 const int rr = ai * 128 + wr * 64 + m * 16 + fr, row = u.pm * 256 + rr; const float rs = rtab_get(lds, ui, rr)[0];
;                 float sq = 0.f;
; #pragma unroll
;                 for (int bj = 0; bj < 2; ++bj) {
;                     const int c = bj * 128 + wc * 32 + fq * 8;
;                     f32x4 v0 = acc[ai][bj][m][0] * rs, v1 = acc[ai][bj][m][1] * rs;
;                     if (pn < 6) { if (pn < 2) { v0 = v0 * QS_SB; v1 = v1 * QS_SB; } *(u32x4*)(QKV + (size_t)row * 1536 + pn * 256 + c) = pack8(v0, v1); }
;                     else if (pn == 6) { *(u32x4*)(CKV + (size_t)row * 256 + c) = pack8(v0, v1); sq += sq8(v0, v1); }
;                     else if (pn == 7) { *(u32x4*)(CQ + (size_t)row * 384 + c) = pack8(v0, v1); sq += sq8(v0, v1); }
;                     else if (bj == 0) { *(u32x4*)(CQ + (size_t)row * 384 + 256 + c) = pack8(v0, v1); sq += sq8(v0, v1); }
.LBB0_412:
	ds_read_b32 v104, v150 offset:256
	v_add3_u32 v98, s3, v151, 32
	v_ashrrev_i32_e32 v99, 31, v98
	v_mad_i64_i32 v[102:103], s[6:7], v98, s59, 0
	v_lshlrev_b64 v[100:101], 9, v[98:99]
	s_waitcnt lgkmcnt(0)
	v_pk_mul_f32 v[96:97], v[96:97], v[104:105] op_sel_hi:[1,0]
	v_pk_mul_f32 v[94:95], v[94:95], v[104:105] op_sel_hi:[1,0]
	v_pk_mul_f32 v[108:109], v[92:93], v[104:105] op_sel_hi:[1,0]
	v_pk_mul_f32 v[106:107], v[90:91], v[104:105] op_sel_hi:[1,0]
	s_and_b64 vcc, exec, s[18:19]
	s_mov_b64 s[64:65], -1
	s_cbranch_vccnz .LBB0_422
	v_cvt_pk_bf16_f32 v90, v94, v95
	v_cvt_pk_bf16_f32 v91, v96, v97
	v_cvt_pk_bf16_f32 v92, v106, v107
	v_cvt_pk_bf16_f32 v93, v108, v109
	s_cmp_lt_i32 s26, 7
	s_cbranch_scc1 .LBB0_419
	s_cmp_lg_u32 s26, 7
	s_cbranch_scc0 .LBB0_416
	v_lshl_add_u64 v[110:111], s[40:41], 0, v[102:103]
	v_lshl_add_u64 v[110:111], v[110:111], 0, v[0:1]
	v_mov_b32_e32 v112, v95
	v_mov_b32_e32 v113, v107
	global_store_dwordx4 v[110:111], v[90:93], off offset:512
	v_mov_b32_e32 v110, v94
	v_mov_b32_e32 v111, v106
	v_pk_mul_f32 v[112:113], v[112:113], v[112:113]
	v_mov_b32_e32 v116, v97
	v_mov_b32_e32 v117, v109
	v_pk_fma_f32 v[110:111], v[110:111], v[110:111], v[112:113]
	v_mov_b32_e32 v112, v96
	v_mov_b32_e32 v113, v108
	v_pk_mul_f32 v[116:117], v[116:117], v[116:117]
	s_mov_b64 s[64:65], 0
	v_pk_fma_f32 v[112:113], v[112:113], v[112:113], v[116:117]
	s_nop 0
	v_pk_add_f32 v[110:111], v[110:111], v[112:113]
	s_nop 0
	v_add_f32_e32 v110, v110, v111
.LBB0_416:
	s_andn2_b64 vcc, exec, s[64:65]
	s_cbranch_vccnz .LBB0_418
	v_lshl_add_u64 v[110:111], s[40:41], 0, v[102:103]
	v_lshl_add_u64 v[110:111], v[110:111], 0, v[0:1]
	v_mov_b32_e32 v112, v95
	v_mov_b32_e32 v113, v107
	global_store_dwordx4 v[110:111], v[90:93], off
	v_mov_b32_e32 v110, v94
	v_mov_b32_e32 v111, v106
	v_pk_mul_f32 v[112:113], v[112:113], v[112:113]
	v_mov_b32_e32 v116, v97
	v_mov_b32_e32 v117, v109
	v_pk_fma_f32 v[110:111], v[110:111], v[110:111], v[112:113]
	v_mov_b32_e32 v112, v96
	v_mov_b32_e32 v113, v108
	v_pk_mul_f32 v[116:117], v[116:117], v[116:117]
	s_nop 0
	v_pk_fma_f32 v[112:113], v[112:113], v[112:113], v[116:117]
	s_nop 0
	v_pk_add_f32 v[110:111], v[110:111], v[112:113]
	s_nop 0
	v_add_f32_e32 v110, v110, v111

; __device__ __forceinline__ u32x4 pack8(f32x4 a, f32x4 b) { u32x4 w; w.x = pk2(a[0], a[1]); w.y = pk2(a[2], a[3]); w.z = pk2(b[0], b[1]); w.w = pk2(b[2], b[3]); return w; }
; __device__ __forceinline__ float sq8(const f32x4& a, const f32x4& b) { return ((a[0] * a[0] + a[1] * a[1]) + (a[2] * a[2] + a[3] * a[3])) + ((b[0] * b[0] + b[1] * b[1]) + (b[2] * b[2] + b[3] * b[3])); }
;     __device__ __forceinline__ void operator()(const f32x4 (&acc)[2][2][4][2], const Unit& u, int ui, int wr, int wc, int fr, int fq, LAS unsigned char* lds) const {
;     ...
;                     f32x4 v0 = acc[ai][bj][m][0] * rs, v1 = acc[ai][bj][m][1] * rs;
;                     if (pn < 6) { if (pn < 2) { v0 = v0 * QS_SB; v1 = v1 * QS_SB; } *(u32x4*)(QKV + (size_t)row * 1536 + pn * 256 + c) = pack8(v0, v1); }
;                     else if (pn == 6) { *(u32x4*)(CKV + (size_t)row * 256 + c) = pack8(v0, v1); sq += sq8(v0, v1); }
.LBB0_419:
	s_andn2_b64 vcc, exec, s[64:65]
	s_cbranch_vccnz .LBB0_421
	v_lshl_add_u64 v[110:111], s[38:39], 0, v[100:101]
	v_lshl_add_u64 v[110:111], v[110:111], 0, v[0:1]
	global_store_dwordx4 v[110:111], v[90:93], off
	v_mov_b32_e32 v110, v97
	v_mov_b32_e32 v111, v109
	v_mov_b32_e32 v92, v95
	v_mov_b32_e32 v93, v107
	v_mov_b32_e32 v90, v94
	v_mov_b32_e32 v91, v106
	v_pk_mul_f32 v[92:93], v[92:93], v[92:93]
	v_pk_mul_f32 v[110:111], v[110:111], v[110:111]
	v_pk_fma_f32 v[90:91], v[90:91], v[90:91], v[92:93]
	v_mov_b32_e32 v92, v96
	v_mov_b32_e32 v93, v108
	v_pk_fma_f32 v[92:93], v[92:93], v[92:93], v[110:111]
	s_nop 0
	v_pk_add_f32 v[90:91], v[90:91], v[92:93]
	s_nop 0
	v_add_f32_e32 v110, v90, v91

; __device__ __forceinline__ u32x4 pack8(f32x4 a, f32x4 b) { u32x4 w; w.x = pk2(a[0], a[1]); w.y = pk2(a[2], a[3]); w.z = pk2(b[0], b[1]); w.w = pk2(b[2], b[3]); return w; }
;     __device__ __forceinline__ void operator()(const f32x4 (&acc)[2][2][4][2], const Unit& u, int ui, int wr, int wc, int fr, int fq, LAS unsigned char* lds) const {
;     ...
;                     f32x4 v0 = acc[ai][bj][m][0] * rs, v1 = acc[ai][bj][m][1] * rs;
;                     if (pn < 6) { if (pn < 2) { v0 = v0 * QS_SB; v1 = v1 * QS_SB; } *(u32x4*)(QKV + (size_t)row * 1536 + pn * 256 + c) = pack8(v0, v1); }
.LBB0_422:
	s_movk_i32 s6, 0xc00
	v_mad_i64_i32 v[90:91], s[6:7], v98, s6, 0
	v_lshl_add_u64 v[90:91], s[36:37], 0, v[90:91]
	s_and_b64 vcc, exec, s[64:65]
	v_lshl_add_u64 v[90:91], s[62:63], 1, v[90:91]
	s_cbranch_vccz .LBB0_424
	v_pk_mul_f32 v[92:93], v[96:97], s[96:97] op_sel_hi:[1,0]
	v_pk_mul_f32 v[110:111], v[94:95], s[96:97] op_sel_hi:[1,0]
	v_pk_mul_f32 v[112:113], v[108:109], s[96:97] op_sel_hi:[1,0]
	v_pk_mul_f32 v[116:117], v[106:107], s[96:97] op_sel_hi:[1,0]
	v_cndmask_b32_e64 v105, v109, v113, s[12:13]
	v_cndmask_b32_e64 v108, v108, v112, s[12:13]
	v_cndmask_b32_e64 v107, v107, v117, s[12:13]
	v_cndmask_b32_e64 v106, v106, v116, s[12:13]
	v_cndmask_b32_e64 v93, v97, v93, s[12:13]
	v_cndmask_b32_e64 v96, v96, v92, s[12:13]
	v_cndmask_b32_e64 v92, v95, v111, s[12:13]
	v_cndmask_b32_e64 v94, v94, v110, s[12:13]
	v_cvt_pk_bf16_f32 v92, v94, v92
	v_cvt_pk_bf16_f32 v93, v96, v93
	v_cvt_pk_bf16_f32 v94, v106, v107
	v_cvt_pk_bf16_f32 v95, v108, v105
	v_lshl_add_u64 v[96:97], v[90:91], 0, v[0:1]
	v_mov_b32_e32 v110, 0
	global_store_dwordx4 v[96:97], v[92:95], off

; __device__ __forceinline__ float xor32(float x) { auto rr = __builtin_amdgcn_permlane32_swap(__float_as_uint(x), __float_as_uint(x), false, false); return __uint_as_float(((unsigned)(threadIdx.x & 32)) ? rr[0] : rr[1]); }
; __device__ __forceinline__ u32x4 pack8(f32x4 a, f32x4 b) { u32x4 w; w.x = pk2(a[0], a[1]); w.y = pk2(a[2], a[3]); w.z = pk2(b[0], b[1]); w.w = pk2(b[2], b[3]); return w; }
;     __device__ __forceinline__ void operator()(const f32x4 (&acc)[2][2][4][2], const Unit& u, int ui, int wr, int wc, int fr, int fq, LAS unsigned char* lds) const {
;     ...
;                     else if (wc == 0) {
;                         const int ib = 8 * (fq & 1);
;                         const f32x4 c0 = *(const f32x4*)(COS + (size_t)row * 16 + ib), c1 = *(const f32x4*)(COS + (size_t)row * 16 + ib + 4);
;                         const f32x4 s0 = *(const f32x4*)(SIN + (size_t)row * 16 + ib), s1 = *(const f32x4*)(SIN + (size_t)row * 16 + ib + 4);
;                         f32x4 p0, p1;
; #pragma unroll
;                         for (int i = 0; i < 4; ++i) { p0[i] = xor32(v0[i]); p1[i] = xor32(v1[i]); }
;                         const float sg = (fq < 2) ? -1.f : 1.f;
;                         const f32x4 o0 = v0 * c0 + p0 * s0 * sg, o1 = v1 * c1 + p1 * s1 * sg;
;                         *(u32x4*)(KR + (size_t)row * 32 + fq * 8) = pack8(o0, o1);
.LBB0_427:
	s_cmp_lt_i32 s26, 7
	s_cbranch_scc1 .LBB0_435
	s_cmp_lg_u32 s26, 7
	s_cbranch_scc0 .LBB0_432
	s_andn2_b64 vcc, exec, s[56:57]
	s_cbranch_vccnz .LBB0_431
	v_lshlrev_b64 v[112:113], 2, v[92:93]
	v_lshl_add_u64 v[94:95], s[44:45], 0, v[112:113]
	v_lshlrev_b32_e32 v116, 2, v128
	v_mov_b32_e32 v117, v1
	v_lshl_add_u64 v[112:113], s[46:47], 0, v[112:113]
	v_lshl_add_u64 v[104:105], v[94:95], 0, v[116:117]
	v_lshl_add_u64 v[112:113], v[112:113], 0, v[116:117]
	s_waitcnt vmcnt(10)
	v_mov_b32_e32 v94, v214
	v_mov_b32_e32 v95, v215
	v_mov_b32_e32 v96, v216
	v_mov_b32_e32 v97, v217
	v_mov_b32_e32 v104, v218
	v_mov_b32_e32 v105, v219
	v_mov_b32_e32 v106, v220
	v_mov_b32_e32 v107, v221
	v_mov_b32_e32 v116, v222
	v_mov_b32_e32 v117, v223
	v_mov_b32_e32 v118, v224
	v_mov_b32_e32 v119, v225
	v_mov_b32_e32 v120, v226
	v_mov_b32_e32 v121, v227
	v_mov_b32_e32 v122, v228
	v_mov_b32_e32 v123, v229
	global_load_dwordx4 v[214:217], v[206:207], off
	global_load_dwordx4 v[218:221], v[206:207], off offset:16
	global_load_dwordx4 v[222:225], v[208:209], off
	global_load_dwordx4 v[226:229], v[208:209], off offset:16
	v_mov_b32_e32 v111, v86
	v_mov_b32_e32 v112, v86
	s_nop 1
	v_permlane32_swap_b32_e32 v111, v112
	v_cndmask_b32_e64 v112, v111, v112, s[4:5]
	v_mov_b32_e32 v111, v82
	v_mov_b32_e32 v113, v82
	s_nop 1
	v_permlane32_swap_b32_e32 v111, v113
	v_cndmask_b32_e64 v124, v111, v113, s[4:5]
	v_mov_b32_e32 v111, v87
	v_mov_b32_e32 v113, v87
	s_nop 1
	v_permlane32_swap_b32_e32 v111, v113
	v_cndmask_b32_e64 v113, v111, v113, s[4:5]
	v_mov_b32_e32 v111, v83
	v_mov_b32_e32 v125, v83
	s_nop 1
	v_permlane32_swap_b32_e32 v111, v125
	v_cndmask_b32_e64 v125, v111, v125, s[4:5]
	v_mov_b32_e32 v111, v88
	v_mov_b32_e32 v126, v88
	s_nop 1
	v_permlane32_swap_b32_e32 v111, v126
	v_cndmask_b32_e64 v126, v111, v126, s[4:5]
	v_mov_b32_e32 v111, v84
	v_mov_b32_e32 v127, v84
	s_nop 1
	v_permlane32_swap_b32_e32 v111, v127
	v_cndmask_b32_e64 v130, v111, v127, s[4:5]
	v_mov_b32_e32 v111, v89
	v_mov_b32_e32 v127, v89
	s_nop 1
	v_permlane32_swap_b32_e32 v111, v127
	v_cndmask_b32_e64 v127, v111, v127, s[4:5]
	v_mov_b32_e32 v111, v85
	v_mov_b32_e32 v129, v85
	s_nop 1
	v_permlane32_swap_b32_e32 v111, v129
	v_cndmask_b32_e64 v131, v111, v129, s[4:5]
	v_lshlrev_b64 v[108:109], 6, v[98:99]
	s_waitcnt lgkmcnt(0)
	v_pk_mul_f32 v[118:119], v[118:119], v[126:127]
	v_pk_mul_f32 v[112:113], v[116:117], v[112:113]
	v_mov_b32_e32 v116, v114
	v_mov_b32_e32 v117, v114
	v_pk_mul_f32 v[112:113], v[114:115], v[112:113]
	v_pk_mul_f32 v[118:119], v[116:117], v[118:119]
	v_pk_fma_f32 v[94:95], v[86:87], v[94:95], v[112:113]
	v_pk_fma_f32 v[96:97], v[88:89], v[96:97], v[118:119]
	v_pk_mul_f32 v[112:113], v[122:123], v[130:131]
	v_pk_mul_f32 v[118:119], v[120:121], v[124:125]
	v_pk_mul_f32 v[112:113], v[116:117], v[112:113]
	v_pk_mul_f32 v[118:119], v[114:115], v[118:119]
	v_pk_fma_f32 v[106:107], v[84:85], v[106:107], v[112:113]
	v_pk_fma_f32 v[104:105], v[82:83], v[104:105], v[118:119]
	v_cvt_pk_bf16_f32 v94, v94, v95
	v_cvt_pk_bf16_f32 v95, v96, v97
	v_cvt_pk_bf16_f32 v96, v104, v105
	v_cvt_pk_bf16_f32 v97, v106, v107
	v_lshl_add_u64 v[104:105], s[42:43], 0, v[108:109]
	v_lshlrev_b32_e32 v106, 1, v149
	v_mov_b32_e32 v107, v1
	v_lshl_add_u64 v[104:105], v[104:105], 0, v[106:107]
	global_store_dwordx4 v[104:105], v[94:97], off

; __device__ __forceinline__ u32x4 pack8(f32x4 a, f32x4 b) { u32x4 w; w.x = pk2(a[0], a[1]); w.y = pk2(a[2], a[3]); w.z = pk2(b[0], b[1]); w.w = pk2(b[2], b[3]); return w; }
; __device__ __forceinline__ float sq8(const f32x4& a, const f32x4& b) { return ((a[0] * a[0] + a[1] * a[1]) + (a[2] * a[2] + a[3] * a[3])) + ((b[0] * b[0] + b[1] * b[1]) + (b[2] * b[2] + b[3] * b[3])); }
;     __device__ __forceinline__ void operator()(const f32x4 (&acc)[2][2][4][2], const Unit& u, int ui, int wr, int wc, int fr, int fq, LAS unsigned char* lds) const {
;     ...
;                     else if (pn == 7) { *(u32x4*)(CQ + (size_t)row * 384 + c) = pack8(v0, v1); sq += sq8(v0, v1); }
;                     else if (bj == 0) { *(u32x4*)(CQ + (size_t)row * 384 + 256 + c) = pack8(v0, v1); sq += sq8(v0, v1); }
.LBB0_432:
	s_andn2_b64 vcc, exec, s[64:65]
	v_mov_b32_e32 v94, v110
	s_cbranch_vccnz .LBB0_434
	v_lshl_add_u64 v[102:103], s[40:41], 0, v[102:103]
	v_cvt_pk_bf16_f32 v94, v86, v87
	v_cvt_pk_bf16_f32 v95, v88, v89
	v_cvt_pk_bf16_f32 v96, v82, v83
	v_cvt_pk_bf16_f32 v97, v84, v85
	v_lshl_add_u64 v[102:103], v[102:103], 0, v[0:1]
	global_store_dwordx4 v[102:103], v[94:97], off offset:256
	v_mov_b32_e32 v102, v89
	v_mov_b32_e32 v103, v85
	v_mov_b32_e32 v96, v87
	v_mov_b32_e32 v97, v83
	v_mov_b32_e32 v94, v86
	v_mov_b32_e32 v95, v82
	v_pk_mul_f32 v[96:97], v[96:97], v[96:97]
	v_pk_mul_f32 v[102:103], v[102:103], v[102:103]
	v_pk_fma_f32 v[94:95], v[94:95], v[94:95], v[96:97]
	v_mov_b32_e32 v96, v88
	v_mov_b32_e32 v97, v84
	v_pk_fma_f32 v[96:97], v[96:97], v[96:97], v[102:103]
	s_nop 0
	v_pk_add_f32 v[94:95], v[94:95], v[96:97]
	s_nop 0
	v_add_f32_e32 v94, v94, v95
	v_add_f32_e32 v94, v94, v110

; __device__ __forceinline__ u32x4 pack8(f32x4 a, f32x4 b) { u32x4 w; w.x = pk2(a[0], a[1]); w.y = pk2(a[2], a[3]); w.z = pk2(b[0], b[1]); w.w = pk2(b[2], b[3]); return w; }
; __device__ __forceinline__ float sq8(const f32x4& a, const f32x4& b) { return ((a[0] * a[0] + a[1] * a[1]) + (a[2] * a[2] + a[3] * a[3])) + ((b[0] * b[0] + b[1] * b[1]) + (b[2] * b[2] + b[3] * b[3])); }
;     __device__ __forceinline__ void operator()(const f32x4 (&acc)[2][2][4][2], const Unit& u, int ui, int wr, int wc, int fr, int fq, LAS unsigned char* lds) const {
;     ...
;                     else if (pn == 6) { *(u32x4*)(CKV + (size_t)row * 256 + c) = pack8(v0, v1); sq += sq8(v0, v1); }
.LBB0_435:
	s_andn2_b64 vcc, exec, s[64:65]
	s_cbranch_vccnz .LBB0_437
	v_lshl_add_u64 v[100:101], s[38:39], 0, v[100:101]
	v_cvt_pk_bf16_f32 v94, v86, v87
	v_cvt_pk_bf16_f32 v95, v88, v89
	v_cvt_pk_bf16_f32 v96, v82, v83
	v_cvt_pk_bf16_f32 v97, v84, v85
	v_lshl_add_u64 v[100:101], v[100:101], 0, v[0:1]
	global_store_dwordx4 v[100:101], v[94:97], off offset:256
	v_mov_b32_e32 v100, v89
	v_mov_b32_e32 v101, v85
	v_mov_b32_e32 v96, v87
	v_mov_b32_e32 v97, v83
	v_mov_b32_e32 v94, v86
	v_mov_b32_e32 v95, v82
	v_pk_mul_f32 v[96:97], v[96:97], v[96:97]
	v_pk_mul_f32 v[100:101], v[100:101], v[100:101]
	v_pk_fma_f32 v[94:95], v[94:95], v[94:95], v[96:97]
	v_mov_b32_e32 v96, v88
	v_mov_b32_e32 v97, v84
	v_pk_fma_f32 v[96:97], v[96:97], v[96:97], v[100:101]
	s_nop 0
	v_pk_add_f32 v[94:95], v[94:95], v[96:97]
	s_nop 0
	v_add_f32_e32 v94, v94, v95
	v_add_f32_e32 v94, v94, v110

; __device__ __forceinline__ u32x4 pack8(f32x4 a, f32x4 b) { u32x4 w; w.x = pk2(a[0], a[1]); w.y = pk2(a[2], a[3]); w.z = pk2(b[0], b[1]); w.w = pk2(b[2], b[3]); return w; }
; __device__ __forceinline__ float fq_sum(float v) { v += xor16(v); v += xor32(v); return v; }
;     __device__ __forceinline__ void operator()(const f32x4 (&acc)[2][2][4][2], const Unit& u, int ui, int wr, int wc, int fr, int fq, LAS unsigned char* lds) const {
;     ...
;                     f32x4 v0 = acc[ai][bj][m][0] * rs, v1 = acc[ai][bj][m][1] * rs;
;                     if (pn < 6) { if (pn < 2) { v0 = v0 * QS_SB; v1 = v1 * QS_SB; } *(u32x4*)(QKV + (size_t)row * 1536 + pn * 256 + c) = pack8(v0, v1); }
;     ...
;                 if (pn >= 6) {
;                     sq = fq_sum(sq);
;                     if (fq == 0) { if (pn == 6) SQK[(size_t)row * 4 + wc] = sq; else SQQ[(size_t)row * 8 + (pn - 7) * 4 + wc] = sq; }
.LBB0_438:
	v_pk_mul_f32 v[94:95], v[88:89], s[96:97] op_sel_hi:[1,0]
	v_pk_mul_f32 v[96:97], v[86:87], s[96:97] op_sel_hi:[1,0]
	v_pk_mul_f32 v[100:101], v[84:85], s[96:97] op_sel_hi:[1,0]
	v_pk_mul_f32 v[102:103], v[82:83], s[96:97] op_sel_hi:[1,0]
	v_cndmask_b32_e64 v85, v85, v101, s[12:13]
	v_cndmask_b32_e64 v100, v84, v100, s[12:13]
	v_cndmask_b32_e64 v84, v83, v103, s[12:13]
	v_cndmask_b32_e64 v101, v82, v102, s[12:13]
	v_cndmask_b32_e64 v83, v89, v95, s[12:13]
	v_cndmask_b32_e64 v88, v88, v94, s[12:13]
	v_cndmask_b32_e64 v82, v87, v97, s[12:13]
	v_cndmask_b32_e64 v86, v86, v96, s[12:13]
	v_cvt_pk_bf16_f32 v82, v86, v82
	v_cvt_pk_bf16_f32 v83, v88, v83
	v_cvt_pk_bf16_f32 v84, v101, v84
	v_cvt_pk_bf16_f32 v85, v100, v85
	v_lshl_add_u64 v[86:87], v[90:91], 0, v[0:1]
	v_mov_b32_e32 v94, v110
	global_store_dwordx4 v[86:87], v[82:85], off offset:256
	s_and_b64 vcc, exec, s[20:21]
	s_cbranch_vccnz .LBB0_442
.LBB0_439:
	v_mov_b32_e32 v82, v94
	v_mov_b32_e32 v83, v94
	v_readlane_b32 s6, v255, 6
	s_nop 0
	v_permlane16_swap_b32_e32 v82, v83
	v_readlane_b32 s7, v255, 7
	s_nop 1
	v_cndmask_b32_e64 v82, v82, v83, s[6:7]
	v_add_f32_e32 v82, v94, v82
	v_mov_b32_e32 v83, v82
	v_mov_b32_e32 v84, v82
	s_nop 1
	v_permlane32_swap_b32_e32 v83, v84
	s_and_saveexec_b64 s[64:65], s[16:17]
	s_cbranch_execz .LBB0_441
	v_cndmask_b32_e64 v83, v83, v84, s[4:5]
	v_lshlrev_b64 v[84:85], 5, v[98:99]
	v_lshl_add_u64 v[84:85], s[48:49], 0, v[84:85]
	v_add_f32_e32 v86, v82, v83
	v_lshl_add_u64 v[82:83], s[50:51], 0, v[92:93]
	v_lshl_add_u64 v[84:85], s[88:89], 2, v[84:85]
	v_cndmask_b32_e64 v83, v85, v83, s[14:15]
	v_cndmask_b32_e64 v82, v84, v82, s[14:15]
	s_lshl_b32 s6, s91, 2
	s_mov_b32 s7, s89
	v_lshl_add_u64 v[82:83], v[82:83], 0, s[6:7]
	global_store_dword v[82:83], v86, off

; __device__ __forceinline__ u32x4 pack8(f32x4 a, f32x4 b) { u32x4 w; w.x = pk2(a[0], a[1]); w.y = pk2(a[2], a[3]); w.z = pk2(b[0], b[1]); w.w = pk2(b[2], b[3]); return w; }
; __device__ __forceinline__ float sq8(const f32x4& a, const f32x4& b) { return ((a[0] * a[0] + a[1] * a[1]) + (a[2] * a[2] + a[3] * a[3])) + ((b[0] * b[0] + b[1] * b[1]) + (b[2] * b[2] + b[3] * b[3])); }
; __device__ __forceinline__ f32x2 rtab_get(LAS unsigned char* lds, int ui, int r) { return ((const LAS f32x2*)(lds + RTAB_OFF))[(ui & 1) * 256 + r]; }
;     __device__ __forceinline__ void operator()(const f32x4 (&acc)[2][2][4][2], const Unit& u, int ui, int wr, int wc, int fr, int fq, LAS unsigned char* lds) const {
;     ...
;                 const int rr = ai * 128 + wr * 64 + m * 16 + fr, row = u.pm * 256 + rr; const float rs = rtab_get(lds, ui, rr)[0];
;                 float sq = 0.f;
; #pragma unroll
;                 for (int bj = 0; bj < 2; ++bj) {
;                     const int c = bj * 128 + wc * 32 + fq * 8;
;                     f32x4 v0 = acc[ai][bj][m][0] * rs, v1 = acc[ai][bj][m][1] * rs;
;                     if (pn < 6) { if (pn < 2) { v0 = v0 * QS_SB; v1 = v1 * QS_SB; } *(u32x4*)(QKV + (size_t)row * 1536 + pn * 256 + c) = pack8(v0, v1); }
;                     else if (pn == 6) { *(u32x4*)(CKV + (size_t)row * 256 + c) = pack8(v0, v1); sq += sq8(v0, v1); }
;                     else if (pn == 7) { *(u32x4*)(CQ + (size_t)row * 384 + c) = pack8(v0, v1); sq += sq8(v0, v1); }
;                     else if (bj == 0) { *(u32x4*)(CQ + (size_t)row * 384 + 256 + c) = pack8(v0, v1); sq += sq8(v0, v1); }
.LBB0_442:
	ds_read_b32 v88, v150 offset:384
	v_add3_u32 v82, s3, v151, 48
	v_ashrrev_i32_e32 v83, 31, v82
	v_mad_i64_i32 v[86:87], s[6:7], v82, s59, 0
	v_lshlrev_b64 v[84:85], 9, v[82:83]
	s_waitcnt lgkmcnt(0)
	v_pk_mul_f32 v[80:81], v[80:81], v[88:89] op_sel_hi:[1,0]
	v_pk_mul_f32 v[78:79], v[78:79], v[88:89] op_sel_hi:[1,0]
	v_pk_mul_f32 v[92:93], v[76:77], v[88:89] op_sel_hi:[1,0]
	v_pk_mul_f32 v[90:91], v[74:75], v[88:89] op_sel_hi:[1,0]
	s_and_b64 vcc, exec, s[18:19]
	s_mov_b64 s[64:65], -1
	s_cbranch_vccnz .LBB0_452
	v_cvt_pk_bf16_f32 v74, v78, v79
	v_cvt_pk_bf16_f32 v75, v80, v81
	v_cvt_pk_bf16_f32 v76, v90, v91
	v_cvt_pk_bf16_f32 v77, v92, v93
	s_cmp_lt_i32 s26, 7
	s_cbranch_scc1 .LBB0_449
	s_cmp_lg_u32 s26, 7
	s_cbranch_scc0 .LBB0_446
	v_lshl_add_u64 v[94:95], s[40:41], 0, v[86:87]
	v_lshl_add_u64 v[94:95], v[94:95], 0, v[0:1]
	v_mov_b32_e32 v96, v79
	v_mov_b32_e32 v97, v91
	global_store_dwordx4 v[94:95], v[74:77], off offset:512
	v_mov_b32_e32 v94, v78
	v_mov_b32_e32 v95, v90
	v_pk_mul_f32 v[96:97], v[96:97], v[96:97]
	v_mov_b32_e32 v98, v81
	v_mov_b32_e32 v99, v93
	v_pk_fma_f32 v[94:95], v[94:95], v[94:95], v[96:97]
	v_mov_b32_e32 v96, v80
	v_mov_b32_e32 v97, v92
	v_pk_mul_f32 v[98:99], v[98:99], v[98:99]
	s_mov_b64 s[64:65], 0
	v_pk_fma_f32 v[96:97], v[96:97], v[96:97], v[98:99]
	s_nop 0
	v_pk_add_f32 v[94:95], v[94:95], v[96:97]
	s_nop 0
	v_add_f32_e32 v94, v94, v95
.LBB0_446:
	s_andn2_b64 vcc, exec, s[64:65]
	s_cbranch_vccnz .LBB0_448
	v_lshl_add_u64 v[94:95], s[40:41], 0, v[86:87]
	v_lshl_add_u64 v[94:95], v[94:95], 0, v[0:1]
	v_mov_b32_e32 v96, v79
	v_mov_b32_e32 v97, v91
	global_store_dwordx4 v[94:95], v[74:77], off
	v_mov_b32_e32 v94, v78
	v_mov_b32_e32 v95, v90
	v_pk_mul_f32 v[96:97], v[96:97], v[96:97]
	v_mov_b32_e32 v98, v81
	v_mov_b32_e32 v99, v93
	v_pk_fma_f32 v[94:95], v[94:95], v[94:95], v[96:97]
	v_mov_b32_e32 v96, v80
	v_mov_b32_e32 v97, v92
	v_pk_mul_f32 v[98:99], v[98:99], v[98:99]
	s_nop 0
	v_pk_fma_f32 v[96:97], v[96:97], v[96:97], v[98:99]
	s_nop 0
	v_pk_add_f32 v[94:95], v[94:95], v[96:97]
	s_nop 0
	v_add_f32_e32 v94, v94, v95

; __device__ __forceinline__ u32x4 pack8(f32x4 a, f32x4 b) { u32x4 w; w.x = pk2(a[0], a[1]); w.y = pk2(a[2], a[3]); w.z = pk2(b[0], b[1]); w.w = pk2(b[2], b[3]); return w; }
; __device__ __forceinline__ float sq8(const f32x4& a, const f32x4& b) { return ((a[0] * a[0] + a[1] * a[1]) + (a[2] * a[2] + a[3] * a[3])) + ((b[0] * b[0] + b[1] * b[1]) + (b[2] * b[2] + b[3] * b[3])); }
;     __device__ __forceinline__ void operator()(const f32x4 (&acc)[2][2][4][2], const Unit& u, int ui, int wr, int wc, int fr, int fq, LAS unsigned char* lds) const {
;     ...
;                     else if (pn == 6) { *(u32x4*)(CKV + (size_t)row * 256 + c) = pack8(v0, v1); sq += sq8(v0, v1); }
.LBB0_449:
	s_andn2_b64 vcc, exec, s[64:65]
	s_cbranch_vccnz .LBB0_451
	v_lshl_add_u64 v[94:95], s[38:39], 0, v[84:85]
	v_lshl_add_u64 v[94:95], v[94:95], 0, v[0:1]
	global_store_dwordx4 v[94:95], v[74:77], off
	v_mov_b32_e32 v94, v81
	v_mov_b32_e32 v95, v93
	v_mov_b32_e32 v76, v79
	v_mov_b32_e32 v77, v91
	v_mov_b32_e32 v74, v78
	v_mov_b32_e32 v75, v90
	v_pk_mul_f32 v[76:77], v[76:77], v[76:77]
	v_pk_mul_f32 v[94:95], v[94:95], v[94:95]
	v_pk_fma_f32 v[74:75], v[74:75], v[74:75], v[76:77]
	v_mov_b32_e32 v76, v80
	v_mov_b32_e32 v77, v92
	v_pk_fma_f32 v[76:77], v[76:77], v[76:77], v[94:95]
	s_nop 0
	v_pk_add_f32 v[74:75], v[74:75], v[76:77]
	s_nop 0
	v_add_f32_e32 v94, v74, v75

; __device__ __forceinline__ u32x4 pack8(f32x4 a, f32x4 b) { u32x4 w; w.x = pk2(a[0], a[1]); w.y = pk2(a[2], a[3]); w.z = pk2(b[0], b[1]); w.w = pk2(b[2], b[3]); return w; }
;     __device__ __forceinline__ void operator()(const f32x4 (&acc)[2][2][4][2], const Unit& u, int ui, int wr, int wc, int fr, int fq, LAS unsigned char* lds) const {
;     ...
;                     f32x4 v0 = acc[ai][bj][m][0] * rs, v1 = acc[ai][bj][m][1] * rs;
;                     if (pn < 6) { if (pn < 2) { v0 = v0 * QS_SB; v1 = v1 * QS_SB; } *(u32x4*)(QKV + (size_t)row * 1536 + pn * 256 + c) = pack8(v0, v1); }
.LBB0_452:
	s_movk_i32 s3, 0xc00
	v_mad_i64_i32 v[74:75], s[6:7], v82, s3, 0
	v_lshl_add_u64 v[74:75], s[36:37], 0, v[74:75]
	s_and_b64 vcc, exec, s[64:65]
	v_lshl_add_u64 v[74:75], s[62:63], 1, v[74:75]
	s_cbranch_vccz .LBB0_454
	v_pk_mul_f32 v[76:77], v[80:81], s[96:97] op_sel_hi:[1,0]
	v_pk_mul_f32 v[94:95], v[78:79], s[96:97] op_sel_hi:[1,0]
	v_pk_mul_f32 v[96:97], v[92:93], s[96:97] op_sel_hi:[1,0]
	v_pk_mul_f32 v[98:99], v[90:91], s[96:97] op_sel_hi:[1,0]
	v_cndmask_b32_e64 v89, v93, v97, s[12:13]
	v_cndmask_b32_e64 v92, v92, v96, s[12:13]
	v_cndmask_b32_e64 v91, v91, v99, s[12:13]
	v_cndmask_b32_e64 v90, v90, v98, s[12:13]
	v_cndmask_b32_e64 v77, v81, v77, s[12:13]
	v_cndmask_b32_e64 v80, v80, v76, s[12:13]
	v_cndmask_b32_e64 v76, v79, v95, s[12:13]
	v_cndmask_b32_e64 v78, v78, v94, s[12:13]
	v_cvt_pk_bf16_f32 v76, v78, v76
	v_cvt_pk_bf16_f32 v77, v80, v77
	v_cvt_pk_bf16_f32 v78, v90, v91
	v_cvt_pk_bf16_f32 v79, v92, v89
	v_lshl_add_u64 v[80:81], v[74:75], 0, v[0:1]
	v_mov_b32_e32 v94, 0
	global_store_dwordx4 v[80:81], v[76:79], off

; __device__ __forceinline__ float xor32(float x) { auto rr = __builtin_amdgcn_permlane32_swap(__float_as_uint(x), __float_as_uint(x), false, false); return __uint_as_float(((unsigned)(threadIdx.x & 32)) ? rr[0] : rr[1]); }
; __device__ __forceinline__ u32x4 pack8(f32x4 a, f32x4 b) { u32x4 w; w.x = pk2(a[0], a[1]); w.y = pk2(a[2], a[3]); w.z = pk2(b[0], b[1]); w.w = pk2(b[2], b[3]); return w; }
;     __device__ __forceinline__ void operator()(const f32x4 (&acc)[2][2][4][2], const Unit& u, int ui, int wr, int wc, int fr, int fq, LAS unsigned char* lds) const {
;     ...
;                     else if (wc == 0) {
;                         const int ib = 8 * (fq & 1);
;                         const f32x4 c0 = *(const f32x4*)(COS + (size_t)row * 16 + ib), c1 = *(const f32x4*)(COS + (size_t)row * 16 + ib + 4);
;                         const f32x4 s0 = *(const f32x4*)(SIN + (size_t)row * 16 + ib), s1 = *(const f32x4*)(SIN + (size_t)row * 16 + ib + 4);
;                         f32x4 p0, p1;
; #pragma unroll
;                         for (int i = 0; i < 4; ++i) { p0[i] = xor32(v0[i]); p1[i] = xor32(v1[i]); }
;                         const float sg = (fq < 2) ? -1.f : 1.f;
;                         const f32x4 o0 = v0 * c0 + p0 * s0 * sg, o1 = v1 * c1 + p1 * s1 * sg;
;                         *(u32x4*)(KR + (size_t)row * 32 + fq * 8) = pack8(o0, o1);
.LBB0_457:
	s_cmp_lt_i32 s26, 7
	s_cbranch_scc1 .LBB0_465
	s_cmp_lg_u32 s26, 7
	s_cbranch_scc0 .LBB0_462
	s_andn2_b64 vcc, exec, s[56:57]
	s_cbranch_vccnz .LBB0_461
	v_lshlrev_b64 v[96:97], 2, v[76:77]
	v_lshl_add_u64 v[78:79], s[44:45], 0, v[96:97]
	v_lshlrev_b32_e32 v98, 2, v128
	v_mov_b32_e32 v99, v1
	v_lshl_add_u64 v[96:97], s[46:47], 0, v[96:97]
	v_lshl_add_u64 v[88:89], v[78:79], 0, v[98:99]
	v_lshl_add_u64 v[100:101], v[96:97], 0, v[98:99]
	s_waitcnt vmcnt(10)
	v_mov_b32_e32 v78, v174
	v_mov_b32_e32 v79, v175
	v_mov_b32_e32 v80, v176
	v_mov_b32_e32 v81, v177
	v_mov_b32_e32 v88, v178
	v_mov_b32_e32 v89, v179
	v_mov_b32_e32 v90, v180
	v_mov_b32_e32 v91, v181
	v_mov_b32_e32 v96, v182
	v_mov_b32_e32 v97, v183
	v_mov_b32_e32 v98, v184
	v_mov_b32_e32 v99, v185
	v_mov_b32_e32 v100, v230
	v_mov_b32_e32 v101, v231
	v_mov_b32_e32 v102, v232
	v_mov_b32_e32 v103, v233
	global_load_dwordx4 v[174:177], v[206:207], off offset:1024
	global_load_dwordx4 v[178:181], v[206:207], off offset:1040
	global_load_dwordx4 v[182:185], v[208:209], off offset:1024
	global_load_dwordx4 v[230:233], v[208:209], off offset:1040
	v_mov_b32_e32 v95, v70
	v_mov_b32_e32 v104, v70
	s_nop 1
	v_permlane32_swap_b32_e32 v95, v104
	v_cndmask_b32_e64 v104, v95, v104, s[4:5]
	v_mov_b32_e32 v95, v66
	v_mov_b32_e32 v105, v66
	s_nop 1
	v_permlane32_swap_b32_e32 v95, v105
	v_cndmask_b32_e64 v106, v95, v105, s[4:5]
	v_mov_b32_e32 v95, v71
	v_mov_b32_e32 v105, v71
	s_nop 1
	v_permlane32_swap_b32_e32 v95, v105
	v_cndmask_b32_e64 v105, v95, v105, s[4:5]
	v_mov_b32_e32 v95, v67
	v_mov_b32_e32 v107, v67
	s_nop 1
	v_permlane32_swap_b32_e32 v95, v107
	v_cndmask_b32_e64 v107, v95, v107, s[4:5]
	v_mov_b32_e32 v95, v72
	v_mov_b32_e32 v108, v72
	s_nop 1
	v_permlane32_swap_b32_e32 v95, v108
	v_cndmask_b32_e64 v108, v95, v108, s[4:5]
	v_mov_b32_e32 v95, v68
	v_mov_b32_e32 v109, v68
	s_nop 1
	v_permlane32_swap_b32_e32 v95, v109
	v_cndmask_b32_e64 v110, v95, v109, s[4:5]
	v_mov_b32_e32 v95, v73
	v_mov_b32_e32 v109, v73
	s_nop 1
	v_permlane32_swap_b32_e32 v95, v109
	v_cndmask_b32_e64 v109, v95, v109, s[4:5]
	v_mov_b32_e32 v95, v69
	v_mov_b32_e32 v111, v69
	s_nop 1
	v_permlane32_swap_b32_e32 v95, v111
	v_cndmask_b32_e64 v111, v95, v111, s[4:5]
	v_lshlrev_b64 v[92:93], 6, v[82:83]
	s_waitcnt lgkmcnt(0)
	v_pk_mul_f32 v[98:99], v[98:99], v[108:109]
	v_pk_mul_f32 v[96:97], v[96:97], v[104:105]
	v_mov_b32_e32 v104, v114
	v_mov_b32_e32 v105, v114
	v_pk_mul_f32 v[96:97], v[114:115], v[96:97]
	v_pk_mul_f32 v[98:99], v[104:105], v[98:99]
	v_pk_fma_f32 v[78:79], v[70:71], v[78:79], v[96:97]
	v_pk_fma_f32 v[80:81], v[72:73], v[80:81], v[98:99]
	v_pk_mul_f32 v[96:97], v[102:103], v[110:111]
	v_pk_mul_f32 v[98:99], v[100:101], v[106:107]
	v_pk_mul_f32 v[96:97], v[104:105], v[96:97]
	v_pk_mul_f32 v[98:99], v[114:115], v[98:99]
	v_pk_fma_f32 v[90:91], v[68:69], v[90:91], v[96:97]
	v_pk_fma_f32 v[88:89], v[66:67], v[88:89], v[98:99]
	v_cvt_pk_bf16_f32 v78, v78, v79
	v_cvt_pk_bf16_f32 v79, v80, v81
	v_cvt_pk_bf16_f32 v80, v88, v89
	v_cvt_pk_bf16_f32 v81, v90, v91
	v_lshl_add_u64 v[88:89], s[42:43], 0, v[92:93]
	v_lshlrev_b32_e32 v90, 1, v149
	v_mov_b32_e32 v91, v1
	v_lshl_add_u64 v[88:89], v[88:89], 0, v[90:91]
	global_store_dwordx4 v[88:89], v[78:81], off

; __device__ __forceinline__ u32x4 pack8(f32x4 a, f32x4 b) { u32x4 w; w.x = pk2(a[0], a[1]); w.y = pk2(a[2], a[3]); w.z = pk2(b[0], b[1]); w.w = pk2(b[2], b[3]); return w; }
; __device__ __forceinline__ float sq8(const f32x4& a, const f32x4& b) { return ((a[0] * a[0] + a[1] * a[1]) + (a[2] * a[2] + a[3] * a[3])) + ((b[0] * b[0] + b[1] * b[1]) + (b[2] * b[2] + b[3] * b[3])); }
;     __device__ __forceinline__ void operator()(const f32x4 (&acc)[2][2][4][2], const Unit& u, int ui, int wr, int wc, int fr, int fq, LAS unsigned char* lds) const {
;     ...
;                     else if (pn == 7) { *(u32x4*)(CQ + (size_t)row * 384 + c) = pack8(v0, v1); sq += sq8(v0, v1); }
;                     else if (bj == 0) { *(u32x4*)(CQ + (size_t)row * 384 + 256 + c) = pack8(v0, v1); sq += sq8(v0, v1); }
.LBB0_462:
	s_andn2_b64 vcc, exec, s[64:65]
	v_mov_b32_e32 v78, v94
	s_cbranch_vccnz .LBB0_464
	v_lshl_add_u64 v[86:87], s[40:41], 0, v[86:87]
	v_cvt_pk_bf16_f32 v78, v70, v71
	v_cvt_pk_bf16_f32 v79, v72, v73
	v_cvt_pk_bf16_f32 v80, v66, v67
	v_cvt_pk_bf16_f32 v81, v68, v69
	v_lshl_add_u64 v[86:87], v[86:87], 0, v[0:1]
	global_store_dwordx4 v[86:87], v[78:81], off offset:256
	v_mov_b32_e32 v86, v73
	v_mov_b32_e32 v87, v69
	v_mov_b32_e32 v80, v71
	v_mov_b32_e32 v81, v67
	v_mov_b32_e32 v78, v70
	v_mov_b32_e32 v79, v66
	v_pk_mul_f32 v[80:81], v[80:81], v[80:81]
	v_pk_mul_f32 v[86:87], v[86:87], v[86:87]
	v_pk_fma_f32 v[78:79], v[78:79], v[78:79], v[80:81]
	v_mov_b32_e32 v80, v72
	v_mov_b32_e32 v81, v68
	v_pk_fma_f32 v[80:81], v[80:81], v[80:81], v[86:87]
	s_nop 0
	v_pk_add_f32 v[78:79], v[78:79], v[80:81]
	s_nop 0
	v_add_f32_e32 v78, v78, v79
	v_add_f32_e32 v78, v78, v94

; __device__ __forceinline__ u32x4 pack8(f32x4 a, f32x4 b) { u32x4 w; w.x = pk2(a[0], a[1]); w.y = pk2(a[2], a[3]); w.z = pk2(b[0], b[1]); w.w = pk2(b[2], b[3]); return w; }
; __device__ __forceinline__ float sq8(const f32x4& a, const f32x4& b) { return ((a[0] * a[0] + a[1] * a[1]) + (a[2] * a[2] + a[3] * a[3])) + ((b[0] * b[0] + b[1] * b[1]) + (b[2] * b[2] + b[3] * b[3])); }
;     __device__ __forceinline__ void operator()(const f32x4 (&acc)[2][2][4][2], const Unit& u, int ui, int wr, int wc, int fr, int fq, LAS unsigned char* lds) const {
;     ...
;                     else if (pn == 6) { *(u32x4*)(CKV + (size_t)row * 256 + c) = pack8(v0, v1); sq += sq8(v0, v1); }
.LBB0_465:
	s_andn2_b64 vcc, exec, s[64:65]
	s_cbranch_vccnz .LBB0_467
	v_lshl_add_u64 v[84:85], s[38:39], 0, v[84:85]
	v_cvt_pk_bf16_f32 v78, v70, v71
	v_cvt_pk_bf16_f32 v79, v72, v73
	v_cvt_pk_bf16_f32 v80, v66, v67
	v_cvt_pk_bf16_f32 v81, v68, v69
	v_lshl_add_u64 v[84:85], v[84:85], 0, v[0:1]
	global_store_dwordx4 v[84:85], v[78:81], off offset:256
	v_mov_b32_e32 v84, v73
	v_mov_b32_e32 v85, v69
	v_mov_b32_e32 v80, v71
	v_mov_b32_e32 v81, v67
	v_mov_b32_e32 v78, v70
	v_mov_b32_e32 v79, v66
	v_pk_mul_f32 v[80:81], v[80:81], v[80:81]
	v_pk_mul_f32 v[84:85], v[84:85], v[84:85]
	v_pk_fma_f32 v[78:79], v[78:79], v[78:79], v[80:81]
	v_mov_b32_e32 v80, v72
	v_mov_b32_e32 v81, v68
	v_pk_fma_f32 v[80:81], v[80:81], v[80:81], v[84:85]
	s_nop 0
	v_pk_add_f32 v[78:79], v[78:79], v[80:81]
	s_nop 0
	v_add_f32_e32 v78, v78, v79
	v_add_f32_e32 v78, v78, v94

; __device__ __forceinline__ u32x4 pack8(f32x4 a, f32x4 b) { u32x4 w; w.x = pk2(a[0], a[1]); w.y = pk2(a[2], a[3]); w.z = pk2(b[0], b[1]); w.w = pk2(b[2], b[3]); return w; }
; __device__ __forceinline__ float fq_sum(float v) { v += xor16(v); v += xor32(v); return v; }
;     __device__ __forceinline__ void operator()(const f32x4 (&acc)[2][2][4][2], const Unit& u, int ui, int wr, int wc, int fr, int fq, LAS unsigned char* lds) const {
;     ...
;                     f32x4 v0 = acc[ai][bj][m][0] * rs, v1 = acc[ai][bj][m][1] * rs;
;                     if (pn < 6) { if (pn < 2) { v0 = v0 * QS_SB; v1 = v1 * QS_SB; } *(u32x4*)(QKV + (size_t)row * 1536 + pn * 256 + c) = pack8(v0, v1); }
;     ...
;                 if (pn >= 6) {
;                     sq = fq_sum(sq);
;                     if (fq == 0) { if (pn == 6) SQK[(size_t)row * 4 + wc] = sq; else SQQ[(size_t)row * 8 + (pn - 7) * 4 + wc] = sq; }
.LBB0_468:
	v_pk_mul_f32 v[78:79], v[72:73], s[96:97] op_sel_hi:[1,0]
	v_pk_mul_f32 v[80:81], v[70:71], s[96:97] op_sel_hi:[1,0]
	v_pk_mul_f32 v[84:85], v[68:69], s[96:97] op_sel_hi:[1,0]
	v_pk_mul_f32 v[86:87], v[66:67], s[96:97] op_sel_hi:[1,0]
	v_cndmask_b32_e64 v69, v69, v85, s[12:13]
	v_cndmask_b32_e64 v84, v68, v84, s[12:13]
	v_cndmask_b32_e64 v68, v67, v87, s[12:13]
	v_cndmask_b32_e64 v85, v66, v86, s[12:13]
	v_cndmask_b32_e64 v67, v73, v79, s[12:13]
	v_cndmask_b32_e64 v72, v72, v78, s[12:13]
	v_cndmask_b32_e64 v66, v71, v81, s[12:13]
	v_cndmask_b32_e64 v70, v70, v80, s[12:13]
	v_cvt_pk_bf16_f32 v66, v70, v66
	v_cvt_pk_bf16_f32 v67, v72, v67
	v_cvt_pk_bf16_f32 v68, v85, v68
	v_cvt_pk_bf16_f32 v69, v84, v69
	v_lshl_add_u64 v[70:71], v[74:75], 0, v[0:1]
	v_mov_b32_e32 v78, v94
	global_store_dwordx4 v[70:71], v[66:69], off offset:256
	s_and_b64 vcc, exec, s[20:21]
	s_cbranch_vccnz .LBB0_472
.LBB0_469:
	v_mov_b32_e32 v66, v78
	v_mov_b32_e32 v67, v78
	v_readlane_b32 s6, v255, 6
	s_nop 0
	v_permlane16_swap_b32_e32 v66, v67
	v_readlane_b32 s7, v255, 7
	s_nop 1
	v_cndmask_b32_e64 v66, v66, v67, s[6:7]
	v_add_f32_e32 v66, v78, v66
	v_mov_b32_e32 v67, v66
	v_mov_b32_e32 v68, v66
	s_nop 1
	v_permlane32_swap_b32_e32 v67, v68
	s_and_saveexec_b64 s[64:65], s[16:17]
	s_cbranch_execz .LBB0_471
	v_cndmask_b32_e64 v67, v67, v68, s[4:5]
	v_lshlrev_b64 v[68:69], 5, v[82:83]
	v_lshl_add_u64 v[68:69], s[48:49], 0, v[68:69]
	v_add_f32_e32 v70, v66, v67
	v_lshl_add_u64 v[66:67], s[50:51], 0, v[76:77]
	v_lshl_add_u64 v[68:69], s[88:89], 2, v[68:69]
	v_cndmask_b32_e64 v67, v69, v67, s[14:15]
	v_cndmask_b32_e64 v66, v68, v66, s[14:15]
	s_lshl_b32 s6, s91, 2
	s_mov_b32 s7, s89
	v_lshl_add_u64 v[66:67], v[66:67], 0, s[6:7]
	global_store_dword v[66:67], v70, off

; __device__ __forceinline__ u32x4 pack8(f32x4 a, f32x4 b) { u32x4 w; w.x = pk2(a[0], a[1]); w.y = pk2(a[2], a[3]); w.z = pk2(b[0], b[1]); w.w = pk2(b[2], b[3]); return w; }
; __device__ __forceinline__ float sq8(const f32x4& a, const f32x4& b) { return ((a[0] * a[0] + a[1] * a[1]) + (a[2] * a[2] + a[3] * a[3])) + ((b[0] * b[0] + b[1] * b[1]) + (b[2] * b[2] + b[3] * b[3])); }
; __device__ __forceinline__ f32x2 rtab_get(LAS unsigned char* lds, int ui, int r) { return ((const LAS f32x2*)(lds + RTAB_OFF))[(ui & 1) * 256 + r]; }
;     __device__ __forceinline__ void operator()(const f32x4 (&acc)[2][2][4][2], const Unit& u, int ui, int wr, int wc, int fr, int fq, LAS unsigned char* lds) const {
;     ...
;                 const int rr = ai * 128 + wr * 64 + m * 16 + fr, row = u.pm * 256 + rr; const float rs = rtab_get(lds, ui, rr)[0];
;                 float sq = 0.f;
; #pragma unroll
;                 for (int bj = 0; bj < 2; ++bj) {
;                     const int c = bj * 128 + wc * 32 + fq * 8;
;                     f32x4 v0 = acc[ai][bj][m][0] * rs, v1 = acc[ai][bj][m][1] * rs;
;                     if (pn < 6) { if (pn < 2) { v0 = v0 * QS_SB; v1 = v1 * QS_SB; } *(u32x4*)(QKV + (size_t)row * 1536 + pn * 256 + c) = pack8(v0, v1); }
;                     else if (pn == 6) { *(u32x4*)(CKV + (size_t)row * 256 + c) = pack8(v0, v1); sq += sq8(v0, v1); }
;                     else if (pn == 7) { *(u32x4*)(CQ + (size_t)row * 384 + c) = pack8(v0, v1); sq += sq8(v0, v1); }
;                     else if (bj == 0) { *(u32x4*)(CQ + (size_t)row * 384 + 256 + c) = pack8(v0, v1); sq += sq8(v0, v1); }
.LBB0_472:
	ds_read_b32 v72, v150 offset:1024
	v_add_u32_e32 v66, 0x80, v138
	v_ashrrev_i32_e32 v67, 31, v66
	v_mad_i64_i32 v[70:71], s[6:7], v66, s59, 0
	v_lshlrev_b64 v[68:69], 9, v[66:67]
	s_waitcnt lgkmcnt(0)
	v_pk_mul_f32 v[64:65], v[64:65], v[72:73] op_sel_hi:[1,0]
	v_pk_mul_f32 v[62:63], v[62:63], v[72:73] op_sel_hi:[1,0]
	v_pk_mul_f32 v[76:77], v[60:61], v[72:73] op_sel_hi:[1,0]
	v_pk_mul_f32 v[74:75], v[58:59], v[72:73] op_sel_hi:[1,0]
	s_and_b64 vcc, exec, s[18:19]
	s_mov_b64 s[64:65], -1
	s_cbranch_vccnz .LBB0_482
	v_cvt_pk_bf16_f32 v58, v62, v63
	v_cvt_pk_bf16_f32 v59, v64, v65
	v_cvt_pk_bf16_f32 v60, v74, v75
	v_cvt_pk_bf16_f32 v61, v76, v77
	s_cmp_lt_i32 s26, 7
	s_cbranch_scc1 .LBB0_479
	s_cmp_lg_u32 s26, 7
	s_cbranch_scc0 .LBB0_476
	v_lshl_add_u64 v[78:79], s[40:41], 0, v[70:71]
	v_lshl_add_u64 v[78:79], v[78:79], 0, v[0:1]
	v_mov_b32_e32 v80, v63
	v_mov_b32_e32 v81, v75
	global_store_dwordx4 v[78:79], v[58:61], off offset:512
	v_mov_b32_e32 v78, v62
	v_mov_b32_e32 v79, v74
	v_pk_mul_f32 v[80:81], v[80:81], v[80:81]
	v_mov_b32_e32 v82, v65
	v_mov_b32_e32 v83, v77
	v_pk_fma_f32 v[78:79], v[78:79], v[78:79], v[80:81]
	v_mov_b32_e32 v80, v64
	v_mov_b32_e32 v81, v76
	v_pk_mul_f32 v[82:83], v[82:83], v[82:83]
	s_mov_b64 s[64:65], 0
	v_pk_fma_f32 v[80:81], v[80:81], v[80:81], v[82:83]
	s_nop 0
	v_pk_add_f32 v[78:79], v[78:79], v[80:81]
	s_nop 0
	v_add_f32_e32 v78, v78, v79
.LBB0_476:
	s_andn2_b64 vcc, exec, s[64:65]
	s_cbranch_vccnz .LBB0_478
	v_lshl_add_u64 v[78:79], s[40:41], 0, v[70:71]
	v_lshl_add_u64 v[78:79], v[78:79], 0, v[0:1]
	v_mov_b32_e32 v80, v63
	v_mov_b32_e32 v81, v75
	global_store_dwordx4 v[78:79], v[58:61], off
	v_mov_b32_e32 v78, v62
	v_mov_b32_e32 v79, v74
	v_pk_mul_f32 v[80:81], v[80:81], v[80:81]
	v_mov_b32_e32 v82, v65
	v_mov_b32_e32 v83, v77
	v_pk_fma_f32 v[78:79], v[78:79], v[78:79], v[80:81]
	v_mov_b32_e32 v80, v64
	v_mov_b32_e32 v81, v76
	v_pk_mul_f32 v[82:83], v[82:83], v[82:83]
	s_nop 0
	v_pk_fma_f32 v[80:81], v[80:81], v[80:81], v[82:83]
	s_nop 0
	v_pk_add_f32 v[78:79], v[78:79], v[80:81]
	s_nop 0
	v_add_f32_e32 v78, v78, v79

; __device__ __forceinline__ u32x4 pack8(f32x4 a, f32x4 b) { u32x4 w; w.x = pk2(a[0], a[1]); w.y = pk2(a[2], a[3]); w.z = pk2(b[0], b[1]); w.w = pk2(b[2], b[3]); return w; }
; __device__ __forceinline__ float sq8(const f32x4& a, const f32x4& b) { return ((a[0] * a[0] + a[1] * a[1]) + (a[2] * a[2] + a[3] * a[3])) + ((b[0] * b[0] + b[1] * b[1]) + (b[2] * b[2] + b[3] * b[3])); }
;     __device__ __forceinline__ void operator()(const f32x4 (&acc)[2][2][4][2], const Unit& u, int ui, int wr, int wc, int fr, int fq, LAS unsigned char* lds) const {
;     ...
;                     else if (pn == 6) { *(u32x4*)(CKV + (size_t)row * 256 + c) = pack8(v0, v1); sq += sq8(v0, v1); }
.LBB0_479:
	s_andn2_b64 vcc, exec, s[64:65]
	s_cbranch_vccnz .LBB0_481
	v_lshl_add_u64 v[78:79], s[38:39], 0, v[68:69]
	v_lshl_add_u64 v[78:79], v[78:79], 0, v[0:1]
	global_store_dwordx4 v[78:79], v[58:61], off
	v_mov_b32_e32 v78, v65
	v_mov_b32_e32 v79, v77
	v_mov_b32_e32 v60, v63
	v_mov_b32_e32 v61, v75
	v_mov_b32_e32 v58, v62
	v_mov_b32_e32 v59, v74
	v_pk_mul_f32 v[60:61], v[60:61], v[60:61]
	v_pk_mul_f32 v[78:79], v[78:79], v[78:79]
	v_pk_fma_f32 v[58:59], v[58:59], v[58:59], v[60:61]
	v_mov_b32_e32 v60, v64
	v_mov_b32_e32 v61, v76
	v_pk_fma_f32 v[60:61], v[60:61], v[60:61], v[78:79]
	s_nop 0
	v_pk_add_f32 v[58:59], v[58:59], v[60:61]
	s_nop 0
	v_add_f32_e32 v78, v58, v59

; __device__ __forceinline__ u32x4 pack8(f32x4 a, f32x4 b) { u32x4 w; w.x = pk2(a[0], a[1]); w.y = pk2(a[2], a[3]); w.z = pk2(b[0], b[1]); w.w = pk2(b[2], b[3]); return w; }
;     __device__ __forceinline__ void operator()(const f32x4 (&acc)[2][2][4][2], const Unit& u, int ui, int wr, int wc, int fr, int fq, LAS unsigned char* lds) const {
;     ...
;                     f32x4 v0 = acc[ai][bj][m][0] * rs, v1 = acc[ai][bj][m][1] * rs;
;                     if (pn < 6) { if (pn < 2) { v0 = v0 * QS_SB; v1 = v1 * QS_SB; } *(u32x4*)(QKV + (size_t)row * 1536 + pn * 256 + c) = pack8(v0, v1); }
.LBB0_482:
	v_mad_i64_i32 v[58:59], s[6:7], v66, s3, 0
	v_lshl_add_u64 v[58:59], s[36:37], 0, v[58:59]
	s_and_b64 vcc, exec, s[64:65]
	v_lshl_add_u64 v[58:59], s[62:63], 1, v[58:59]
	s_cbranch_vccz .LBB0_484
	v_pk_mul_f32 v[60:61], v[64:65], s[96:97] op_sel_hi:[1,0]
	v_pk_mul_f32 v[78:79], v[62:63], s[96:97] op_sel_hi:[1,0]
	v_pk_mul_f32 v[80:81], v[76:77], s[96:97] op_sel_hi:[1,0]
	v_pk_mul_f32 v[82:83], v[74:75], s[96:97] op_sel_hi:[1,0]
	v_cndmask_b32_e64 v73, v77, v81, s[12:13]
	v_cndmask_b32_e64 v76, v76, v80, s[12:13]
	v_cndmask_b32_e64 v75, v75, v83, s[12:13]
	v_cndmask_b32_e64 v74, v74, v82, s[12:13]
	v_cndmask_b32_e64 v61, v65, v61, s[12:13]
	v_cndmask_b32_e64 v64, v64, v60, s[12:13]
	v_cndmask_b32_e64 v60, v63, v79, s[12:13]
	v_cndmask_b32_e64 v62, v62, v78, s[12:13]
	v_cvt_pk_bf16_f32 v60, v62, v60
	v_cvt_pk_bf16_f32 v61, v64, v61
	v_cvt_pk_bf16_f32 v62, v74, v75
	v_cvt_pk_bf16_f32 v63, v76, v73
	v_lshl_add_u64 v[64:65], v[58:59], 0, v[0:1]
	v_mov_b32_e32 v78, 0
	global_store_dwordx4 v[64:65], v[60:63], off

; __device__ __forceinline__ float xor32(float x) { auto rr = __builtin_amdgcn_permlane32_swap(__float_as_uint(x), __float_as_uint(x), false, false); return __uint_as_float(((unsigned)(threadIdx.x & 32)) ? rr[0] : rr[1]); }
; __device__ __forceinline__ u32x4 pack8(f32x4 a, f32x4 b) { u32x4 w; w.x = pk2(a[0], a[1]); w.y = pk2(a[2], a[3]); w.z = pk2(b[0], b[1]); w.w = pk2(b[2], b[3]); return w; }
;     __device__ __forceinline__ void operator()(const f32x4 (&acc)[2][2][4][2], const Unit& u, int ui, int wr, int wc, int fr, int fq, LAS unsigned char* lds) const {
;     ...
;                     else if (wc == 0) {
;                         const int ib = 8 * (fq & 1);
;                         const f32x4 c0 = *(const f32x4*)(COS + (size_t)row * 16 + ib), c1 = *(const f32x4*)(COS + (size_t)row * 16 + ib + 4);
;                         const f32x4 s0 = *(const f32x4*)(SIN + (size_t)row * 16 + ib), s1 = *(const f32x4*)(SIN + (size_t)row * 16 + ib + 4);
;                         f32x4 p0, p1;
; #pragma unroll
;                         for (int i = 0; i < 4; ++i) { p0[i] = xor32(v0[i]); p1[i] = xor32(v1[i]); }
;                         const float sg = (fq < 2) ? -1.f : 1.f;
;                         const f32x4 o0 = v0 * c0 + p0 * s0 * sg, o1 = v1 * c1 + p1 * s1 * sg;
;                         *(u32x4*)(KR + (size_t)row * 32 + fq * 8) = pack8(o0, o1);
.LBB0_487:
	s_cmp_lt_i32 s26, 7
	s_cbranch_scc1 .LBB0_495
	s_cmp_lg_u32 s26, 7
	s_cbranch_scc0 .LBB0_492
	s_andn2_b64 vcc, exec, s[56:57]
	s_cbranch_vccnz .LBB0_491
	v_lshlrev_b64 v[80:81], 2, v[60:61]
	v_lshl_add_u64 v[62:63], s[44:45], 0, v[80:81]
	v_lshlrev_b32_e32 v82, 2, v128
	v_mov_b32_e32 v83, v1
	v_lshl_add_u64 v[80:81], s[46:47], 0, v[80:81]
	v_lshl_add_u64 v[72:73], v[62:63], 0, v[82:83]
	v_lshl_add_u64 v[84:85], v[80:81], 0, v[82:83]
	s_waitcnt vmcnt(10)
	v_mov_b32_e32 v62, v214
	v_mov_b32_e32 v63, v215
	v_mov_b32_e32 v64, v216
	v_mov_b32_e32 v65, v217
	v_mov_b32_e32 v72, v218
	v_mov_b32_e32 v73, v219
	v_mov_b32_e32 v74, v220
	v_mov_b32_e32 v75, v221
	v_mov_b32_e32 v80, v222
	v_mov_b32_e32 v81, v223
	v_mov_b32_e32 v82, v224
	v_mov_b32_e32 v83, v225
	v_mov_b32_e32 v84, v226
	v_mov_b32_e32 v85, v227
	v_mov_b32_e32 v86, v228
	v_mov_b32_e32 v87, v229
	global_load_dwordx4 v[214:217], v[206:207], off offset:2048
	global_load_dwordx4 v[218:221], v[206:207], off offset:2064
	global_load_dwordx4 v[222:225], v[208:209], off offset:2048
	global_load_dwordx4 v[226:229], v[208:209], off offset:2064
	v_mov_b32_e32 v79, v54
	v_mov_b32_e32 v88, v54
	s_nop 1
	v_permlane32_swap_b32_e32 v79, v88
	v_cndmask_b32_e64 v88, v79, v88, s[4:5]
	v_mov_b32_e32 v79, v50
	v_mov_b32_e32 v89, v50
	s_nop 1
	v_permlane32_swap_b32_e32 v79, v89
	v_cndmask_b32_e64 v90, v79, v89, s[4:5]
	v_mov_b32_e32 v79, v55
	v_mov_b32_e32 v89, v55
	s_nop 1
	v_permlane32_swap_b32_e32 v79, v89
	v_cndmask_b32_e64 v89, v79, v89, s[4:5]
	v_mov_b32_e32 v79, v51
	v_mov_b32_e32 v91, v51
	s_nop 1
	v_permlane32_swap_b32_e32 v79, v91
	v_cndmask_b32_e64 v91, v79, v91, s[4:5]
	v_mov_b32_e32 v79, v56
	v_mov_b32_e32 v92, v56
	s_nop 1
	v_permlane32_swap_b32_e32 v79, v92
	v_cndmask_b32_e64 v92, v79, v92, s[4:5]
	v_mov_b32_e32 v79, v52
	v_mov_b32_e32 v93, v52
	s_nop 1
	v_permlane32_swap_b32_e32 v79, v93
	v_cndmask_b32_e64 v94, v79, v93, s[4:5]
	v_mov_b32_e32 v79, v57
	v_mov_b32_e32 v93, v57
	s_nop 1
	v_permlane32_swap_b32_e32 v79, v93
	v_cndmask_b32_e64 v93, v79, v93, s[4:5]
	v_mov_b32_e32 v79, v53
	v_mov_b32_e32 v95, v53
	s_nop 1
	v_permlane32_swap_b32_e32 v79, v95
	v_cndmask_b32_e64 v95, v79, v95, s[4:5]
	v_lshlrev_b64 v[76:77], 6, v[66:67]
	s_waitcnt lgkmcnt(0)
	v_pk_mul_f32 v[82:83], v[82:83], v[92:93]
	v_pk_mul_f32 v[80:81], v[80:81], v[88:89]
	v_mov_b32_e32 v88, v114
	v_mov_b32_e32 v89, v114
	v_pk_mul_f32 v[80:81], v[114:115], v[80:81]
	v_pk_mul_f32 v[82:83], v[88:89], v[82:83]
	v_pk_fma_f32 v[62:63], v[54:55], v[62:63], v[80:81]
	v_pk_fma_f32 v[64:65], v[56:57], v[64:65], v[82:83]
	v_pk_mul_f32 v[80:81], v[86:87], v[94:95]
	v_pk_mul_f32 v[82:83], v[84:85], v[90:91]
	v_pk_mul_f32 v[80:81], v[88:89], v[80:81]
	v_pk_mul_f32 v[82:83], v[114:115], v[82:83]
	v_pk_fma_f32 v[74:75], v[52:53], v[74:75], v[80:81]
	v_pk_fma_f32 v[72:73], v[50:51], v[72:73], v[82:83]
	v_cvt_pk_bf16_f32 v62, v62, v63
	v_cvt_pk_bf16_f32 v63, v64, v65
	v_cvt_pk_bf16_f32 v64, v72, v73
	v_cvt_pk_bf16_f32 v65, v74, v75
	v_lshl_add_u64 v[72:73], s[42:43], 0, v[76:77]
	v_lshlrev_b32_e32 v74, 1, v149
	v_mov_b32_e32 v75, v1
	v_lshl_add_u64 v[72:73], v[72:73], 0, v[74:75]
	global_store_dwordx4 v[72:73], v[62:65], off

; __device__ __forceinline__ u32x4 pack8(f32x4 a, f32x4 b) { u32x4 w; w.x = pk2(a[0], a[1]); w.y = pk2(a[2], a[3]); w.z = pk2(b[0], b[1]); w.w = pk2(b[2], b[3]); return w; }
; __device__ __forceinline__ float sq8(const f32x4& a, const f32x4& b) { return ((a[0] * a[0] + a[1] * a[1]) + (a[2] * a[2] + a[3] * a[3])) + ((b[0] * b[0] + b[1] * b[1]) + (b[2] * b[2] + b[3] * b[3])); }
;     __device__ __forceinline__ void operator()(const f32x4 (&acc)[2][2][4][2], const Unit& u, int ui, int wr, int wc, int fr, int fq, LAS unsigned char* lds) const {
;     ...
;                     else if (pn == 7) { *(u32x4*)(CQ + (size_t)row * 384 + c) = pack8(v0, v1); sq += sq8(v0, v1); }
;                     else if (bj == 0) { *(u32x4*)(CQ + (size_t)row * 384 + 256 + c) = pack8(v0, v1); sq += sq8(v0, v1); }
.LBB0_492:
	s_andn2_b64 vcc, exec, s[64:65]
	v_mov_b32_e32 v62, v78
	s_cbranch_vccnz .LBB0_494
	v_lshl_add_u64 v[70:71], s[40:41], 0, v[70:71]
	v_cvt_pk_bf16_f32 v62, v54, v55
	v_cvt_pk_bf16_f32 v63, v56, v57
	v_cvt_pk_bf16_f32 v64, v50, v51
	v_cvt_pk_bf16_f32 v65, v52, v53
	v_lshl_add_u64 v[70:71], v[70:71], 0, v[0:1]
	global_store_dwordx4 v[70:71], v[62:65], off offset:256
	v_mov_b32_e32 v70, v57
	v_mov_b32_e32 v71, v53
	v_mov_b32_e32 v64, v55
	v_mov_b32_e32 v65, v51
	v_mov_b32_e32 v62, v54
	v_mov_b32_e32 v63, v50
	v_pk_mul_f32 v[64:65], v[64:65], v[64:65]
	v_pk_mul_f32 v[70:71], v[70:71], v[70:71]
	v_pk_fma_f32 v[62:63], v[62:63], v[62:63], v[64:65]
	v_mov_b32_e32 v64, v56
	v_mov_b32_e32 v65, v52
	v_pk_fma_f32 v[64:65], v[64:65], v[64:65], v[70:71]
	s_nop 0
	v_pk_add_f32 v[62:63], v[62:63], v[64:65]
	s_nop 0
	v_add_f32_e32 v62, v62, v63
	v_add_f32_e32 v62, v62, v78

; __device__ __forceinline__ u32x4 pack8(f32x4 a, f32x4 b) { u32x4 w; w.x = pk2(a[0], a[1]); w.y = pk2(a[2], a[3]); w.z = pk2(b[0], b[1]); w.w = pk2(b[2], b[3]); return w; }
; __device__ __forceinline__ float sq8(const f32x4& a, const f32x4& b) { return ((a[0] * a[0] + a[1] * a[1]) + (a[2] * a[2] + a[3] * a[3])) + ((b[0] * b[0] + b[1] * b[1]) + (b[2] * b[2] + b[3] * b[3])); }
;     __device__ __forceinline__ void operator()(const f32x4 (&acc)[2][2][4][2], const Unit& u, int ui, int wr, int wc, int fr, int fq, LAS unsigned char* lds) const {
;     ...
;                     else if (pn == 6) { *(u32x4*)(CKV + (size_t)row * 256 + c) = pack8(v0, v1); sq += sq8(v0, v1); }
.LBB0_495:
	s_andn2_b64 vcc, exec, s[64:65]
	s_cbranch_vccnz .LBB0_497
	v_lshl_add_u64 v[68:69], s[38:39], 0, v[68:69]
	v_cvt_pk_bf16_f32 v62, v54, v55
	v_cvt_pk_bf16_f32 v63, v56, v57
	v_cvt_pk_bf16_f32 v64, v50, v51
	v_cvt_pk_bf16_f32 v65, v52, v53
	v_lshl_add_u64 v[68:69], v[68:69], 0, v[0:1]
	global_store_dwordx4 v[68:69], v[62:65], off offset:256
	v_mov_b32_e32 v68, v57
	v_mov_b32_e32 v69, v53
	v_mov_b32_e32 v64, v55
	v_mov_b32_e32 v65, v51
	v_mov_b32_e32 v62, v54
	v_mov_b32_e32 v63, v50
	v_pk_mul_f32 v[64:65], v[64:65], v[64:65]
	v_pk_mul_f32 v[68:69], v[68:69], v[68:69]
	v_pk_fma_f32 v[62:63], v[62:63], v[62:63], v[64:65]
	v_mov_b32_e32 v64, v56
	v_mov_b32_e32 v65, v52
	v_pk_fma_f32 v[64:65], v[64:65], v[64:65], v[68:69]
	s_nop 0
	v_pk_add_f32 v[62:63], v[62:63], v[64:65]
	s_nop 0
	v_add_f32_e32 v62, v62, v63
	v_add_f32_e32 v62, v62, v78

; __device__ __forceinline__ u32x4 pack8(f32x4 a, f32x4 b) { u32x4 w; w.x = pk2(a[0], a[1]); w.y = pk2(a[2], a[3]); w.z = pk2(b[0], b[1]); w.w = pk2(b[2], b[3]); return w; }
; __device__ __forceinline__ float fq_sum(float v) { v += xor16(v); v += xor32(v); return v; }
;     __device__ __forceinline__ void operator()(const f32x4 (&acc)[2][2][4][2], const Unit& u, int ui, int wr, int wc, int fr, int fq, LAS unsigned char* lds) const {
;     ...
;                     f32x4 v0 = acc[ai][bj][m][0] * rs, v1 = acc[ai][bj][m][1] * rs;
;                     if (pn < 6) { if (pn < 2) { v0 = v0 * QS_SB; v1 = v1 * QS_SB; } *(u32x4*)(QKV + (size_t)row * 1536 + pn * 256 + c) = pack8(v0, v1); }
;     ...
;                 if (pn >= 6) {
;                     sq = fq_sum(sq);
;                     if (fq == 0) { if (pn == 6) SQK[(size_t)row * 4 + wc] = sq; else SQQ[(size_t)row * 8 + (pn - 7) * 4 + wc] = sq; }
.LBB0_498:
	v_pk_mul_f32 v[62:63], v[56:57], s[96:97] op_sel_hi:[1,0]
	v_pk_mul_f32 v[64:65], v[54:55], s[96:97] op_sel_hi:[1,0]
	v_pk_mul_f32 v[68:69], v[52:53], s[96:97] op_sel_hi:[1,0]
	v_pk_mul_f32 v[70:71], v[50:51], s[96:97] op_sel_hi:[1,0]
	v_cndmask_b32_e64 v53, v53, v69, s[12:13]
	v_cndmask_b32_e64 v68, v52, v68, s[12:13]
	v_cndmask_b32_e64 v52, v51, v71, s[12:13]
	v_cndmask_b32_e64 v69, v50, v70, s[12:13]
	v_cndmask_b32_e64 v51, v57, v63, s[12:13]
	v_cndmask_b32_e64 v56, v56, v62, s[12:13]
	v_cndmask_b32_e64 v50, v55, v65, s[12:13]
	v_cndmask_b32_e64 v54, v54, v64, s[12:13]
	v_cvt_pk_bf16_f32 v50, v54, v50
	v_cvt_pk_bf16_f32 v51, v56, v51
	v_cvt_pk_bf16_f32 v52, v69, v52
	v_cvt_pk_bf16_f32 v53, v68, v53
	v_lshl_add_u64 v[54:55], v[58:59], 0, v[0:1]
	v_mov_b32_e32 v62, v78
	global_store_dwordx4 v[54:55], v[50:53], off offset:256
	s_and_b64 vcc, exec, s[20:21]
	s_cbranch_vccnz .LBB0_502
.LBB0_499:
	v_mov_b32_e32 v50, v62
	v_mov_b32_e32 v51, v62
	v_readlane_b32 s6, v255, 6
	s_nop 0
	v_permlane16_swap_b32_e32 v50, v51
	v_readlane_b32 s7, v255, 7
	s_nop 1
	v_cndmask_b32_e64 v50, v50, v51, s[6:7]
	v_add_f32_e32 v50, v62, v50
	v_mov_b32_e32 v51, v50
	v_mov_b32_e32 v52, v50
	s_nop 1
	v_permlane32_swap_b32_e32 v51, v52
	s_and_saveexec_b64 s[64:65], s[16:17]
	s_cbranch_execz .LBB0_501
	v_cndmask_b32_e64 v51, v51, v52, s[4:5]
	v_lshlrev_b64 v[52:53], 5, v[66:67]
	v_lshl_add_u64 v[52:53], s[48:49], 0, v[52:53]
	v_add_f32_e32 v54, v50, v51
	v_lshl_add_u64 v[50:51], s[50:51], 0, v[60:61]
	v_lshl_add_u64 v[52:53], s[88:89], 2, v[52:53]
	v_cndmask_b32_e64 v51, v53, v51, s[14:15]
	v_cndmask_b32_e64 v50, v52, v50, s[14:15]
	s_lshl_b32 s6, s91, 2
	s_mov_b32 s7, s89
	v_lshl_add_u64 v[50:51], v[50:51], 0, s[6:7]
	global_store_dword v[50:51], v54, off

; __device__ __forceinline__ u32x4 pack8(f32x4 a, f32x4 b) { u32x4 w; w.x = pk2(a[0], a[1]); w.y = pk2(a[2], a[3]); w.z = pk2(b[0], b[1]); w.w = pk2(b[2], b[3]); return w; }
; __device__ __forceinline__ float sq8(const f32x4& a, const f32x4& b) { return ((a[0] * a[0] + a[1] * a[1]) + (a[2] * a[2] + a[3] * a[3])) + ((b[0] * b[0] + b[1] * b[1]) + (b[2] * b[2] + b[3] * b[3])); }
; __device__ __forceinline__ f32x2 rtab_get(LAS unsigned char* lds, int ui, int r) { return ((const LAS f32x2*)(lds + RTAB_OFF))[(ui & 1) * 256 + r]; }
;     __device__ __forceinline__ void operator()(const f32x4 (&acc)[2][2][4][2], const Unit& u, int ui, int wr, int wc, int fr, int fq, LAS unsigned char* lds) const {
;     ...
;                 const int rr = ai * 128 + wr * 64 + m * 16 + fr, row = u.pm * 256 + rr; const float rs = rtab_get(lds, ui, rr)[0];
;                 float sq = 0.f;
; #pragma unroll
;                 for (int bj = 0; bj < 2; ++bj) {
;                     const int c = bj * 128 + wc * 32 + fq * 8;
;                     f32x4 v0 = acc[ai][bj][m][0] * rs, v1 = acc[ai][bj][m][1] * rs;
;                     if (pn < 6) { if (pn < 2) { v0 = v0 * QS_SB; v1 = v1 * QS_SB; } *(u32x4*)(QKV + (size_t)row * 1536 + pn * 256 + c) = pack8(v0, v1); }
;                     else if (pn == 6) { *(u32x4*)(CKV + (size_t)row * 256 + c) = pack8(v0, v1); sq += sq8(v0, v1); }
;                     else if (pn == 7) { *(u32x4*)(CQ + (size_t)row * 384 + c) = pack8(v0, v1); sq += sq8(v0, v1); }
;                     else if (bj == 0) { *(u32x4*)(CQ + (size_t)row * 384 + 256 + c) = pack8(v0, v1); sq += sq8(v0, v1); }
.LBB0_502:
	ds_read_b32 v56, v150 offset:1152
	v_add_u32_e32 v50, 0x90, v138
	v_ashrrev_i32_e32 v51, 31, v50
	v_mad_i64_i32 v[54:55], s[6:7], v50, s59, 0
	v_lshlrev_b64 v[52:53], 9, v[50:51]
	s_waitcnt lgkmcnt(0)
	v_pk_mul_f32 v[48:49], v[48:49], v[56:57] op_sel_hi:[1,0]
	v_pk_mul_f32 v[46:47], v[46:47], v[56:57] op_sel_hi:[1,0]
	v_pk_mul_f32 v[60:61], v[44:45], v[56:57] op_sel_hi:[1,0]
	v_pk_mul_f32 v[58:59], v[42:43], v[56:57] op_sel_hi:[1,0]
	s_and_b64 vcc, exec, s[18:19]
	s_mov_b64 s[64:65], -1
	s_cbranch_vccnz .LBB0_512
	v_cvt_pk_bf16_f32 v42, v46, v47
	v_cvt_pk_bf16_f32 v43, v48, v49
	v_cvt_pk_bf16_f32 v44, v58, v59
	v_cvt_pk_bf16_f32 v45, v60, v61
	s_cmp_lt_i32 s26, 7
	s_cbranch_scc1 .LBB0_509
	s_cmp_lg_u32 s26, 7
	s_cbranch_scc0 .LBB0_506
	v_lshl_add_u64 v[62:63], s[40:41], 0, v[54:55]
	v_lshl_add_u64 v[62:63], v[62:63], 0, v[0:1]
	v_mov_b32_e32 v64, v47
	v_mov_b32_e32 v65, v59
	global_store_dwordx4 v[62:63], v[42:45], off offset:512
	v_mov_b32_e32 v62, v46
	v_mov_b32_e32 v63, v58
	v_pk_mul_f32 v[64:65], v[64:65], v[64:65]
	v_mov_b32_e32 v66, v49
	v_mov_b32_e32 v67, v61
	v_pk_fma_f32 v[62:63], v[62:63], v[62:63], v[64:65]
	v_mov_b32_e32 v64, v48
	v_mov_b32_e32 v65, v60
	v_pk_mul_f32 v[66:67], v[66:67], v[66:67]
	s_mov_b64 s[64:65], 0
	v_pk_fma_f32 v[64:65], v[64:65], v[64:65], v[66:67]
	s_nop 0
	v_pk_add_f32 v[62:63], v[62:63], v[64:65]
	s_nop 0
	v_add_f32_e32 v62, v62, v63
.LBB0_506:
	s_andn2_b64 vcc, exec, s[64:65]
	s_cbranch_vccnz .LBB0_508
	v_lshl_add_u64 v[62:63], s[40:41], 0, v[54:55]
	v_lshl_add_u64 v[62:63], v[62:63], 0, v[0:1]
	v_mov_b32_e32 v64, v47
	v_mov_b32_e32 v65, v59
	global_store_dwordx4 v[62:63], v[42:45], off
	v_mov_b32_e32 v62, v46
	v_mov_b32_e32 v63, v58
	v_pk_mul_f32 v[64:65], v[64:65], v[64:65]
	v_mov_b32_e32 v66, v49
	v_mov_b32_e32 v67, v61
	v_pk_fma_f32 v[62:63], v[62:63], v[62:63], v[64:65]
	v_mov_b32_e32 v64, v48
	v_mov_b32_e32 v65, v60
	v_pk_mul_f32 v[66:67], v[66:67], v[66:67]
	s_nop 0
	v_pk_fma_f32 v[64:65], v[64:65], v[64:65], v[66:67]
	s_nop 0
	v_pk_add_f32 v[62:63], v[62:63], v[64:65]
	s_nop 0
	v_add_f32_e32 v62, v62, v63

; __device__ __forceinline__ u32x4 pack8(f32x4 a, f32x4 b) { u32x4 w; w.x = pk2(a[0], a[1]); w.y = pk2(a[2], a[3]); w.z = pk2(b[0], b[1]); w.w = pk2(b[2], b[3]); return w; }
; __device__ __forceinline__ float sq8(const f32x4& a, const f32x4& b) { return ((a[0] * a[0] + a[1] * a[1]) + (a[2] * a[2] + a[3] * a[3])) + ((b[0] * b[0] + b[1] * b[1]) + (b[2] * b[2] + b[3] * b[3])); }
;     __device__ __forceinline__ void operator()(const f32x4 (&acc)[2][2][4][2], const Unit& u, int ui, int wr, int wc, int fr, int fq, LAS unsigned char* lds) const {
;     ...
;                     else if (pn == 6) { *(u32x4*)(CKV + (size_t)row * 256 + c) = pack8(v0, v1); sq += sq8(v0, v1); }
.LBB0_509:
	s_andn2_b64 vcc, exec, s[64:65]
	s_cbranch_vccnz .LBB0_511
	v_lshl_add_u64 v[62:63], s[38:39], 0, v[52:53]
	v_lshl_add_u64 v[62:63], v[62:63], 0, v[0:1]
	global_store_dwordx4 v[62:63], v[42:45], off
	v_mov_b32_e32 v62, v49
	v_mov_b32_e32 v63, v61
	v_mov_b32_e32 v44, v47
	v_mov_b32_e32 v45, v59
	v_mov_b32_e32 v42, v46
	v_mov_b32_e32 v43, v58
	v_pk_mul_f32 v[44:45], v[44:45], v[44:45]
	v_pk_mul_f32 v[62:63], v[62:63], v[62:63]
	v_pk_fma_f32 v[42:43], v[42:43], v[42:43], v[44:45]
	v_mov_b32_e32 v44, v48
	v_mov_b32_e32 v45, v60
	v_pk_fma_f32 v[44:45], v[44:45], v[44:45], v[62:63]
	s_nop 0
	v_pk_add_f32 v[42:43], v[42:43], v[44:45]
	s_nop 0
	v_add_f32_e32 v62, v42, v43

; __device__ __forceinline__ u32x4 pack8(f32x4 a, f32x4 b) { u32x4 w; w.x = pk2(a[0], a[1]); w.y = pk2(a[2], a[3]); w.z = pk2(b[0], b[1]); w.w = pk2(b[2], b[3]); return w; }
;     __device__ __forceinline__ void operator()(const f32x4 (&acc)[2][2][4][2], const Unit& u, int ui, int wr, int wc, int fr, int fq, LAS unsigned char* lds) const {
;     ...
;                     f32x4 v0 = acc[ai][bj][m][0] * rs, v1 = acc[ai][bj][m][1] * rs;
;                     if (pn < 6) { if (pn < 2) { v0 = v0 * QS_SB; v1 = v1 * QS_SB; } *(u32x4*)(QKV + (size_t)row * 1536 + pn * 256 + c) = pack8(v0, v1); }
.LBB0_512:
	v_mad_i64_i32 v[42:43], s[6:7], v50, s3, 0
	v_lshl_add_u64 v[42:43], s[36:37], 0, v[42:43]
	s_and_b64 vcc, exec, s[64:65]
	v_lshl_add_u64 v[42:43], s[62:63], 1, v[42:43]
	s_cbranch_vccz .LBB0_514
	v_pk_mul_f32 v[44:45], v[48:49], s[96:97] op_sel_hi:[1,0]
	v_pk_mul_f32 v[62:63], v[46:47], s[96:97] op_sel_hi:[1,0]
	v_pk_mul_f32 v[64:65], v[60:61], s[96:97] op_sel_hi:[1,0]
	v_pk_mul_f32 v[66:67], v[58:59], s[96:97] op_sel_hi:[1,0]
	v_cndmask_b32_e64 v57, v61, v65, s[12:13]
	v_cndmask_b32_e64 v60, v60, v64, s[12:13]
	v_cndmask_b32_e64 v59, v59, v67, s[12:13]
	v_cndmask_b32_e64 v58, v58, v66, s[12:13]
	v_cndmask_b32_e64 v45, v49, v45, s[12:13]
	v_cndmask_b32_e64 v48, v48, v44, s[12:13]
	v_cndmask_b32_e64 v44, v47, v63, s[12:13]
	v_cndmask_b32_e64 v46, v46, v62, s[12:13]
	v_cvt_pk_bf16_f32 v44, v46, v44
	v_cvt_pk_bf16_f32 v45, v48, v45
	v_cvt_pk_bf16_f32 v46, v58, v59
	v_cvt_pk_bf16_f32 v47, v60, v57
	v_lshl_add_u64 v[48:49], v[42:43], 0, v[0:1]
	v_mov_b32_e32 v62, 0
	global_store_dwordx4 v[48:49], v[44:47], off

; __device__ __forceinline__ float xor32(float x) { auto rr = __builtin_amdgcn_permlane32_swap(__float_as_uint(x), __float_as_uint(x), false, false); return __uint_as_float(((unsigned)(threadIdx.x & 32)) ? rr[0] : rr[1]); }
; __device__ __forceinline__ u32x4 pack8(f32x4 a, f32x4 b) { u32x4 w; w.x = pk2(a[0], a[1]); w.y = pk2(a[2], a[3]); w.z = pk2(b[0], b[1]); w.w = pk2(b[2], b[3]); return w; }
;     __device__ __forceinline__ void operator()(const f32x4 (&acc)[2][2][4][2], const Unit& u, int ui, int wr, int wc, int fr, int fq, LAS unsigned char* lds) const {
;     ...
;                     else if (wc == 0) {
;                         const int ib = 8 * (fq & 1);
;                         const f32x4 c0 = *(const f32x4*)(COS + (size_t)row * 16 + ib), c1 = *(const f32x4*)(COS + (size_t)row * 16 + ib + 4);
;                         const f32x4 s0 = *(const f32x4*)(SIN + (size_t)row * 16 + ib), s1 = *(const f32x4*)(SIN + (size_t)row * 16 + ib + 4);
;                         f32x4 p0, p1;
; #pragma unroll
;                         for (int i = 0; i < 4; ++i) { p0[i] = xor32(v0[i]); p1[i] = xor32(v1[i]); }
;                         const float sg = (fq < 2) ? -1.f : 1.f;
;                         const f32x4 o0 = v0 * c0 + p0 * s0 * sg, o1 = v1 * c1 + p1 * s1 * sg;
;                         *(u32x4*)(KR + (size_t)row * 32 + fq * 8) = pack8(o0, o1);
.LBB0_517:
	s_cmp_lt_i32 s26, 7
	s_cbranch_scc1 .LBB0_525
	s_cmp_lg_u32 s26, 7
	s_cbranch_scc0 .LBB0_522
	s_andn2_b64 vcc, exec, s[56:57]
	s_cbranch_vccnz .LBB0_521
	v_lshlrev_b64 v[64:65], 2, v[44:45]
	v_lshl_add_u64 v[46:47], s[44:45], 0, v[64:65]
	v_lshlrev_b32_e32 v66, 2, v128
	v_mov_b32_e32 v67, v1
	v_lshl_add_u64 v[64:65], s[46:47], 0, v[64:65]
	v_lshl_add_u64 v[56:57], v[46:47], 0, v[66:67]
	v_lshl_add_u64 v[68:69], v[64:65], 0, v[66:67]
	s_waitcnt vmcnt(10)
	v_mov_b32_e32 v46, v174
	v_mov_b32_e32 v47, v175
	v_mov_b32_e32 v48, v176
	v_mov_b32_e32 v49, v177
	v_mov_b32_e32 v56, v178
	v_mov_b32_e32 v57, v179
	v_mov_b32_e32 v58, v180
	v_mov_b32_e32 v59, v181
	v_mov_b32_e32 v64, v182
	v_mov_b32_e32 v65, v183
	v_mov_b32_e32 v66, v184
	v_mov_b32_e32 v67, v185
	v_mov_b32_e32 v68, v230
	v_mov_b32_e32 v69, v231
	v_mov_b32_e32 v70, v232
	v_mov_b32_e32 v71, v233
	global_load_dwordx4 v[174:177], v[206:207], off offset:3072
	global_load_dwordx4 v[178:181], v[206:207], off offset:3088
	global_load_dwordx4 v[182:185], v[208:209], off offset:3072
	global_load_dwordx4 v[230:233], v[208:209], off offset:3088
	v_mov_b32_e32 v63, v38
	v_mov_b32_e32 v72, v38
	s_nop 1
	v_permlane32_swap_b32_e32 v63, v72
	v_cndmask_b32_e64 v72, v63, v72, s[4:5]
	v_mov_b32_e32 v63, v34
	v_mov_b32_e32 v73, v34
	s_nop 1
	v_permlane32_swap_b32_e32 v63, v73
	v_cndmask_b32_e64 v74, v63, v73, s[4:5]
	v_mov_b32_e32 v63, v39
	v_mov_b32_e32 v73, v39
	s_nop 1
	v_permlane32_swap_b32_e32 v63, v73
	v_cndmask_b32_e64 v73, v63, v73, s[4:5]
	v_mov_b32_e32 v63, v35
	v_mov_b32_e32 v75, v35
	s_nop 1
	v_permlane32_swap_b32_e32 v63, v75
	v_cndmask_b32_e64 v75, v63, v75, s[4:5]
	v_mov_b32_e32 v63, v40
	v_mov_b32_e32 v76, v40
	s_nop 1
	v_permlane32_swap_b32_e32 v63, v76
	v_cndmask_b32_e64 v76, v63, v76, s[4:5]
	v_mov_b32_e32 v63, v36
	v_mov_b32_e32 v77, v36
	s_nop 1
	v_permlane32_swap_b32_e32 v63, v77
	v_cndmask_b32_e64 v78, v63, v77, s[4:5]
	v_mov_b32_e32 v63, v41
	v_mov_b32_e32 v77, v41
	s_nop 1
	v_permlane32_swap_b32_e32 v63, v77
	v_cndmask_b32_e64 v77, v63, v77, s[4:5]
	v_mov_b32_e32 v63, v37
	v_mov_b32_e32 v79, v37
	s_nop 1
	v_permlane32_swap_b32_e32 v63, v79
	v_cndmask_b32_e64 v79, v63, v79, s[4:5]
	v_lshlrev_b64 v[60:61], 6, v[50:51]
	s_waitcnt lgkmcnt(0)
	v_pk_mul_f32 v[66:67], v[66:67], v[76:77]
	v_pk_mul_f32 v[64:65], v[64:65], v[72:73]
	v_mov_b32_e32 v72, v114
	v_mov_b32_e32 v73, v114
	v_pk_mul_f32 v[64:65], v[114:115], v[64:65]
	v_pk_mul_f32 v[66:67], v[72:73], v[66:67]
	v_pk_fma_f32 v[46:47], v[38:39], v[46:47], v[64:65]
	v_pk_fma_f32 v[48:49], v[40:41], v[48:49], v[66:67]
	v_pk_mul_f32 v[64:65], v[70:71], v[78:79]
	v_pk_mul_f32 v[66:67], v[68:69], v[74:75]
	v_pk_mul_f32 v[64:65], v[72:73], v[64:65]
	v_pk_mul_f32 v[66:67], v[114:115], v[66:67]
	v_pk_fma_f32 v[58:59], v[36:37], v[58:59], v[64:65]
	v_pk_fma_f32 v[56:57], v[34:35], v[56:57], v[66:67]
	v_cvt_pk_bf16_f32 v46, v46, v47
	v_cvt_pk_bf16_f32 v47, v48, v49
	v_cvt_pk_bf16_f32 v48, v56, v57
	v_cvt_pk_bf16_f32 v49, v58, v59
	v_lshl_add_u64 v[56:57], s[42:43], 0, v[60:61]
	v_lshlrev_b32_e32 v58, 1, v149
	v_mov_b32_e32 v59, v1
	v_lshl_add_u64 v[56:57], v[56:57], 0, v[58:59]
	global_store_dwordx4 v[56:57], v[46:49], off

; __device__ __forceinline__ u32x4 pack8(f32x4 a, f32x4 b) { u32x4 w; w.x = pk2(a[0], a[1]); w.y = pk2(a[2], a[3]); w.z = pk2(b[0], b[1]); w.w = pk2(b[2], b[3]); return w; }
; __device__ __forceinline__ float sq8(const f32x4& a, const f32x4& b) { return ((a[0] * a[0] + a[1] * a[1]) + (a[2] * a[2] + a[3] * a[3])) + ((b[0] * b[0] + b[1] * b[1]) + (b[2] * b[2] + b[3] * b[3])); }
;     __device__ __forceinline__ void operator()(const f32x4 (&acc)[2][2][4][2], const Unit& u, int ui, int wr, int wc, int fr, int fq, LAS unsigned char* lds) const {
;     ...
;                     else if (pn == 7) { *(u32x4*)(CQ + (size_t)row * 384 + c) = pack8(v0, v1); sq += sq8(v0, v1); }
;                     else if (bj == 0) { *(u32x4*)(CQ + (size_t)row * 384 + 256 + c) = pack8(v0, v1); sq += sq8(v0, v1); }
.LBB0_522:
	s_andn2_b64 vcc, exec, s[64:65]
	v_mov_b32_e32 v46, v62
	s_cbranch_vccnz .LBB0_524
	v_lshl_add_u64 v[54:55], s[40:41], 0, v[54:55]
	v_cvt_pk_bf16_f32 v46, v38, v39
	v_cvt_pk_bf16_f32 v47, v40, v41
	v_cvt_pk_bf16_f32 v48, v34, v35
	v_cvt_pk_bf16_f32 v49, v36, v37
	v_lshl_add_u64 v[54:55], v[54:55], 0, v[0:1]
	global_store_dwordx4 v[54:55], v[46:49], off offset:256
	v_mov_b32_e32 v54, v41
	v_mov_b32_e32 v55, v37
	v_mov_b32_e32 v48, v39
	v_mov_b32_e32 v49, v35
	v_mov_b32_e32 v46, v38
	v_mov_b32_e32 v47, v34
	v_pk_mul_f32 v[48:49], v[48:49], v[48:49]
	v_pk_mul_f32 v[54:55], v[54:55], v[54:55]
	v_pk_fma_f32 v[46:47], v[46:47], v[46:47], v[48:49]
	v_mov_b32_e32 v48, v40
	v_mov_b32_e32 v49, v36
	v_pk_fma_f32 v[48:49], v[48:49], v[48:49], v[54:55]
	s_nop 0
	v_pk_add_f32 v[46:47], v[46:47], v[48:49]
	s_nop 0
	v_add_f32_e32 v46, v46, v47
	v_add_f32_e32 v46, v46, v62

; __device__ __forceinline__ u32x4 pack8(f32x4 a, f32x4 b) { u32x4 w; w.x = pk2(a[0], a[1]); w.y = pk2(a[2], a[3]); w.z = pk2(b[0], b[1]); w.w = pk2(b[2], b[3]); return w; }
; __device__ __forceinline__ float sq8(const f32x4& a, const f32x4& b) { return ((a[0] * a[0] + a[1] * a[1]) + (a[2] * a[2] + a[3] * a[3])) + ((b[0] * b[0] + b[1] * b[1]) + (b[2] * b[2] + b[3] * b[3])); }
;     __device__ __forceinline__ void operator()(const f32x4 (&acc)[2][2][4][2], const Unit& u, int ui, int wr, int wc, int fr, int fq, LAS unsigned char* lds) const {
;     ...
;                     else if (pn == 6) { *(u32x4*)(CKV + (size_t)row * 256 + c) = pack8(v0, v1); sq += sq8(v0, v1); }
.LBB0_525:
	s_andn2_b64 vcc, exec, s[64:65]
	s_cbranch_vccnz .LBB0_527
	v_lshl_add_u64 v[52:53], s[38:39], 0, v[52:53]
	v_cvt_pk_bf16_f32 v46, v38, v39
	v_cvt_pk_bf16_f32 v47, v40, v41
	v_cvt_pk_bf16_f32 v48, v34, v35
	v_cvt_pk_bf16_f32 v49, v36, v37
	v_lshl_add_u64 v[52:53], v[52:53], 0, v[0:1]
	global_store_dwordx4 v[52:53], v[46:49], off offset:256
	v_mov_b32_e32 v52, v41
	v_mov_b32_e32 v53, v37
	v_mov_b32_e32 v48, v39
	v_mov_b32_e32 v49, v35
	v_mov_b32_e32 v46, v38
	v_mov_b32_e32 v47, v34
	v_pk_mul_f32 v[48:49], v[48:49], v[48:49]
	v_pk_mul_f32 v[52:53], v[52:53], v[52:53]
	v_pk_fma_f32 v[46:47], v[46:47], v[46:47], v[48:49]
	v_mov_b32_e32 v48, v40
	v_mov_b32_e32 v49, v36
	v_pk_fma_f32 v[48:49], v[48:49], v[48:49], v[52:53]
	s_nop 0
	v_pk_add_f32 v[46:47], v[46:47], v[48:49]
	s_nop 0
	v_add_f32_e32 v46, v46, v47
	v_add_f32_e32 v46, v46, v62

; __device__ __forceinline__ u32x4 pack8(f32x4 a, f32x4 b) { u32x4 w; w.x = pk2(a[0], a[1]); w.y = pk2(a[2], a[3]); w.z = pk2(b[0], b[1]); w.w = pk2(b[2], b[3]); return w; }
; __device__ __forceinline__ float fq_sum(float v) { v += xor16(v); v += xor32(v); return v; }
;     __device__ __forceinline__ void operator()(const f32x4 (&acc)[2][2][4][2], const Unit& u, int ui, int wr, int wc, int fr, int fq, LAS unsigned char* lds) const {
;     ...
;                     f32x4 v0 = acc[ai][bj][m][0] * rs, v1 = acc[ai][bj][m][1] * rs;
;                     if (pn < 6) { if (pn < 2) { v0 = v0 * QS_SB; v1 = v1 * QS_SB; } *(u32x4*)(QKV + (size_t)row * 1536 + pn * 256 + c) = pack8(v0, v1); }
;     ...
;                 if (pn >= 6) {
;                     sq = fq_sum(sq);
;                     if (fq == 0) { if (pn == 6) SQK[(size_t)row * 4 + wc] = sq; else SQQ[(size_t)row * 8 + (pn - 7) * 4 + wc] = sq; }
.LBB0_528:
	v_pk_mul_f32 v[46:47], v[40:41], s[96:97] op_sel_hi:[1,0]
	v_pk_mul_f32 v[48:49], v[38:39], s[96:97] op_sel_hi:[1,0]
	v_pk_mul_f32 v[52:53], v[36:37], s[96:97] op_sel_hi:[1,0]
	v_pk_mul_f32 v[54:55], v[34:35], s[96:97] op_sel_hi:[1,0]
	v_cndmask_b32_e64 v37, v37, v53, s[12:13]
	v_cndmask_b32_e64 v52, v36, v52, s[12:13]
	v_cndmask_b32_e64 v36, v35, v55, s[12:13]
	v_cndmask_b32_e64 v53, v34, v54, s[12:13]
	v_cndmask_b32_e64 v35, v41, v47, s[12:13]
	v_cndmask_b32_e64 v40, v40, v46, s[12:13]
	v_cndmask_b32_e64 v34, v39, v49, s[12:13]
	v_cndmask_b32_e64 v38, v38, v48, s[12:13]
	v_cvt_pk_bf16_f32 v34, v38, v34
	v_cvt_pk_bf16_f32 v35, v40, v35
	v_cvt_pk_bf16_f32 v36, v53, v36
	v_cvt_pk_bf16_f32 v37, v52, v37
	v_lshl_add_u64 v[38:39], v[42:43], 0, v[0:1]
	v_mov_b32_e32 v46, v62
	global_store_dwordx4 v[38:39], v[34:37], off offset:256
	s_and_b64 vcc, exec, s[20:21]
	s_cbranch_vccnz .LBB0_532
.LBB0_529:
	v_mov_b32_e32 v34, v46
	v_mov_b32_e32 v35, v46
	v_readlane_b32 s6, v255, 6
	s_nop 0
	v_permlane16_swap_b32_e32 v34, v35
	v_readlane_b32 s7, v255, 7
	s_nop 1
	v_cndmask_b32_e64 v34, v34, v35, s[6:7]
	v_add_f32_e32 v34, v46, v34
	v_mov_b32_e32 v35, v34
	v_mov_b32_e32 v36, v34
	s_nop 1
	v_permlane32_swap_b32_e32 v35, v36
	s_and_saveexec_b64 s[64:65], s[16:17]
	s_cbranch_execz .LBB0_531
	v_cndmask_b32_e64 v35, v35, v36, s[4:5]
	v_lshlrev_b64 v[36:37], 5, v[50:51]
	v_lshl_add_u64 v[36:37], s[48:49], 0, v[36:37]
	v_add_f32_e32 v38, v34, v35
	v_lshl_add_u64 v[34:35], s[50:51], 0, v[44:45]
	v_lshl_add_u64 v[36:37], s[88:89], 2, v[36:37]
	v_cndmask_b32_e64 v35, v37, v35, s[14:15]
	v_cndmask_b32_e64 v34, v36, v34, s[14:15]
	s_lshl_b32 s6, s91, 2
	s_mov_b32 s7, s89
	v_lshl_add_u64 v[34:35], v[34:35], 0, s[6:7]
	global_store_dword v[34:35], v38, off

; __device__ __forceinline__ u32x4 pack8(f32x4 a, f32x4 b) { u32x4 w; w.x = pk2(a[0], a[1]); w.y = pk2(a[2], a[3]); w.z = pk2(b[0], b[1]); w.w = pk2(b[2], b[3]); return w; }
; __device__ __forceinline__ float sq8(const f32x4& a, const f32x4& b) { return ((a[0] * a[0] + a[1] * a[1]) + (a[2] * a[2] + a[3] * a[3])) + ((b[0] * b[0] + b[1] * b[1]) + (b[2] * b[2] + b[3] * b[3])); }
; __device__ __forceinline__ f32x2 rtab_get(LAS unsigned char* lds, int ui, int r) { return ((const LAS f32x2*)(lds + RTAB_OFF))[(ui & 1) * 256 + r]; }
;     __device__ __forceinline__ void operator()(const f32x4 (&acc)[2][2][4][2], const Unit& u, int ui, int wr, int wc, int fr, int fq, LAS unsigned char* lds) const {
;     ...
;                 const int rr = ai * 128 + wr * 64 + m * 16 + fr, row = u.pm * 256 + rr; const float rs = rtab_get(lds, ui, rr)[0];
;                 float sq = 0.f;
; #pragma unroll
;                 for (int bj = 0; bj < 2; ++bj) {
;                     const int c = bj * 128 + wc * 32 + fq * 8;
;                     f32x4 v0 = acc[ai][bj][m][0] * rs, v1 = acc[ai][bj][m][1] * rs;
;                     if (pn < 6) { if (pn < 2) { v0 = v0 * QS_SB; v1 = v1 * QS_SB; } *(u32x4*)(QKV + (size_t)row * 1536 + pn * 256 + c) = pack8(v0, v1); }
;                     else if (pn == 6) { *(u32x4*)(CKV + (size_t)row * 256 + c) = pack8(v0, v1); sq += sq8(v0, v1); }
;                     else if (pn == 7) { *(u32x4*)(CQ + (size_t)row * 384 + c) = pack8(v0, v1); sq += sq8(v0, v1); }
;                     else if (bj == 0) { *(u32x4*)(CQ + (size_t)row * 384 + 256 + c) = pack8(v0, v1); sq += sq8(v0, v1); }
.LBB0_532:
	ds_read_b32 v40, v150 offset:1280
	v_add_u32_e32 v34, 0xa0, v138
	v_ashrrev_i32_e32 v35, 31, v34
	v_mad_i64_i32 v[38:39], s[6:7], v34, s59, 0
	v_lshlrev_b64 v[36:37], 9, v[34:35]
	s_waitcnt lgkmcnt(0)
	v_pk_mul_f32 v[32:33], v[32:33], v[40:41] op_sel_hi:[1,0]
	v_pk_mul_f32 v[30:31], v[30:31], v[40:41] op_sel_hi:[1,0]
	v_pk_mul_f32 v[44:45], v[28:29], v[40:41] op_sel_hi:[1,0]
	v_pk_mul_f32 v[42:43], v[26:27], v[40:41] op_sel_hi:[1,0]
	s_and_b64 vcc, exec, s[18:19]
	s_mov_b64 s[64:65], -1
	s_cbranch_vccnz .LBB0_542
	v_cvt_pk_bf16_f32 v26, v30, v31
	v_cvt_pk_bf16_f32 v27, v32, v33
	v_cvt_pk_bf16_f32 v28, v42, v43
	v_cvt_pk_bf16_f32 v29, v44, v45
	s_cmp_lt_i32 s26, 7
	s_cbranch_scc1 .LBB0_539
	s_cmp_lg_u32 s26, 7
	s_cbranch_scc0 .LBB0_536
	v_lshl_add_u64 v[46:47], s[40:41], 0, v[38:39]
	v_lshl_add_u64 v[46:47], v[46:47], 0, v[0:1]
	v_mov_b32_e32 v48, v31
	v_mov_b32_e32 v49, v43
	global_store_dwordx4 v[46:47], v[26:29], off offset:512
	v_mov_b32_e32 v46, v30
	v_mov_b32_e32 v47, v42
	v_pk_mul_f32 v[48:49], v[48:49], v[48:49]
	v_mov_b32_e32 v50, v33
	v_mov_b32_e32 v51, v45
	v_pk_fma_f32 v[46:47], v[46:47], v[46:47], v[48:49]
	v_mov_b32_e32 v48, v32
	v_mov_b32_e32 v49, v44
	v_pk_mul_f32 v[50:51], v[50:51], v[50:51]
	s_mov_b64 s[64:65], 0
	v_pk_fma_f32 v[48:49], v[48:49], v[48:49], v[50:51]
	s_nop 0
	v_pk_add_f32 v[46:47], v[46:47], v[48:49]
	s_nop 0
	v_add_f32_e32 v46, v46, v47
.LBB0_536:
	s_andn2_b64 vcc, exec, s[64:65]
	s_cbranch_vccnz .LBB0_538
	v_lshl_add_u64 v[46:47], s[40:41], 0, v[38:39]
	v_lshl_add_u64 v[46:47], v[46:47], 0, v[0:1]
	v_mov_b32_e32 v48, v31
	v_mov_b32_e32 v49, v43
	global_store_dwordx4 v[46:47], v[26:29], off
	v_mov_b32_e32 v46, v30
	v_mov_b32_e32 v47, v42
	v_pk_mul_f32 v[48:49], v[48:49], v[48:49]
	v_mov_b32_e32 v50, v33
	v_mov_b32_e32 v51, v45
	v_pk_fma_f32 v[46:47], v[46:47], v[46:47], v[48:49]
	v_mov_b32_e32 v48, v32
	v_mov_b32_e32 v49, v44
	v_pk_mul_f32 v[50:51], v[50:51], v[50:51]
	s_nop 0
	v_pk_fma_f32 v[48:49], v[48:49], v[48:49], v[50:51]
	s_nop 0
	v_pk_add_f32 v[46:47], v[46:47], v[48:49]
	s_nop 0
	v_add_f32_e32 v46, v46, v47

; __device__ __forceinline__ u32x4 pack8(f32x4 a, f32x4 b) { u32x4 w; w.x = pk2(a[0], a[1]); w.y = pk2(a[2], a[3]); w.z = pk2(b[0], b[1]); w.w = pk2(b[2], b[3]); return w; }
; __device__ __forceinline__ float sq8(const f32x4& a, const f32x4& b) { return ((a[0] * a[0] + a[1] * a[1]) + (a[2] * a[2] + a[3] * a[3])) + ((b[0] * b[0] + b[1] * b[1]) + (b[2] * b[2] + b[3] * b[3])); }
;     __device__ __forceinline__ void operator()(const f32x4 (&acc)[2][2][4][2], const Unit& u, int ui, int wr, int wc, int fr, int fq, LAS unsigned char* lds) const {
;     ...
;                     else if (pn == 6) { *(u32x4*)(CKV + (size_t)row * 256 + c) = pack8(v0, v1); sq += sq8(v0, v1); }
.LBB0_539:
	s_andn2_b64 vcc, exec, s[64:65]
	s_cbranch_vccnz .LBB0_541
	v_lshl_add_u64 v[46:47], s[38:39], 0, v[36:37]
	v_lshl_add_u64 v[46:47], v[46:47], 0, v[0:1]
	global_store_dwordx4 v[46:47], v[26:29], off
	v_mov_b32_e32 v46, v33
	v_mov_b32_e32 v47, v45
	v_mov_b32_e32 v28, v31
	v_mov_b32_e32 v29, v43
	v_mov_b32_e32 v26, v30
	v_mov_b32_e32 v27, v42
	v_pk_mul_f32 v[28:29], v[28:29], v[28:29]
	v_pk_mul_f32 v[46:47], v[46:47], v[46:47]
	v_pk_fma_f32 v[26:27], v[26:27], v[26:27], v[28:29]
	v_mov_b32_e32 v28, v32
	v_mov_b32_e32 v29, v44
	v_pk_fma_f32 v[28:29], v[28:29], v[28:29], v[46:47]
	s_nop 0
	v_pk_add_f32 v[26:27], v[26:27], v[28:29]
	s_nop 0
	v_add_f32_e32 v46, v26, v27

; __device__ __forceinline__ u32x4 pack8(f32x4 a, f32x4 b) { u32x4 w; w.x = pk2(a[0], a[1]); w.y = pk2(a[2], a[3]); w.z = pk2(b[0], b[1]); w.w = pk2(b[2], b[3]); return w; }
;     __device__ __forceinline__ void operator()(const f32x4 (&acc)[2][2][4][2], const Unit& u, int ui, int wr, int wc, int fr, int fq, LAS unsigned char* lds) const {
;     ...
;                     f32x4 v0 = acc[ai][bj][m][0] * rs, v1 = acc[ai][bj][m][1] * rs;
;                     if (pn < 6) { if (pn < 2) { v0 = v0 * QS_SB; v1 = v1 * QS_SB; } *(u32x4*)(QKV + (size_t)row * 1536 + pn * 256 + c) = pack8(v0, v1); }
.LBB0_542:
	v_mad_i64_i32 v[26:27], s[6:7], v34, s3, 0
	v_lshl_add_u64 v[26:27], s[36:37], 0, v[26:27]
	s_and_b64 vcc, exec, s[64:65]
	v_lshl_add_u64 v[26:27], s[62:63], 1, v[26:27]
	s_cbranch_vccz .LBB0_544
	v_pk_mul_f32 v[28:29], v[32:33], s[96:97] op_sel_hi:[1,0]
	v_pk_mul_f32 v[46:47], v[30:31], s[96:97] op_sel_hi:[1,0]
	v_pk_mul_f32 v[48:49], v[44:45], s[96:97] op_sel_hi:[1,0]
	v_pk_mul_f32 v[50:51], v[42:43], s[96:97] op_sel_hi:[1,0]
	v_cndmask_b32_e64 v41, v45, v49, s[12:13]
	v_cndmask_b32_e64 v44, v44, v48, s[12:13]
	v_cndmask_b32_e64 v43, v43, v51, s[12:13]
	v_cndmask_b32_e64 v42, v42, v50, s[12:13]
	v_cndmask_b32_e64 v29, v33, v29, s[12:13]
	v_cndmask_b32_e64 v32, v32, v28, s[12:13]
	v_cndmask_b32_e64 v28, v31, v47, s[12:13]
	v_cndmask_b32_e64 v30, v30, v46, s[12:13]
	v_cvt_pk_bf16_f32 v28, v30, v28
	v_cvt_pk_bf16_f32 v29, v32, v29
	v_cvt_pk_bf16_f32 v30, v42, v43
	v_cvt_pk_bf16_f32 v31, v44, v41
	v_lshl_add_u64 v[32:33], v[26:27], 0, v[0:1]
	v_mov_b32_e32 v46, 0
	global_store_dwordx4 v[32:33], v[28:31], off

; __device__ __forceinline__ float xor32(float x) { auto rr = __builtin_amdgcn_permlane32_swap(__float_as_uint(x), __float_as_uint(x), false, false); return __uint_as_float(((unsigned)(threadIdx.x & 32)) ? rr[0] : rr[1]); }
; __device__ __forceinline__ u32x4 pack8(f32x4 a, f32x4 b) { u32x4 w; w.x = pk2(a[0], a[1]); w.y = pk2(a[2], a[3]); w.z = pk2(b[0], b[1]); w.w = pk2(b[2], b[3]); return w; }
;     __device__ __forceinline__ void operator()(const f32x4 (&acc)[2][2][4][2], const Unit& u, int ui, int wr, int wc, int fr, int fq, LAS unsigned char* lds) const {
;     ...
;                     else if (wc == 0) {
;                         const int ib = 8 * (fq & 1);
;                         const f32x4 c0 = *(const f32x4*)(COS + (size_t)row * 16 + ib), c1 = *(const f32x4*)(COS + (size_t)row * 16 + ib + 4);
;                         const f32x4 s0 = *(const f32x4*)(SIN + (size_t)row * 16 + ib), s1 = *(const f32x4*)(SIN + (size_t)row * 16 + ib + 4);
;                         f32x4 p0, p1;
; #pragma unroll
;                         for (int i = 0; i < 4; ++i) { p0[i] = xor32(v0[i]); p1[i] = xor32(v1[i]); }
;                         const float sg = (fq < 2) ? -1.f : 1.f;
;                         const f32x4 o0 = v0 * c0 + p0 * s0 * sg, o1 = v1 * c1 + p1 * s1 * sg;
;                         *(u32x4*)(KR + (size_t)row * 32 + fq * 8) = pack8(o0, o1);
.LBB0_547:
	s_cmp_lt_i32 s26, 7
	s_cbranch_scc1 .LBB0_555
	s_cmp_lg_u32 s26, 7
	s_cbranch_scc0 .LBB0_552
	s_andn2_b64 vcc, exec, s[56:57]
	s_cbranch_vccnz .LBB0_551
	v_lshlrev_b64 v[48:49], 2, v[28:29]
	v_lshl_add_u64 v[30:31], s[44:45], 0, v[48:49]
	v_lshlrev_b32_e32 v50, 2, v128
	v_mov_b32_e32 v51, v1
	v_lshl_add_u64 v[48:49], s[46:47], 0, v[48:49]
	v_lshl_add_u64 v[40:41], v[30:31], 0, v[50:51]
	v_lshl_add_u64 v[52:53], v[48:49], 0, v[50:51]
	s_waitcnt vmcnt(10)
	v_mov_b32_e32 v30, v214
	v_mov_b32_e32 v31, v215
	v_mov_b32_e32 v32, v216
	v_mov_b32_e32 v33, v217
	v_mov_b32_e32 v40, v218
	v_mov_b32_e32 v41, v219
	v_mov_b32_e32 v42, v220
	v_mov_b32_e32 v43, v221
	v_mov_b32_e32 v48, v222
	v_mov_b32_e32 v49, v223
	v_mov_b32_e32 v50, v224
	v_mov_b32_e32 v51, v225
	v_mov_b32_e32 v52, v226
	v_mov_b32_e32 v53, v227
	v_mov_b32_e32 v54, v228
	v_mov_b32_e32 v55, v229
	v_mov_b32_e32 v47, v22
	v_mov_b32_e32 v56, v22
	s_nop 1
	v_permlane32_swap_b32_e32 v47, v56
	v_cndmask_b32_e64 v56, v47, v56, s[4:5]
	v_mov_b32_e32 v47, v18
	v_mov_b32_e32 v57, v18
	s_nop 1
	v_permlane32_swap_b32_e32 v47, v57
	v_cndmask_b32_e64 v58, v47, v57, s[4:5]
	v_mov_b32_e32 v47, v23
	v_mov_b32_e32 v57, v23
	s_nop 1
	v_permlane32_swap_b32_e32 v47, v57
	v_cndmask_b32_e64 v57, v47, v57, s[4:5]
	v_mov_b32_e32 v47, v19
	v_mov_b32_e32 v59, v19
	s_nop 1
	v_permlane32_swap_b32_e32 v47, v59
	v_cndmask_b32_e64 v59, v47, v59, s[4:5]
	v_mov_b32_e32 v47, v24
	v_mov_b32_e32 v60, v24
	s_nop 1
	v_permlane32_swap_b32_e32 v47, v60
	v_cndmask_b32_e64 v60, v47, v60, s[4:5]
	v_mov_b32_e32 v47, v20
	v_mov_b32_e32 v61, v20
	s_nop 1
	v_permlane32_swap_b32_e32 v47, v61
	v_cndmask_b32_e64 v62, v47, v61, s[4:5]
	v_mov_b32_e32 v47, v25
	v_mov_b32_e32 v61, v25
	s_nop 1
	v_permlane32_swap_b32_e32 v47, v61
	v_cndmask_b32_e64 v61, v47, v61, s[4:5]
	v_mov_b32_e32 v47, v21
	v_mov_b32_e32 v63, v21
	s_nop 1
	v_permlane32_swap_b32_e32 v47, v63
	v_cndmask_b32_e64 v63, v47, v63, s[4:5]
	v_lshlrev_b64 v[44:45], 6, v[34:35]
	s_waitcnt lgkmcnt(0)
	v_pk_mul_f32 v[50:51], v[50:51], v[60:61]
	v_pk_mul_f32 v[48:49], v[48:49], v[56:57]
	v_mov_b32_e32 v56, v114
	v_mov_b32_e32 v57, v114
	v_pk_mul_f32 v[48:49], v[114:115], v[48:49]
	v_pk_mul_f32 v[50:51], v[56:57], v[50:51]
	v_pk_fma_f32 v[30:31], v[22:23], v[30:31], v[48:49]
	v_pk_fma_f32 v[32:33], v[24:25], v[32:33], v[50:51]
	v_pk_mul_f32 v[48:49], v[54:55], v[62:63]
	v_pk_mul_f32 v[50:51], v[52:53], v[58:59]
	v_pk_mul_f32 v[48:49], v[56:57], v[48:49]
	v_pk_mul_f32 v[50:51], v[114:115], v[50:51]
	v_pk_fma_f32 v[42:43], v[20:21], v[42:43], v[48:49]
	v_pk_fma_f32 v[40:41], v[18:19], v[40:41], v[50:51]
	v_cvt_pk_bf16_f32 v30, v30, v31
	v_cvt_pk_bf16_f32 v31, v32, v33
	v_cvt_pk_bf16_f32 v32, v40, v41
	v_cvt_pk_bf16_f32 v33, v42, v43
	v_lshl_add_u64 v[40:41], s[42:43], 0, v[44:45]
	v_lshlrev_b32_e32 v42, 1, v149
	v_mov_b32_e32 v43, v1
	v_lshl_add_u64 v[40:41], v[40:41], 0, v[42:43]
	global_store_dwordx4 v[40:41], v[30:33], off

; __device__ __forceinline__ u32x4 pack8(f32x4 a, f32x4 b) { u32x4 w; w.x = pk2(a[0], a[1]); w.y = pk2(a[2], a[3]); w.z = pk2(b[0], b[1]); w.w = pk2(b[2], b[3]); return w; }
; __device__ __forceinline__ float sq8(const f32x4& a, const f32x4& b) { return ((a[0] * a[0] + a[1] * a[1]) + (a[2] * a[2] + a[3] * a[3])) + ((b[0] * b[0] + b[1] * b[1]) + (b[2] * b[2] + b[3] * b[3])); }
;     __device__ __forceinline__ void operator()(const f32x4 (&acc)[2][2][4][2], const Unit& u, int ui, int wr, int wc, int fr, int fq, LAS unsigned char* lds) const {
;     ...
;                     else if (pn == 7) { *(u32x4*)(CQ + (size_t)row * 384 + c) = pack8(v0, v1); sq += sq8(v0, v1); }
;                     else if (bj == 0) { *(u32x4*)(CQ + (size_t)row * 384 + 256 + c) = pack8(v0, v1); sq += sq8(v0, v1); }
.LBB0_552:
	s_andn2_b64 vcc, exec, s[64:65]
	v_mov_b32_e32 v30, v46
	s_cbranch_vccnz .LBB0_554
	v_lshl_add_u64 v[38:39], s[40:41], 0, v[38:39]
	v_cvt_pk_bf16_f32 v30, v22, v23
	v_cvt_pk_bf16_f32 v31, v24, v25
	v_cvt_pk_bf16_f32 v32, v18, v19
	v_cvt_pk_bf16_f32 v33, v20, v21
	v_lshl_add_u64 v[38:39], v[38:39], 0, v[0:1]
	global_store_dwordx4 v[38:39], v[30:33], off offset:256
	v_mov_b32_e32 v38, v25
	v_mov_b32_e32 v39, v21
	v_mov_b32_e32 v32, v23
	v_mov_b32_e32 v33, v19
	v_mov_b32_e32 v30, v22
	v_mov_b32_e32 v31, v18
	v_pk_mul_f32 v[32:33], v[32:33], v[32:33]
	v_pk_mul_f32 v[38:39], v[38:39], v[38:39]
	v_pk_fma_f32 v[30:31], v[30:31], v[30:31], v[32:33]
	v_mov_b32_e32 v32, v24
	v_mov_b32_e32 v33, v20
	v_pk_fma_f32 v[32:33], v[32:33], v[32:33], v[38:39]
	s_nop 0
	v_pk_add_f32 v[30:31], v[30:31], v[32:33]
	s_nop 0
	v_add_f32_e32 v30, v30, v31
	v_add_f32_e32 v30, v30, v46

; __device__ __forceinline__ u32x4 pack8(f32x4 a, f32x4 b) { u32x4 w; w.x = pk2(a[0], a[1]); w.y = pk2(a[2], a[3]); w.z = pk2(b[0], b[1]); w.w = pk2(b[2], b[3]); return w; }
; __device__ __forceinline__ float sq8(const f32x4& a, const f32x4& b) { return ((a[0] * a[0] + a[1] * a[1]) + (a[2] * a[2] + a[3] * a[3])) + ((b[0] * b[0] + b[1] * b[1]) + (b[2] * b[2] + b[3] * b[3])); }
;     __device__ __forceinline__ void operator()(const f32x4 (&acc)[2][2][4][2], const Unit& u, int ui, int wr, int wc, int fr, int fq, LAS unsigned char* lds) const {
;     ...
;                     else if (pn == 6) { *(u32x4*)(CKV + (size_t)row * 256 + c) = pack8(v0, v1); sq += sq8(v0, v1); }
.LBB0_555:
	s_andn2_b64 vcc, exec, s[64:65]
	s_cbranch_vccnz .LBB0_557
	v_lshl_add_u64 v[36:37], s[38:39], 0, v[36:37]
	v_cvt_pk_bf16_f32 v30, v22, v23
	v_cvt_pk_bf16_f32 v31, v24, v25
	v_cvt_pk_bf16_f32 v32, v18, v19
	v_cvt_pk_bf16_f32 v33, v20, v21
	v_lshl_add_u64 v[36:37], v[36:37], 0, v[0:1]
	global_store_dwordx4 v[36:37], v[30:33], off offset:256
	v_mov_b32_e32 v36, v25
	v_mov_b32_e32 v37, v21
	v_mov_b32_e32 v32, v23
	v_mov_b32_e32 v33, v19
	v_mov_b32_e32 v30, v22
	v_mov_b32_e32 v31, v18
	v_pk_mul_f32 v[32:33], v[32:33], v[32:33]
	v_pk_mul_f32 v[36:37], v[36:37], v[36:37]
	v_pk_fma_f32 v[30:31], v[30:31], v[30:31], v[32:33]
	v_mov_b32_e32 v32, v24
	v_mov_b32_e32 v33, v20
	v_pk_fma_f32 v[32:33], v[32:33], v[32:33], v[36:37]
	s_nop 0
	v_pk_add_f32 v[30:31], v[30:31], v[32:33]
	s_nop 0
	v_add_f32_e32 v30, v30, v31
	v_add_f32_e32 v30, v30, v46

; __device__ __forceinline__ u32x4 pack8(f32x4 a, f32x4 b) { u32x4 w; w.x = pk2(a[0], a[1]); w.y = pk2(a[2], a[3]); w.z = pk2(b[0], b[1]); w.w = pk2(b[2], b[3]); return w; }
; __device__ __forceinline__ float fq_sum(float v) { v += xor16(v); v += xor32(v); return v; }
;     __device__ __forceinline__ void operator()(const f32x4 (&acc)[2][2][4][2], const Unit& u, int ui, int wr, int wc, int fr, int fq, LAS unsigned char* lds) const {
;     ...
;                     f32x4 v0 = acc[ai][bj][m][0] * rs, v1 = acc[ai][bj][m][1] * rs;
;                     if (pn < 6) { if (pn < 2) { v0 = v0 * QS_SB; v1 = v1 * QS_SB; } *(u32x4*)(QKV + (size_t)row * 1536 + pn * 256 + c) = pack8(v0, v1); }
;     ...
;                 if (pn >= 6) {
;                     sq = fq_sum(sq);
;                     if (fq == 0) { if (pn == 6) SQK[(size_t)row * 4 + wc] = sq; else SQQ[(size_t)row * 8 + (pn - 7) * 4 + wc] = sq; }
.LBB0_558:
	v_pk_mul_f32 v[30:31], v[24:25], s[96:97] op_sel_hi:[1,0]
	v_pk_mul_f32 v[32:33], v[22:23], s[96:97] op_sel_hi:[1,0]
	v_pk_mul_f32 v[36:37], v[20:21], s[96:97] op_sel_hi:[1,0]
	v_pk_mul_f32 v[38:39], v[18:19], s[96:97] op_sel_hi:[1,0]
	v_cndmask_b32_e64 v21, v21, v37, s[12:13]
	v_cndmask_b32_e64 v36, v20, v36, s[12:13]
	v_cndmask_b32_e64 v20, v19, v39, s[12:13]
	v_cndmask_b32_e64 v37, v18, v38, s[12:13]
	v_cndmask_b32_e64 v19, v25, v31, s[12:13]
	v_cndmask_b32_e64 v24, v24, v30, s[12:13]
	v_cndmask_b32_e64 v18, v23, v33, s[12:13]
	v_cndmask_b32_e64 v22, v22, v32, s[12:13]
	v_cvt_pk_bf16_f32 v18, v22, v18
	v_cvt_pk_bf16_f32 v19, v24, v19
	v_cvt_pk_bf16_f32 v20, v37, v20
	v_cvt_pk_bf16_f32 v21, v36, v21
	v_lshl_add_u64 v[22:23], v[26:27], 0, v[0:1]
	v_mov_b32_e32 v30, v46
	global_store_dwordx4 v[22:23], v[18:21], off offset:256
	s_and_b64 vcc, exec, s[20:21]
	s_cbranch_vccnz .LBB0_562
.LBB0_559:
	v_mov_b32_e32 v18, v30
	v_mov_b32_e32 v19, v30
	v_readlane_b32 s6, v255, 6
	s_nop 0
	v_permlane16_swap_b32_e32 v18, v19
	v_readlane_b32 s7, v255, 7
	s_nop 1
	v_cndmask_b32_e64 v18, v18, v19, s[6:7]
	v_add_f32_e32 v18, v30, v18
	v_mov_b32_e32 v19, v18
	v_mov_b32_e32 v20, v18
	s_nop 1
	v_permlane32_swap_b32_e32 v19, v20
	s_and_saveexec_b64 s[64:65], s[16:17]
	s_cbranch_execz .LBB0_561
	v_cndmask_b32_e64 v19, v19, v20, s[4:5]
	v_lshlrev_b64 v[20:21], 5, v[34:35]
	v_lshl_add_u64 v[20:21], s[48:49], 0, v[20:21]
	v_add_f32_e32 v22, v18, v19
	v_lshl_add_u64 v[18:19], s[50:51], 0, v[28:29]
	v_lshl_add_u64 v[20:21], s[88:89], 2, v[20:21]
	v_cndmask_b32_e64 v19, v21, v19, s[14:15]
	v_cndmask_b32_e64 v18, v20, v18, s[14:15]
	s_lshl_b32 s6, s91, 2
	s_mov_b32 s7, s89
	v_lshl_add_u64 v[18:19], v[18:19], 0, s[6:7]
	global_store_dword v[18:19], v22, off

; __device__ __forceinline__ u32x4 pack8(f32x4 a, f32x4 b) { u32x4 w; w.x = pk2(a[0], a[1]); w.y = pk2(a[2], a[3]); w.z = pk2(b[0], b[1]); w.w = pk2(b[2], b[3]); return w; }
; __device__ __forceinline__ float sq8(const f32x4& a, const f32x4& b) { return ((a[0] * a[0] + a[1] * a[1]) + (a[2] * a[2] + a[3] * a[3])) + ((b[0] * b[0] + b[1] * b[1]) + (b[2] * b[2] + b[3] * b[3])); }
; __device__ __forceinline__ f32x2 rtab_get(LAS unsigned char* lds, int ui, int r) { return ((const LAS f32x2*)(lds + RTAB_OFF))[(ui & 1) * 256 + r]; }
;     __device__ __forceinline__ void operator()(const f32x4 (&acc)[2][2][4][2], const Unit& u, int ui, int wr, int wc, int fr, int fq, LAS unsigned char* lds) const {
;     ...
;                 const int rr = ai * 128 + wr * 64 + m * 16 + fr, row = u.pm * 256 + rr; const float rs = rtab_get(lds, ui, rr)[0];
;                 float sq = 0.f;
; #pragma unroll
;                 for (int bj = 0; bj < 2; ++bj) {
;                     const int c = bj * 128 + wc * 32 + fq * 8;
;                     f32x4 v0 = acc[ai][bj][m][0] * rs, v1 = acc[ai][bj][m][1] * rs;
;                     if (pn < 6) { if (pn < 2) { v0 = v0 * QS_SB; v1 = v1 * QS_SB; } *(u32x4*)(QKV + (size_t)row * 1536 + pn * 256 + c) = pack8(v0, v1); }
;                     else if (pn == 6) { *(u32x4*)(CKV + (size_t)row * 256 + c) = pack8(v0, v1); sq += sq8(v0, v1); }
;                     else if (pn == 7) { *(u32x4*)(CQ + (size_t)row * 384 + c) = pack8(v0, v1); sq += sq8(v0, v1); }
;                     else if (bj == 0) { *(u32x4*)(CQ + (size_t)row * 384 + 256 + c) = pack8(v0, v1); sq += sq8(v0, v1); }
.LBB0_562:
	ds_read_b32 v24, v150 offset:1408
	v_add_u32_e32 v18, 0xb0, v138
	v_ashrrev_i32_e32 v19, 31, v18
	v_mad_i64_i32 v[22:23], s[6:7], v18, s59, 0
	v_lshlrev_b64 v[20:21], 9, v[18:19]
	s_waitcnt lgkmcnt(0)
	v_pk_mul_f32 v[16:17], v[16:17], v[24:25] op_sel_hi:[1,0]
	v_pk_mul_f32 v[14:15], v[14:15], v[24:25] op_sel_hi:[1,0]
	v_pk_mul_f32 v[28:29], v[12:13], v[24:25] op_sel_hi:[1,0]
	v_pk_mul_f32 v[26:27], v[10:11], v[24:25] op_sel_hi:[1,0]
	s_and_b64 vcc, exec, s[18:19]
	s_mov_b64 s[64:65], -1
	s_cbranch_vccnz .LBB0_572
	v_cvt_pk_bf16_f32 v10, v14, v15
	v_cvt_pk_bf16_f32 v11, v16, v17
	v_cvt_pk_bf16_f32 v12, v26, v27
	v_cvt_pk_bf16_f32 v13, v28, v29
	s_cmp_lt_i32 s26, 7
	s_cbranch_scc1 .LBB0_569
	s_cmp_lg_u32 s26, 7
	s_cbranch_scc0 .LBB0_566
	v_lshl_add_u64 v[30:31], s[40:41], 0, v[22:23]
	v_lshl_add_u64 v[30:31], v[30:31], 0, v[0:1]
	v_mov_b32_e32 v32, v15
	v_mov_b32_e32 v33, v27
	global_store_dwordx4 v[30:31], v[10:13], off offset:512
	v_mov_b32_e32 v30, v14
	v_mov_b32_e32 v31, v26
	v_pk_mul_f32 v[32:33], v[32:33], v[32:33]
	v_mov_b32_e32 v34, v17
	v_mov_b32_e32 v35, v29
	v_pk_fma_f32 v[30:31], v[30:31], v[30:31], v[32:33]
	v_mov_b32_e32 v32, v16
	v_mov_b32_e32 v33, v28
	v_pk_mul_f32 v[34:35], v[34:35], v[34:35]
	s_mov_b64 s[64:65], 0
	v_pk_fma_f32 v[32:33], v[32:33], v[32:33], v[34:35]
	s_nop 0
	v_pk_add_f32 v[30:31], v[30:31], v[32:33]
	s_nop 0
	v_add_f32_e32 v30, v30, v31
.LBB0_566:
	s_andn2_b64 vcc, exec, s[64:65]
	s_cbranch_vccnz .LBB0_568
	v_lshl_add_u64 v[30:31], s[40:41], 0, v[22:23]
	v_lshl_add_u64 v[30:31], v[30:31], 0, v[0:1]
	v_mov_b32_e32 v32, v15
	v_mov_b32_e32 v33, v27
	global_store_dwordx4 v[30:31], v[10:13], off
	v_mov_b32_e32 v30, v14
	v_mov_b32_e32 v31, v26
	v_pk_mul_f32 v[32:33], v[32:33], v[32:33]
	v_mov_b32_e32 v34, v17
	v_mov_b32_e32 v35, v29
	v_pk_fma_f32 v[30:31], v[30:31], v[30:31], v[32:33]
	v_mov_b32_e32 v32, v16
	v_mov_b32_e32 v33, v28
	v_pk_mul_f32 v[34:35], v[34:35], v[34:35]
	s_nop 0
	v_pk_fma_f32 v[32:33], v[32:33], v[32:33], v[34:35]
	s_nop 0
	v_pk_add_f32 v[30:31], v[30:31], v[32:33]
	s_nop 0
	v_add_f32_e32 v30, v30, v31

; __device__ __forceinline__ u32x4 pack8(f32x4 a, f32x4 b) { u32x4 w; w.x = pk2(a[0], a[1]); w.y = pk2(a[2], a[3]); w.z = pk2(b[0], b[1]); w.w = pk2(b[2], b[3]); return w; }
; __device__ __forceinline__ float sq8(const f32x4& a, const f32x4& b) { return ((a[0] * a[0] + a[1] * a[1]) + (a[2] * a[2] + a[3] * a[3])) + ((b[0] * b[0] + b[1] * b[1]) + (b[2] * b[2] + b[3] * b[3])); }
;     __device__ __forceinline__ void operator()(const f32x4 (&acc)[2][2][4][2], const Unit& u, int ui, int wr, int wc, int fr, int fq, LAS unsigned char* lds) const {
;     ...
;                     else if (pn == 6) { *(u32x4*)(CKV + (size_t)row * 256 + c) = pack8(v0, v1); sq += sq8(v0, v1); }
.LBB0_569:
	s_andn2_b64 vcc, exec, s[64:65]
	s_cbranch_vccnz .LBB0_571
	v_lshl_add_u64 v[30:31], s[38:39], 0, v[20:21]
	v_lshl_add_u64 v[30:31], v[30:31], 0, v[0:1]
	global_store_dwordx4 v[30:31], v[10:13], off
	v_mov_b32_e32 v30, v17
	v_mov_b32_e32 v31, v29
	v_mov_b32_e32 v12, v15
	v_mov_b32_e32 v13, v27
	v_mov_b32_e32 v10, v14
	v_mov_b32_e32 v11, v26
	v_pk_mul_f32 v[12:13], v[12:13], v[12:13]
	v_pk_mul_f32 v[30:31], v[30:31], v[30:31]
	v_pk_fma_f32 v[10:11], v[10:11], v[10:11], v[12:13]
	v_mov_b32_e32 v12, v16
	v_mov_b32_e32 v13, v28
	v_pk_fma_f32 v[12:13], v[12:13], v[12:13], v[30:31]
	s_nop 0
	v_pk_add_f32 v[10:11], v[10:11], v[12:13]
	s_nop 0
	v_add_f32_e32 v30, v10, v11

; __device__ __forceinline__ u32x4 pack8(f32x4 a, f32x4 b) { u32x4 w; w.x = pk2(a[0], a[1]); w.y = pk2(a[2], a[3]); w.z = pk2(b[0], b[1]); w.w = pk2(b[2], b[3]); return w; }
;     __device__ __forceinline__ void operator()(const f32x4 (&acc)[2][2][4][2], const Unit& u, int ui, int wr, int wc, int fr, int fq, LAS unsigned char* lds) const {
;     ...
;                     f32x4 v0 = acc[ai][bj][m][0] * rs, v1 = acc[ai][bj][m][1] * rs;
;                     if (pn < 6) { if (pn < 2) { v0 = v0 * QS_SB; v1 = v1 * QS_SB; } *(u32x4*)(QKV + (size_t)row * 1536 + pn * 256 + c) = pack8(v0, v1); }
.LBB0_572:
	v_mad_i64_i32 v[10:11], s[6:7], v18, s3, 0
	v_lshl_add_u64 v[10:11], s[36:37], 0, v[10:11]
	s_and_b64 vcc, exec, s[64:65]
	v_lshl_add_u64 v[10:11], s[62:63], 1, v[10:11]
	s_cbranch_vccz .LBB0_574
	v_pk_mul_f32 v[12:13], v[16:17], s[96:97] op_sel_hi:[1,0]
	v_pk_mul_f32 v[30:31], v[14:15], s[96:97] op_sel_hi:[1,0]
	v_pk_mul_f32 v[32:33], v[28:29], s[96:97] op_sel_hi:[1,0]
	v_pk_mul_f32 v[34:35], v[26:27], s[96:97] op_sel_hi:[1,0]
	v_cndmask_b32_e64 v25, v29, v33, s[12:13]
	v_cndmask_b32_e64 v28, v28, v32, s[12:13]
	v_cndmask_b32_e64 v27, v27, v35, s[12:13]
	v_cndmask_b32_e64 v26, v26, v34, s[12:13]
	v_cndmask_b32_e64 v13, v17, v13, s[12:13]
	v_cndmask_b32_e64 v16, v16, v12, s[12:13]
	v_cndmask_b32_e64 v12, v15, v31, s[12:13]
	v_cndmask_b32_e64 v14, v14, v30, s[12:13]
	v_cvt_pk_bf16_f32 v12, v14, v12
	v_cvt_pk_bf16_f32 v13, v16, v13
	v_cvt_pk_bf16_f32 v14, v26, v27
	v_cvt_pk_bf16_f32 v15, v28, v25
	v_lshl_add_u64 v[16:17], v[10:11], 0, v[0:1]
	v_mov_b32_e32 v30, 0
	global_store_dwordx4 v[16:17], v[12:15], off

; __device__ __forceinline__ float xor32(float x) { auto rr = __builtin_amdgcn_permlane32_swap(__float_as_uint(x), __float_as_uint(x), false, false); return __uint_as_float(((unsigned)(threadIdx.x & 32)) ? rr[0] : rr[1]); }
; __device__ __forceinline__ u32x4 pack8(f32x4 a, f32x4 b) { u32x4 w; w.x = pk2(a[0], a[1]); w.y = pk2(a[2], a[3]); w.z = pk2(b[0], b[1]); w.w = pk2(b[2], b[3]); return w; }
;     __device__ __forceinline__ void operator()(const f32x4 (&acc)[2][2][4][2], const Unit& u, int ui, int wr, int wc, int fr, int fq, LAS unsigned char* lds) const {
;     ...
;                     else if (wc == 0) {
;                         const int ib = 8 * (fq & 1);
;                         const f32x4 c0 = *(const f32x4*)(COS + (size_t)row * 16 + ib), c1 = *(const f32x4*)(COS + (size_t)row * 16 + ib + 4);
;                         const f32x4 s0 = *(const f32x4*)(SIN + (size_t)row * 16 + ib), s1 = *(const f32x4*)(SIN + (size_t)row * 16 + ib + 4);
;                         f32x4 p0, p1;
; #pragma unroll
;                         for (int i = 0; i < 4; ++i) { p0[i] = xor32(v0[i]); p1[i] = xor32(v1[i]); }
;                         const float sg = (fq < 2) ? -1.f : 1.f;
;                         const f32x4 o0 = v0 * c0 + p0 * s0 * sg, o1 = v1 * c1 + p1 * s1 * sg;
;                         *(u32x4*)(KR + (size_t)row * 32 + fq * 8) = pack8(o0, o1);
.LBB0_577:
	s_cmp_lt_i32 s26, 7
	s_cbranch_scc1 .LBB0_585
	s_cmp_lg_u32 s26, 7
	s_cbranch_scc0 .LBB0_582
	s_andn2_b64 vcc, exec, s[56:57]
	s_cbranch_vccnz .LBB0_581
	v_lshlrev_b64 v[32:33], 2, v[12:13]
	v_lshl_add_u64 v[14:15], s[44:45], 0, v[32:33]
	v_lshlrev_b32_e32 v34, 2, v128
	v_mov_b32_e32 v35, v1
	v_lshl_add_u64 v[32:33], s[46:47], 0, v[32:33]
	v_lshl_add_u64 v[24:25], v[14:15], 0, v[34:35]
	v_lshl_add_u64 v[36:37], v[32:33], 0, v[34:35]
	s_waitcnt vmcnt(6)
	v_mov_b32_e32 v14, v174
	v_mov_b32_e32 v15, v175
	v_mov_b32_e32 v16, v176
	v_mov_b32_e32 v17, v177
	v_mov_b32_e32 v24, v178
	v_mov_b32_e32 v25, v179
	v_mov_b32_e32 v26, v180
	v_mov_b32_e32 v27, v181
	v_mov_b32_e32 v32, v182
	v_mov_b32_e32 v33, v183
	v_mov_b32_e32 v34, v184
	v_mov_b32_e32 v35, v185
	v_mov_b32_e32 v36, v230
	v_mov_b32_e32 v37, v231
	v_mov_b32_e32 v38, v232
	v_mov_b32_e32 v39, v233
	v_mov_b32_e32 v31, v6
	v_mov_b32_e32 v40, v6
	s_nop 1
	v_permlane32_swap_b32_e32 v31, v40
	v_cndmask_b32_e64 v40, v31, v40, s[4:5]
	v_mov_b32_e32 v31, v2
	v_mov_b32_e32 v41, v2
	s_nop 1
	v_permlane32_swap_b32_e32 v31, v41
	v_cndmask_b32_e64 v42, v31, v41, s[4:5]
	v_mov_b32_e32 v31, v7
	v_mov_b32_e32 v41, v7
	s_nop 1
	v_permlane32_swap_b32_e32 v31, v41
	v_cndmask_b32_e64 v41, v31, v41, s[4:5]
	v_mov_b32_e32 v31, v3
	v_mov_b32_e32 v43, v3
	s_nop 1
	v_permlane32_swap_b32_e32 v31, v43
	v_cndmask_b32_e64 v43, v31, v43, s[4:5]
	v_mov_b32_e32 v31, v8
	v_mov_b32_e32 v44, v8
	s_nop 1
	v_permlane32_swap_b32_e32 v31, v44
	v_cndmask_b32_e64 v44, v31, v44, s[4:5]
	v_mov_b32_e32 v31, v4
	v_mov_b32_e32 v45, v4
	s_nop 1
	v_permlane32_swap_b32_e32 v31, v45
	v_cndmask_b32_e64 v46, v31, v45, s[4:5]
	v_mov_b32_e32 v31, v9
	v_mov_b32_e32 v45, v9
	s_nop 1
	v_permlane32_swap_b32_e32 v31, v45
	v_cndmask_b32_e64 v45, v31, v45, s[4:5]
	v_mov_b32_e32 v31, v5
	v_mov_b32_e32 v47, v5
	s_nop 1
	v_permlane32_swap_b32_e32 v31, v47
	v_cndmask_b32_e64 v47, v31, v47, s[4:5]
	v_lshlrev_b64 v[28:29], 6, v[18:19]
	s_waitcnt lgkmcnt(0)
	v_pk_mul_f32 v[34:35], v[34:35], v[44:45]
	v_pk_mul_f32 v[32:33], v[32:33], v[40:41]
	v_mov_b32_e32 v40, v114
	v_mov_b32_e32 v41, v114
	v_pk_mul_f32 v[32:33], v[114:115], v[32:33]
	v_pk_mul_f32 v[34:35], v[40:41], v[34:35]
	v_pk_fma_f32 v[14:15], v[6:7], v[14:15], v[32:33]
	v_pk_fma_f32 v[16:17], v[8:9], v[16:17], v[34:35]
	v_pk_mul_f32 v[32:33], v[38:39], v[46:47]
	v_pk_mul_f32 v[34:35], v[36:37], v[42:43]
	v_pk_mul_f32 v[32:33], v[40:41], v[32:33]
	v_pk_mul_f32 v[34:35], v[114:115], v[34:35]
	v_pk_fma_f32 v[26:27], v[4:5], v[26:27], v[32:33]
	v_pk_fma_f32 v[24:25], v[2:3], v[24:25], v[34:35]
	v_cvt_pk_bf16_f32 v14, v14, v15
	v_cvt_pk_bf16_f32 v15, v16, v17
	v_cvt_pk_bf16_f32 v16, v24, v25
	v_cvt_pk_bf16_f32 v17, v26, v27
	v_lshl_add_u64 v[24:25], s[42:43], 0, v[28:29]
	v_lshlrev_b32_e32 v26, 1, v149
	v_mov_b32_e32 v27, v1
	v_lshl_add_u64 v[24:25], v[24:25], 0, v[26:27]
	global_store_dwordx4 v[24:25], v[14:17], off

; __device__ __forceinline__ u32x4 pack8(f32x4 a, f32x4 b) { u32x4 w; w.x = pk2(a[0], a[1]); w.y = pk2(a[2], a[3]); w.z = pk2(b[0], b[1]); w.w = pk2(b[2], b[3]); return w; }
; __device__ __forceinline__ float sq8(const f32x4& a, const f32x4& b) { return ((a[0] * a[0] + a[1] * a[1]) + (a[2] * a[2] + a[3] * a[3])) + ((b[0] * b[0] + b[1] * b[1]) + (b[2] * b[2] + b[3] * b[3])); }
;     __device__ __forceinline__ void operator()(const f32x4 (&acc)[2][2][4][2], const Unit& u, int ui, int wr, int wc, int fr, int fq, LAS unsigned char* lds) const {
;     ...
;                     else if (pn == 7) { *(u32x4*)(CQ + (size_t)row * 384 + c) = pack8(v0, v1); sq += sq8(v0, v1); }
;                     else if (bj == 0) { *(u32x4*)(CQ + (size_t)row * 384 + 256 + c) = pack8(v0, v1); sq += sq8(v0, v1); }
.LBB0_582:
	s_andn2_b64 vcc, exec, s[18:19]
	v_mov_b32_e32 v14, v30
	s_cbranch_vccnz .LBB0_584
	v_lshl_add_u64 v[22:23], s[40:41], 0, v[22:23]
	v_cvt_pk_bf16_f32 v14, v6, v7
	v_cvt_pk_bf16_f32 v15, v8, v9
	v_cvt_pk_bf16_f32 v16, v2, v3
	v_cvt_pk_bf16_f32 v17, v4, v5
	v_lshl_add_u64 v[22:23], v[22:23], 0, v[0:1]
	global_store_dwordx4 v[22:23], v[14:17], off offset:256
	v_mov_b32_e32 v22, v9
	v_mov_b32_e32 v23, v5
	v_mov_b32_e32 v16, v7
	v_mov_b32_e32 v17, v3
	v_mov_b32_e32 v14, v6
	v_mov_b32_e32 v15, v2
	v_pk_mul_f32 v[16:17], v[16:17], v[16:17]
	v_pk_mul_f32 v[22:23], v[22:23], v[22:23]
	v_pk_fma_f32 v[14:15], v[14:15], v[14:15], v[16:17]
	v_mov_b32_e32 v16, v8
	v_mov_b32_e32 v17, v4
	v_pk_fma_f32 v[16:17], v[16:17], v[16:17], v[22:23]
	s_nop 0
	v_pk_add_f32 v[14:15], v[14:15], v[16:17]
	s_nop 0
	v_add_f32_e32 v14, v14, v15
	v_add_f32_e32 v14, v14, v30

; __device__ __forceinline__ u32x4 pack8(f32x4 a, f32x4 b) { u32x4 w; w.x = pk2(a[0], a[1]); w.y = pk2(a[2], a[3]); w.z = pk2(b[0], b[1]); w.w = pk2(b[2], b[3]); return w; }
; __device__ __forceinline__ float sq8(const f32x4& a, const f32x4& b) { return ((a[0] * a[0] + a[1] * a[1]) + (a[2] * a[2] + a[3] * a[3])) + ((b[0] * b[0] + b[1] * b[1]) + (b[2] * b[2] + b[3] * b[3])); }
;     __device__ __forceinline__ void operator()(const f32x4 (&acc)[2][2][4][2], const Unit& u, int ui, int wr, int wc, int fr, int fq, LAS unsigned char* lds) const {
;     ...
;                     else if (pn == 6) { *(u32x4*)(CKV + (size_t)row * 256 + c) = pack8(v0, v1); sq += sq8(v0, v1); }
.LBB0_585:
	s_andn2_b64 vcc, exec, s[18:19]
	s_cbranch_vccnz .LBB0_587
	v_lshl_add_u64 v[20:21], s[38:39], 0, v[20:21]
	v_cvt_pk_bf16_f32 v14, v6, v7
	v_cvt_pk_bf16_f32 v15, v8, v9
	v_cvt_pk_bf16_f32 v16, v2, v3
	v_cvt_pk_bf16_f32 v17, v4, v5
	v_lshl_add_u64 v[20:21], v[20:21], 0, v[0:1]
	global_store_dwordx4 v[20:21], v[14:17], off offset:256
	v_mov_b32_e32 v20, v9
	v_mov_b32_e32 v21, v5
	v_mov_b32_e32 v16, v7
	v_mov_b32_e32 v17, v3
	v_mov_b32_e32 v14, v6
	v_mov_b32_e32 v15, v2
	v_pk_mul_f32 v[16:17], v[16:17], v[16:17]
	v_pk_mul_f32 v[20:21], v[20:21], v[20:21]
	v_pk_fma_f32 v[14:15], v[14:15], v[14:15], v[16:17]
	v_mov_b32_e32 v16, v8
	v_mov_b32_e32 v17, v4
	v_pk_fma_f32 v[16:17], v[16:17], v[16:17], v[20:21]
	s_nop 0
	v_pk_add_f32 v[14:15], v[14:15], v[16:17]
	s_nop 0
	v_add_f32_e32 v14, v14, v15
	v_add_f32_e32 v14, v14, v30

; __device__ __forceinline__ u32x4 pack8(f32x4 a, f32x4 b) { u32x4 w; w.x = pk2(a[0], a[1]); w.y = pk2(a[2], a[3]); w.z = pk2(b[0], b[1]); w.w = pk2(b[2], b[3]); return w; }
; __device__ __forceinline__ float fq_sum(float v) { v += xor16(v); v += xor32(v); return v; }
;     __device__ __forceinline__ void operator()(const f32x4 (&acc)[2][2][4][2], const Unit& u, int ui, int wr, int wc, int fr, int fq, LAS unsigned char* lds) const {
;     ...
;                     f32x4 v0 = acc[ai][bj][m][0] * rs, v1 = acc[ai][bj][m][1] * rs;
;                     if (pn < 6) { if (pn < 2) { v0 = v0 * QS_SB; v1 = v1 * QS_SB; } *(u32x4*)(QKV + (size_t)row * 1536 + pn * 256 + c) = pack8(v0, v1); }
;     ...
;                 if (pn >= 6) {
;                     sq = fq_sum(sq);
;                     if (fq == 0) { if (pn == 6) SQK[(size_t)row * 4 + wc] = sq; else SQQ[(size_t)row * 8 + (pn - 7) * 4 + wc] = sq; }
.LBB0_588:
	v_pk_mul_f32 v[14:15], v[8:9], s[96:97] op_sel_hi:[1,0]
	v_pk_mul_f32 v[16:17], v[6:7], s[96:97] op_sel_hi:[1,0]
	v_pk_mul_f32 v[20:21], v[4:5], s[96:97] op_sel_hi:[1,0]
	v_pk_mul_f32 v[22:23], v[2:3], s[96:97] op_sel_hi:[1,0]
	v_cndmask_b32_e64 v5, v5, v21, s[12:13]
	v_cndmask_b32_e64 v20, v4, v20, s[12:13]
	v_cndmask_b32_e64 v4, v3, v23, s[12:13]
	v_cndmask_b32_e64 v21, v2, v22, s[12:13]
	v_cndmask_b32_e64 v3, v9, v15, s[12:13]
	v_cndmask_b32_e64 v8, v8, v14, s[12:13]
	v_cndmask_b32_e64 v2, v7, v17, s[12:13]
	v_cndmask_b32_e64 v6, v6, v16, s[12:13]
	v_cvt_pk_bf16_f32 v2, v6, v2
	v_cvt_pk_bf16_f32 v3, v8, v3
	v_cvt_pk_bf16_f32 v4, v21, v4
	v_cvt_pk_bf16_f32 v5, v20, v5
	v_lshl_add_u64 v[6:7], v[10:11], 0, v[0:1]
	v_mov_b32_e32 v14, v30
	global_store_dwordx4 v[6:7], v[2:5], off offset:256
	s_and_b64 vcc, exec, s[20:21]
	s_cbranch_vccnz .LBB0_592
.LBB0_589:
	v_mov_b32_e32 v0, v14
	v_mov_b32_e32 v2, v14
	v_readlane_b32 s6, v255, 6
	s_nop 0
	v_permlane16_swap_b32_e32 v0, v2
	v_readlane_b32 s7, v255, 7
	s_nop 1
	v_cndmask_b32_e64 v0, v0, v2, s[6:7]
	v_add_f32_e32 v0, v14, v0
	v_mov_b32_e32 v2, v0
	v_mov_b32_e32 v3, v0
	s_nop 1
	v_permlane32_swap_b32_e32 v2, v3
	s_and_saveexec_b64 s[12:13], s[16:17]
	s_cbranch_execz .LBB0_591
	v_lshlrev_b64 v[4:5], 5, v[18:19]
	v_cndmask_b32_e64 v2, v2, v3, s[4:5]
	v_lshl_add_u64 v[4:5], s[48:49], 0, v[4:5]
	v_add_f32_e32 v0, v0, v2
	v_lshl_add_u64 v[2:3], s[50:51], 0, v[12:13]
	v_lshl_add_u64 v[4:5], s[88:89], 2, v[4:5]
	v_cndmask_b32_e64 v3, v5, v3, s[14:15]
	v_cndmask_b32_e64 v2, v4, v2, s[14:15]
	s_lshl_b32 s88, s91, 2
	v_lshl_add_u64 v[2:3], v[2:3], 0, s[88:89]
	global_store_dword v[2:3], v0, off
